# GEMM peel + K-loops without s_setprio, s_nop (M0 write ahead of address add) and redundant lgkmcnt(0)
# speedup vs baseline: 1.0060x; 1.0060x over previous
.LBB0_210:
	s_ashr_i32 s49, s48, 31
	s_lshl_b64 s[4:5], s[48:49], 19
	s_add_u32 s50, s6, s4
	s_addc_u32 s51, s7, s5
	s_and_b64 s[4:5], s[38:39], exec
	s_cselect_b32 s49, s51, s41
	s_cselect_b32 s64, s50, s40
	s_ashr_i32 s45, s44, 31
	s_lshl_b64 s[4:5], s[44:45], 19
	s_add_u32 s52, s8, s4
	s_addc_u32 s53, s9, s5
	s_and_b64 s[4:5], s[38:39], exec
	s_cselect_b32 s45, s53, s43
	s_cselect_b32 s65, s52, s42
	s_add_u32 s70, s64, 0x80
	s_addc_u32 s71, s49, 0
	s_add_u32 s4, s40, 0x40080
	s_addc_u32 s5, s41, 0
	s_add_u32 s78, s42, 0x100
	v_lshl_add_u64 v[144:145], s[4:5], 0, v[140:141]
	v_lshl_add_u64 v[146:147], s[4:5], 0, v[142:143]
	s_addc_u32 s79, s43, 0
	s_mov_b32 s80, -2
	s_mov_b64 s[42:43], 0
	s_waitcnt lgkmcnt(0)
	s_add_u32 s4, s40, s42
	s_addc_u32 s5, s41, s43
	s_add_u32 s81, s4, 0x100
	s_addc_u32 s82, s5, 0
	s_add_u32 s60, s78, s42
	s_addc_u32 s61, s79, s43
	s_add_u32 s4, s4, 0x180
	s_addc_u32 s5, s5, 0
	s_add_i32 s83, 0, 0x10000
	s_add_i32 s84, 0, 0x14000
	v_add_u32_e32 v2, s83, v151
	s_waitcnt vmcnt(0)
	ds_read_b128 v[154:157], v2
	ds_read_b128 v[158:161], v2 offset:1024
	ds_read_b128 v[162:165], v2 offset:2048
	ds_read_b128 v[166:169], v2 offset:3072
	v_add_u32_e32 v2, s84, v151
	ds_read_b128 v[170:173], v2
	ds_read_b128 v[174:177], v2 offset:1024
	ds_read_b128 v[178:181], v2 offset:2048
	ds_read_b128 v[182:185], v2 offset:3072
	s_cmpk_eq_i32 s42, 0x700
	s_cselect_b32 s13, s71, s5
	s_cselect_b32 s12, s70, s4
	s_cselect_b32 s61, s45, s61
	s_cselect_b32 s60, s65, s60
	s_cselect_b32 s5, s49, s82
	s_cselect_b32 s4, s64, s81
	v_lshl_add_u64 v[148:149], v[144:145], 0, s[42:43]
	s_add_i32 m0, s17, 0xc000
	ds_read_b128 v[186:189], v153
	ds_read_b128 v[190:193], v153 offset:1024
	ds_read_b128 v[204:207], v153 offset:2048
	ds_read_b128 v[208:211], v153 offset:3072
	ds_read_b128 v[212:215], v153 offset:4096
	ds_read_b128 v[216:219], v153 offset:5120
	ds_read_b128 v[220:223], v153 offset:6144
	ds_read_b128 v[224:227], v153 offset:7168
	global_load_lds_dwordx4 v[148:149], off
	s_add_i32 m0, s17, 0xe000
	v_lshl_add_u64 v[148:149], v[146:147], 0, s[42:43]
	global_load_lds_dwordx4 v[148:149], off
	s_waitcnt vmcnt(8)
	s_waitcnt lgkmcnt(0)
	s_barrier
	v_mfma_f32_16x16x32_bf16 v[128:131], v[154:157], v[186:189], 0
	v_mfma_f32_16x16x32_bf16 v[124:127], v[162:165], v[186:189], 0
	v_mfma_f32_16x16x32_bf16 v[112:115], v[154:157], v[204:207], 0
	v_mfma_f32_16x16x32_bf16 v[108:111], v[162:165], v[204:207], 0
	v_mfma_f32_16x16x32_bf16 v[96:99], v[154:157], v[212:215], 0
	v_mfma_f32_16x16x32_bf16 v[92:95], v[162:165], v[212:215], 0
	v_mfma_f32_16x16x32_bf16 v[80:83], v[154:157], v[220:223], 0
	v_mfma_f32_16x16x32_bf16 v[76:79], v[162:165], v[220:223], 0
	v_mfma_f32_16x16x32_bf16 v[128:131], v[158:161], v[190:193], v[128:131]
	v_mfma_f32_16x16x32_bf16 v[124:127], v[166:169], v[190:193], v[124:127]
	v_mfma_f32_16x16x32_bf16 v[112:115], v[158:161], v[208:211], v[112:115]
	v_mfma_f32_16x16x32_bf16 v[108:111], v[166:169], v[208:211], v[108:111]
	v_mfma_f32_16x16x32_bf16 v[96:99], v[158:161], v[216:219], v[96:99]
	v_mfma_f32_16x16x32_bf16 v[92:95], v[166:169], v[216:219], v[92:95]
	v_mfma_f32_16x16x32_bf16 v[80:83], v[158:161], v[224:227], v[80:83]
	v_mfma_f32_16x16x32_bf16 v[76:79], v[166:169], v[224:227], v[76:79]
	v_mfma_f32_16x16x32_bf16 v[120:123], v[170:173], v[186:189], 0
	v_mfma_f32_16x16x32_bf16 v[116:119], v[178:181], v[186:189], 0
	v_mfma_f32_16x16x32_bf16 v[104:107], v[170:173], v[204:207], 0
	v_mfma_f32_16x16x32_bf16 v[100:103], v[178:181], v[204:207], 0
	v_mfma_f32_16x16x32_bf16 v[88:91], v[170:173], v[212:215], 0
	v_mfma_f32_16x16x32_bf16 v[84:87], v[178:181], v[212:215], 0
	v_mfma_f32_16x16x32_bf16 v[72:75], v[170:173], v[220:223], 0
	v_mfma_f32_16x16x32_bf16 v[68:71], v[178:181], v[220:223], 0
	v_mfma_f32_16x16x32_bf16 v[120:123], v[174:177], v[190:193], v[120:123]
	v_mfma_f32_16x16x32_bf16 v[116:119], v[182:185], v[190:193], v[116:119]
	v_mfma_f32_16x16x32_bf16 v[104:107], v[174:177], v[208:211], v[104:107]
	v_mfma_f32_16x16x32_bf16 v[100:103], v[182:185], v[208:211], v[100:103]
	v_mfma_f32_16x16x32_bf16 v[88:91], v[174:177], v[216:219], v[88:91]
	v_mfma_f32_16x16x32_bf16 v[84:87], v[182:185], v[216:219], v[84:87]
	v_mfma_f32_16x16x32_bf16 v[72:75], v[174:177], v[224:227], v[72:75]
	v_mfma_f32_16x16x32_bf16 v[68:71], v[182:185], v[224:227], v[68:71]
	s_barrier
	s_add_i32 s81, s83, s16
	v_lshl_add_u64 v[148:149], s[60:61], 0, v[136:137]
	s_mov_b32 m0, s81
	ds_read_b128 v[186:189], v153 offset:16384
	ds_read_b128 v[190:193], v153 offset:17408
	ds_read_b128 v[204:207], v153 offset:18432
	ds_read_b128 v[208:211], v153 offset:19456
	ds_read_b128 v[212:215], v153 offset:20480
	ds_read_b128 v[216:219], v153 offset:21504
	ds_read_b128 v[220:223], v153 offset:22528
	ds_read_b128 v[224:227], v153 offset:23552
	global_load_lds_dwordx4 v[148:149], off
	s_add_i32 m0, s81, 0x2000
	s_add_u32 s82, s60, 0x40000
	v_lshl_add_u64 v[194:195], s[60:61], 0, v[132:133]
	s_addc_u32 s83, s61, 0
	s_add_i32 s81, s84, s16
	global_load_lds_dwordx4 v[194:195], off
	s_mov_b32 m0, s81
	v_lshl_add_u64 v[196:197], s[82:83], 0, v[136:137]
	global_load_lds_dwordx4 v[196:197], off
	s_add_i32 m0, s81, 0x2000
	v_lshl_add_u64 v[196:197], s[82:83], 0, v[132:133]
	global_load_lds_dwordx4 v[196:197], off
	s_mov_b32 m0, s17
	v_lshl_add_u64 v[196:197], s[4:5], 0, v[138:139]
	global_load_lds_dwordx4 v[196:197], off
	s_mov_b32 m0, s46
	v_lshl_add_u64 v[196:197], s[4:5], 0, v[134:135]
	global_load_lds_dwordx4 v[196:197], off
	s_waitcnt vmcnt(8)
	s_waitcnt lgkmcnt(0)
	s_barrier
	v_mfma_f32_16x16x32_bf16 v[64:67], v[154:157], v[186:189], 0
	v_mfma_f32_16x16x32_bf16 v[60:63], v[162:165], v[186:189], 0
	v_mfma_f32_16x16x32_bf16 v[48:51], v[154:157], v[204:207], 0
	v_mfma_f32_16x16x32_bf16 v[44:47], v[162:165], v[204:207], 0
	v_mfma_f32_16x16x32_bf16 v[32:35], v[154:157], v[212:215], 0
	v_mfma_f32_16x16x32_bf16 v[28:31], v[162:165], v[212:215], 0
	v_mfma_f32_16x16x32_bf16 v[16:19], v[154:157], v[220:223], 0
	v_mfma_f32_16x16x32_bf16 v[12:15], v[162:165], v[220:223], 0
	v_mfma_f32_16x16x32_bf16 v[64:67], v[158:161], v[190:193], v[64:67]
	v_mfma_f32_16x16x32_bf16 v[60:63], v[166:169], v[190:193], v[60:63]
	v_mfma_f32_16x16x32_bf16 v[48:51], v[158:161], v[208:211], v[48:51]
	v_mfma_f32_16x16x32_bf16 v[44:47], v[166:169], v[208:211], v[44:47]
	v_mfma_f32_16x16x32_bf16 v[32:35], v[158:161], v[216:219], v[32:35]
	v_mfma_f32_16x16x32_bf16 v[28:31], v[166:169], v[216:219], v[28:31]
	v_mfma_f32_16x16x32_bf16 v[16:19], v[158:161], v[224:227], v[16:19]
	v_mfma_f32_16x16x32_bf16 v[12:15], v[166:169], v[224:227], v[12:15]
	v_mfma_f32_16x16x32_bf16 v[56:59], v[170:173], v[186:189], 0
	v_mfma_f32_16x16x32_bf16 v[52:55], v[178:181], v[186:189], 0
	v_mfma_f32_16x16x32_bf16 v[40:43], v[170:173], v[204:207], 0
	v_mfma_f32_16x16x32_bf16 v[36:39], v[178:181], v[204:207], 0
	v_mfma_f32_16x16x32_bf16 v[24:27], v[170:173], v[212:215], 0
	v_mfma_f32_16x16x32_bf16 v[20:23], v[178:181], v[212:215], 0
	v_mfma_f32_16x16x32_bf16 v[8:11], v[170:173], v[220:223], 0
	v_mfma_f32_16x16x32_bf16 v[4:7], v[178:181], v[220:223], 0
	v_mfma_f32_16x16x32_bf16 v[56:59], v[174:177], v[190:193], v[56:59]
	v_mfma_f32_16x16x32_bf16 v[52:55], v[182:185], v[190:193], v[52:55]
	v_mfma_f32_16x16x32_bf16 v[40:43], v[174:177], v[208:211], v[40:43]
	v_mfma_f32_16x16x32_bf16 v[36:39], v[182:185], v[208:211], v[36:39]
	v_mfma_f32_16x16x32_bf16 v[24:27], v[174:177], v[216:219], v[24:27]
	v_mfma_f32_16x16x32_bf16 v[20:23], v[182:185], v[216:219], v[20:23]
	v_mfma_f32_16x16x32_bf16 v[8:11], v[174:177], v[224:227], v[8:11]
	v_mfma_f32_16x16x32_bf16 v[4:7], v[182:185], v[224:227], v[4:7]
	s_barrier
	s_add_i32 s81, 0, 0x18000
	v_add_u32_e32 v2, s81, v151
	s_add_i32 s82, 0, 0x1c000
	ds_read_b128 v[154:157], v2
	ds_read_b128 v[158:161], v2 offset:1024
	ds_read_b128 v[162:165], v2 offset:2048
	ds_read_b128 v[166:169], v2 offset:3072
	v_add_u32_e32 v2, s82, v151
	ds_read_b128 v[170:173], v2
	ds_read_b128 v[174:177], v2 offset:1024
	ds_read_b128 v[178:181], v2 offset:2048
	ds_read_b128 v[182:185], v2 offset:3072
	s_add_u32 s4, s4, 0x40000
	s_addc_u32 s5, s5, 0
	s_mov_b32 m0, s47
	v_lshl_add_u64 v[196:197], s[4:5], 0, v[138:139]
	ds_read_b128 v[186:189], v153 offset:32768
	ds_read_b128 v[190:193], v153 offset:33792
	ds_read_b128 v[204:207], v153 offset:34816
	ds_read_b128 v[208:211], v153 offset:35840
	ds_read_b128 v[212:215], v153 offset:36864
	ds_read_b128 v[216:219], v153 offset:37888
	ds_read_b128 v[220:223], v153 offset:38912
	ds_read_b128 v[224:227], v153 offset:39936
	global_load_lds_dwordx4 v[196:197], off
	s_mov_b32 m0, s58
	v_lshl_add_u64 v[196:197], s[4:5], 0, v[134:135]
	global_load_lds_dwordx4 v[196:197], off
	s_waitcnt vmcnt(8)
	s_waitcnt lgkmcnt(0)
	s_barrier
	v_mfma_f32_16x16x32_bf16 v[128:131], v[154:157], v[186:189], v[128:131]
	v_mfma_f32_16x16x32_bf16 v[124:127], v[162:165], v[186:189], v[124:127]
	v_mfma_f32_16x16x32_bf16 v[112:115], v[154:157], v[204:207], v[112:115]
	v_mfma_f32_16x16x32_bf16 v[108:111], v[162:165], v[204:207], v[108:111]
	v_mfma_f32_16x16x32_bf16 v[96:99], v[154:157], v[212:215], v[96:99]
	v_mfma_f32_16x16x32_bf16 v[92:95], v[162:165], v[212:215], v[92:95]
	v_mfma_f32_16x16x32_bf16 v[80:83], v[154:157], v[220:223], v[80:83]
	v_mfma_f32_16x16x32_bf16 v[76:79], v[162:165], v[220:223], v[76:79]
	v_mfma_f32_16x16x32_bf16 v[128:131], v[158:161], v[190:193], v[128:131]
	v_mfma_f32_16x16x32_bf16 v[124:127], v[166:169], v[190:193], v[124:127]
	v_mfma_f32_16x16x32_bf16 v[112:115], v[158:161], v[208:211], v[112:115]
	v_mfma_f32_16x16x32_bf16 v[108:111], v[166:169], v[208:211], v[108:111]
	v_mfma_f32_16x16x32_bf16 v[96:99], v[158:161], v[216:219], v[96:99]
	v_mfma_f32_16x16x32_bf16 v[92:95], v[166:169], v[216:219], v[92:95]
	v_mfma_f32_16x16x32_bf16 v[80:83], v[158:161], v[224:227], v[80:83]
	v_mfma_f32_16x16x32_bf16 v[76:79], v[166:169], v[224:227], v[76:79]
	v_mfma_f32_16x16x32_bf16 v[120:123], v[170:173], v[186:189], v[120:123]
	v_mfma_f32_16x16x32_bf16 v[116:119], v[178:181], v[186:189], v[116:119]
	v_mfma_f32_16x16x32_bf16 v[104:107], v[170:173], v[204:207], v[104:107]
	v_mfma_f32_16x16x32_bf16 v[100:103], v[178:181], v[204:207], v[100:103]
	v_mfma_f32_16x16x32_bf16 v[88:91], v[170:173], v[212:215], v[88:91]
	v_mfma_f32_16x16x32_bf16 v[84:87], v[178:181], v[212:215], v[84:87]
	v_mfma_f32_16x16x32_bf16 v[72:75], v[170:173], v[220:223], v[72:75]
	v_mfma_f32_16x16x32_bf16 v[68:71], v[178:181], v[220:223], v[68:71]
	v_mfma_f32_16x16x32_bf16 v[120:123], v[174:177], v[190:193], v[120:123]
	v_mfma_f32_16x16x32_bf16 v[116:119], v[182:185], v[190:193], v[116:119]
	v_mfma_f32_16x16x32_bf16 v[104:107], v[174:177], v[208:211], v[104:107]
	v_mfma_f32_16x16x32_bf16 v[100:103], v[182:185], v[208:211], v[100:103]
	v_mfma_f32_16x16x32_bf16 v[88:91], v[174:177], v[216:219], v[88:91]
	v_mfma_f32_16x16x32_bf16 v[84:87], v[182:185], v[216:219], v[84:87]
	v_mfma_f32_16x16x32_bf16 v[72:75], v[174:177], v[224:227], v[72:75]
	v_mfma_f32_16x16x32_bf16 v[68:71], v[182:185], v[224:227], v[68:71]
	s_barrier
	s_add_i32 s4, s81, s16
	v_lshl_add_u64 v[148:149], v[148:149], 0, s[34:35]
	s_mov_b32 m0, s4
	ds_read_b128 v[186:189], v153 offset:49152
	ds_read_b128 v[190:193], v153 offset:50176
	ds_read_b128 v[204:207], v153 offset:51200
	ds_read_b128 v[208:211], v153 offset:52224
	ds_read_b128 v[212:215], v153 offset:53248
	ds_read_b128 v[216:219], v153 offset:54272
	ds_read_b128 v[220:223], v153 offset:55296
	ds_read_b128 v[224:227], v153 offset:56320
	global_load_lds_dwordx4 v[148:149], off
	s_add_i32 m0, s4, 0x2000
	s_add_u32 s4, s60, 0x40080
	v_lshl_add_u64 v[148:149], v[194:195], 0, s[34:35]
	s_addc_u32 s5, s61, 0
	s_add_i32 s60, s82, s16
	global_load_lds_dwordx4 v[148:149], off
	s_mov_b32 m0, s60
	v_lshl_add_u64 v[148:149], s[4:5], 0, v[136:137]
	global_load_lds_dwordx4 v[148:149], off
	s_add_i32 m0, s60, 0x2000
	v_lshl_add_u64 v[148:149], s[4:5], 0, v[132:133]
	global_load_lds_dwordx4 v[148:149], off
	s_mov_b32 m0, s74
	v_lshl_add_u64 v[148:149], s[12:13], 0, v[138:139]
	global_load_lds_dwordx4 v[148:149], off
	s_mov_b32 m0, s75
	v_lshl_add_u64 v[148:149], s[12:13], 0, v[134:135]
	global_load_lds_dwordx4 v[148:149], off
	s_waitcnt vmcnt(8)
	s_waitcnt lgkmcnt(0)
	s_barrier
	v_mfma_f32_16x16x32_bf16 v[64:67], v[154:157], v[186:189], v[64:67]
	v_mfma_f32_16x16x32_bf16 v[60:63], v[162:165], v[186:189], v[60:63]
	v_mfma_f32_16x16x32_bf16 v[48:51], v[154:157], v[204:207], v[48:51]
	v_mfma_f32_16x16x32_bf16 v[44:47], v[162:165], v[204:207], v[44:47]
	v_mfma_f32_16x16x32_bf16 v[32:35], v[154:157], v[212:215], v[32:35]
	v_mfma_f32_16x16x32_bf16 v[28:31], v[162:165], v[212:215], v[28:31]
	v_mfma_f32_16x16x32_bf16 v[16:19], v[154:157], v[220:223], v[16:19]
	v_mfma_f32_16x16x32_bf16 v[12:15], v[162:165], v[220:223], v[12:15]
	v_mfma_f32_16x16x32_bf16 v[64:67], v[158:161], v[190:193], v[64:67]
	v_mfma_f32_16x16x32_bf16 v[60:63], v[166:169], v[190:193], v[60:63]
	v_mfma_f32_16x16x32_bf16 v[48:51], v[158:161], v[208:211], v[48:51]
	v_mfma_f32_16x16x32_bf16 v[44:47], v[166:169], v[208:211], v[44:47]
	v_mfma_f32_16x16x32_bf16 v[32:35], v[158:161], v[216:219], v[32:35]
	v_mfma_f32_16x16x32_bf16 v[28:31], v[166:169], v[216:219], v[28:31]
	v_mfma_f32_16x16x32_bf16 v[16:19], v[158:161], v[224:227], v[16:19]
	v_mfma_f32_16x16x32_bf16 v[12:15], v[166:169], v[224:227], v[12:15]
	v_mfma_f32_16x16x32_bf16 v[56:59], v[170:173], v[186:189], v[56:59]
	v_mfma_f32_16x16x32_bf16 v[52:55], v[178:181], v[186:189], v[52:55]
	v_mfma_f32_16x16x32_bf16 v[40:43], v[170:173], v[204:207], v[40:43]
	v_mfma_f32_16x16x32_bf16 v[36:39], v[178:181], v[204:207], v[36:39]
	v_mfma_f32_16x16x32_bf16 v[24:27], v[170:173], v[212:215], v[24:27]
	v_mfma_f32_16x16x32_bf16 v[20:23], v[178:181], v[212:215], v[20:23]
	v_mfma_f32_16x16x32_bf16 v[8:11], v[170:173], v[220:223], v[8:11]
	v_mfma_f32_16x16x32_bf16 v[4:7], v[178:181], v[220:223], v[4:7]
	v_mfma_f32_16x16x32_bf16 v[56:59], v[174:177], v[190:193], v[56:59]
	v_mfma_f32_16x16x32_bf16 v[52:55], v[182:185], v[190:193], v[52:55]
	v_mfma_f32_16x16x32_bf16 v[40:43], v[174:177], v[208:211], v[40:43]
	v_mfma_f32_16x16x32_bf16 v[36:39], v[182:185], v[208:211], v[36:39]
	v_mfma_f32_16x16x32_bf16 v[24:27], v[174:177], v[216:219], v[24:27]
	v_mfma_f32_16x16x32_bf16 v[20:23], v[182:185], v[216:219], v[20:23]
	v_mfma_f32_16x16x32_bf16 v[8:11], v[174:177], v[224:227], v[8:11]
	v_mfma_f32_16x16x32_bf16 v[4:7], v[182:185], v[224:227], v[4:7]
	s_barrier
	s_add_i32 s80, s80, 2
	s_add_u32 s42, s42, 0x100
	s_addc_u32 s43, s43, 0
	s_cmp_gt_u32 s80, 13
.LBB0_211:
	s_add_u32 s4, s40, s42
	s_addc_u32 s5, s41, s43
	s_add_u32 s81, s4, 0x100
	s_addc_u32 s82, s5, 0
	s_add_u32 s60, s78, s42
	s_addc_u32 s61, s79, s43
	s_add_u32 s4, s4, 0x180
	s_addc_u32 s5, s5, 0
	s_add_i32 s83, 0, 0x10000
	s_add_i32 s84, 0, 0x14000
	v_add_u32_e32 v2, s83, v151
	s_waitcnt vmcnt(0)
	ds_read_b128 v[154:157], v2
	ds_read_b128 v[158:161], v2 offset:1024
	ds_read_b128 v[162:165], v2 offset:2048
	ds_read_b128 v[166:169], v2 offset:3072
	v_add_u32_e32 v2, s84, v151
	ds_read_b128 v[170:173], v2
	ds_read_b128 v[174:177], v2 offset:1024
	ds_read_b128 v[178:181], v2 offset:2048
	ds_read_b128 v[182:185], v2 offset:3072
	s_cmpk_eq_i32 s42, 0x700
	s_cselect_b32 s13, s71, s5
	s_cselect_b32 s12, s70, s4
	s_cselect_b32 s61, s45, s61
	s_cselect_b32 s60, s65, s60
	s_cselect_b32 s5, s49, s82
	s_cselect_b32 s4, s64, s81
	v_lshl_add_u64 v[148:149], v[144:145], 0, s[42:43]
	s_add_i32 m0, s17, 0xc000
	ds_read_b128 v[186:189], v153
	ds_read_b128 v[190:193], v153 offset:1024
	ds_read_b128 v[204:207], v153 offset:2048
	ds_read_b128 v[208:211], v153 offset:3072
	ds_read_b128 v[212:215], v153 offset:4096
	ds_read_b128 v[216:219], v153 offset:5120
	ds_read_b128 v[220:223], v153 offset:6144
	ds_read_b128 v[224:227], v153 offset:7168
	global_load_lds_dwordx4 v[148:149], off
	s_add_i32 m0, s17, 0xe000
	v_lshl_add_u64 v[148:149], v[146:147], 0, s[42:43]
	global_load_lds_dwordx4 v[148:149], off
	s_waitcnt vmcnt(8)
	s_waitcnt lgkmcnt(0)
	s_barrier
	v_mfma_f32_16x16x32_bf16 v[128:131], v[154:157], v[186:189], v[128:131]
	v_mfma_f32_16x16x32_bf16 v[124:127], v[162:165], v[186:189], v[124:127]
	v_mfma_f32_16x16x32_bf16 v[112:115], v[154:157], v[204:207], v[112:115]
	v_mfma_f32_16x16x32_bf16 v[108:111], v[162:165], v[204:207], v[108:111]
	v_mfma_f32_16x16x32_bf16 v[96:99], v[154:157], v[212:215], v[96:99]
	v_mfma_f32_16x16x32_bf16 v[92:95], v[162:165], v[212:215], v[92:95]
	v_mfma_f32_16x16x32_bf16 v[80:83], v[154:157], v[220:223], v[80:83]
	v_mfma_f32_16x16x32_bf16 v[76:79], v[162:165], v[220:223], v[76:79]
	v_mfma_f32_16x16x32_bf16 v[128:131], v[158:161], v[190:193], v[128:131]
	v_mfma_f32_16x16x32_bf16 v[124:127], v[166:169], v[190:193], v[124:127]
	v_mfma_f32_16x16x32_bf16 v[112:115], v[158:161], v[208:211], v[112:115]
	v_mfma_f32_16x16x32_bf16 v[108:111], v[166:169], v[208:211], v[108:111]
	v_mfma_f32_16x16x32_bf16 v[96:99], v[158:161], v[216:219], v[96:99]
	v_mfma_f32_16x16x32_bf16 v[92:95], v[166:169], v[216:219], v[92:95]
	v_mfma_f32_16x16x32_bf16 v[80:83], v[158:161], v[224:227], v[80:83]
	v_mfma_f32_16x16x32_bf16 v[76:79], v[166:169], v[224:227], v[76:79]
	v_mfma_f32_16x16x32_bf16 v[120:123], v[170:173], v[186:189], v[120:123]
	v_mfma_f32_16x16x32_bf16 v[116:119], v[178:181], v[186:189], v[116:119]
	v_mfma_f32_16x16x32_bf16 v[104:107], v[170:173], v[204:207], v[104:107]
	v_mfma_f32_16x16x32_bf16 v[100:103], v[178:181], v[204:207], v[100:103]
	v_mfma_f32_16x16x32_bf16 v[88:91], v[170:173], v[212:215], v[88:91]
	v_mfma_f32_16x16x32_bf16 v[84:87], v[178:181], v[212:215], v[84:87]
	v_mfma_f32_16x16x32_bf16 v[72:75], v[170:173], v[220:223], v[72:75]
	v_mfma_f32_16x16x32_bf16 v[68:71], v[178:181], v[220:223], v[68:71]
	v_mfma_f32_16x16x32_bf16 v[120:123], v[174:177], v[190:193], v[120:123]
	v_mfma_f32_16x16x32_bf16 v[116:119], v[182:185], v[190:193], v[116:119]
	v_mfma_f32_16x16x32_bf16 v[104:107], v[174:177], v[208:211], v[104:107]
	v_mfma_f32_16x16x32_bf16 v[100:103], v[182:185], v[208:211], v[100:103]
	v_mfma_f32_16x16x32_bf16 v[88:91], v[174:177], v[216:219], v[88:91]
	v_mfma_f32_16x16x32_bf16 v[84:87], v[182:185], v[216:219], v[84:87]
	v_mfma_f32_16x16x32_bf16 v[72:75], v[174:177], v[224:227], v[72:75]
	v_mfma_f32_16x16x32_bf16 v[68:71], v[182:185], v[224:227], v[68:71]
	s_barrier
	s_add_i32 s81, s83, s16
	v_lshl_add_u64 v[148:149], s[60:61], 0, v[136:137]
	s_mov_b32 m0, s81
	ds_read_b128 v[186:189], v153 offset:16384
	ds_read_b128 v[190:193], v153 offset:17408
	ds_read_b128 v[204:207], v153 offset:18432
	ds_read_b128 v[208:211], v153 offset:19456
	ds_read_b128 v[212:215], v153 offset:20480
	ds_read_b128 v[216:219], v153 offset:21504
	ds_read_b128 v[220:223], v153 offset:22528
	ds_read_b128 v[224:227], v153 offset:23552
	global_load_lds_dwordx4 v[148:149], off
	s_add_i32 m0, s81, 0x2000
	s_add_u32 s82, s60, 0x40000
	v_lshl_add_u64 v[194:195], s[60:61], 0, v[132:133]
	s_addc_u32 s83, s61, 0
	s_add_i32 s81, s84, s16
	global_load_lds_dwordx4 v[194:195], off
	s_mov_b32 m0, s81
	v_lshl_add_u64 v[196:197], s[82:83], 0, v[136:137]
	global_load_lds_dwordx4 v[196:197], off
	s_add_i32 m0, s81, 0x2000
	v_lshl_add_u64 v[196:197], s[82:83], 0, v[132:133]
	global_load_lds_dwordx4 v[196:197], off
	s_mov_b32 m0, s17
	v_lshl_add_u64 v[196:197], s[4:5], 0, v[138:139]
	global_load_lds_dwordx4 v[196:197], off
	s_mov_b32 m0, s46
	v_lshl_add_u64 v[196:197], s[4:5], 0, v[134:135]
	global_load_lds_dwordx4 v[196:197], off
	s_waitcnt vmcnt(8)
	s_waitcnt lgkmcnt(0)
	s_barrier
	v_mfma_f32_16x16x32_bf16 v[64:67], v[154:157], v[186:189], v[64:67]
	v_mfma_f32_16x16x32_bf16 v[60:63], v[162:165], v[186:189], v[60:63]
	v_mfma_f32_16x16x32_bf16 v[48:51], v[154:157], v[204:207], v[48:51]
	v_mfma_f32_16x16x32_bf16 v[44:47], v[162:165], v[204:207], v[44:47]
	v_mfma_f32_16x16x32_bf16 v[32:35], v[154:157], v[212:215], v[32:35]
	v_mfma_f32_16x16x32_bf16 v[28:31], v[162:165], v[212:215], v[28:31]
	v_mfma_f32_16x16x32_bf16 v[16:19], v[154:157], v[220:223], v[16:19]
	v_mfma_f32_16x16x32_bf16 v[12:15], v[162:165], v[220:223], v[12:15]
	v_mfma_f32_16x16x32_bf16 v[64:67], v[158:161], v[190:193], v[64:67]
	v_mfma_f32_16x16x32_bf16 v[60:63], v[166:169], v[190:193], v[60:63]
	v_mfma_f32_16x16x32_bf16 v[48:51], v[158:161], v[208:211], v[48:51]
	v_mfma_f32_16x16x32_bf16 v[44:47], v[166:169], v[208:211], v[44:47]
	v_mfma_f32_16x16x32_bf16 v[32:35], v[158:161], v[216:219], v[32:35]
	v_mfma_f32_16x16x32_bf16 v[28:31], v[166:169], v[216:219], v[28:31]
	v_mfma_f32_16x16x32_bf16 v[16:19], v[158:161], v[224:227], v[16:19]
	v_mfma_f32_16x16x32_bf16 v[12:15], v[166:169], v[224:227], v[12:15]
	v_mfma_f32_16x16x32_bf16 v[56:59], v[170:173], v[186:189], v[56:59]
	v_mfma_f32_16x16x32_bf16 v[52:55], v[178:181], v[186:189], v[52:55]
	v_mfma_f32_16x16x32_bf16 v[40:43], v[170:173], v[204:207], v[40:43]
	v_mfma_f32_16x16x32_bf16 v[36:39], v[178:181], v[204:207], v[36:39]
	v_mfma_f32_16x16x32_bf16 v[24:27], v[170:173], v[212:215], v[24:27]
	v_mfma_f32_16x16x32_bf16 v[20:23], v[178:181], v[212:215], v[20:23]
	v_mfma_f32_16x16x32_bf16 v[8:11], v[170:173], v[220:223], v[8:11]
	v_mfma_f32_16x16x32_bf16 v[4:7], v[178:181], v[220:223], v[4:7]
	v_mfma_f32_16x16x32_bf16 v[56:59], v[174:177], v[190:193], v[56:59]
	v_mfma_f32_16x16x32_bf16 v[52:55], v[182:185], v[190:193], v[52:55]
	v_mfma_f32_16x16x32_bf16 v[40:43], v[174:177], v[208:211], v[40:43]
	v_mfma_f32_16x16x32_bf16 v[36:39], v[182:185], v[208:211], v[36:39]
	v_mfma_f32_16x16x32_bf16 v[24:27], v[174:177], v[216:219], v[24:27]
	v_mfma_f32_16x16x32_bf16 v[20:23], v[182:185], v[216:219], v[20:23]
	v_mfma_f32_16x16x32_bf16 v[8:11], v[174:177], v[224:227], v[8:11]
	v_mfma_f32_16x16x32_bf16 v[4:7], v[182:185], v[224:227], v[4:7]
	s_barrier
	s_add_i32 s81, 0, 0x18000
	v_add_u32_e32 v2, s81, v151
	s_add_i32 s82, 0, 0x1c000
	ds_read_b128 v[154:157], v2
	ds_read_b128 v[158:161], v2 offset:1024
	ds_read_b128 v[162:165], v2 offset:2048
	ds_read_b128 v[166:169], v2 offset:3072
	v_add_u32_e32 v2, s82, v151
	ds_read_b128 v[170:173], v2
	ds_read_b128 v[174:177], v2 offset:1024
	ds_read_b128 v[178:181], v2 offset:2048
	ds_read_b128 v[182:185], v2 offset:3072
	s_add_u32 s4, s4, 0x40000
	s_addc_u32 s5, s5, 0
	s_mov_b32 m0, s47
	v_lshl_add_u64 v[196:197], s[4:5], 0, v[138:139]
	ds_read_b128 v[186:189], v153 offset:32768
	ds_read_b128 v[190:193], v153 offset:33792
	ds_read_b128 v[204:207], v153 offset:34816
	ds_read_b128 v[208:211], v153 offset:35840
	ds_read_b128 v[212:215], v153 offset:36864
	ds_read_b128 v[216:219], v153 offset:37888
	ds_read_b128 v[220:223], v153 offset:38912
	ds_read_b128 v[224:227], v153 offset:39936
	global_load_lds_dwordx4 v[196:197], off
	s_mov_b32 m0, s58
	v_lshl_add_u64 v[196:197], s[4:5], 0, v[134:135]
	global_load_lds_dwordx4 v[196:197], off
	s_waitcnt vmcnt(8)
	s_waitcnt lgkmcnt(0)
	s_barrier
	v_mfma_f32_16x16x32_bf16 v[128:131], v[154:157], v[186:189], v[128:131]
	v_mfma_f32_16x16x32_bf16 v[124:127], v[162:165], v[186:189], v[124:127]
	v_mfma_f32_16x16x32_bf16 v[112:115], v[154:157], v[204:207], v[112:115]
	v_mfma_f32_16x16x32_bf16 v[108:111], v[162:165], v[204:207], v[108:111]
	v_mfma_f32_16x16x32_bf16 v[96:99], v[154:157], v[212:215], v[96:99]
	v_mfma_f32_16x16x32_bf16 v[92:95], v[162:165], v[212:215], v[92:95]
	v_mfma_f32_16x16x32_bf16 v[80:83], v[154:157], v[220:223], v[80:83]
	v_mfma_f32_16x16x32_bf16 v[76:79], v[162:165], v[220:223], v[76:79]
	v_mfma_f32_16x16x32_bf16 v[128:131], v[158:161], v[190:193], v[128:131]
	v_mfma_f32_16x16x32_bf16 v[124:127], v[166:169], v[190:193], v[124:127]
	v_mfma_f32_16x16x32_bf16 v[112:115], v[158:161], v[208:211], v[112:115]
	v_mfma_f32_16x16x32_bf16 v[108:111], v[166:169], v[208:211], v[108:111]
	v_mfma_f32_16x16x32_bf16 v[96:99], v[158:161], v[216:219], v[96:99]
	v_mfma_f32_16x16x32_bf16 v[92:95], v[166:169], v[216:219], v[92:95]
	v_mfma_f32_16x16x32_bf16 v[80:83], v[158:161], v[224:227], v[80:83]
	v_mfma_f32_16x16x32_bf16 v[76:79], v[166:169], v[224:227], v[76:79]
	v_mfma_f32_16x16x32_bf16 v[120:123], v[170:173], v[186:189], v[120:123]
	v_mfma_f32_16x16x32_bf16 v[116:119], v[178:181], v[186:189], v[116:119]
	v_mfma_f32_16x16x32_bf16 v[104:107], v[170:173], v[204:207], v[104:107]
	v_mfma_f32_16x16x32_bf16 v[100:103], v[178:181], v[204:207], v[100:103]
	v_mfma_f32_16x16x32_bf16 v[88:91], v[170:173], v[212:215], v[88:91]
	v_mfma_f32_16x16x32_bf16 v[84:87], v[178:181], v[212:215], v[84:87]
	v_mfma_f32_16x16x32_bf16 v[72:75], v[170:173], v[220:223], v[72:75]
	v_mfma_f32_16x16x32_bf16 v[68:71], v[178:181], v[220:223], v[68:71]
	v_mfma_f32_16x16x32_bf16 v[120:123], v[174:177], v[190:193], v[120:123]
	v_mfma_f32_16x16x32_bf16 v[116:119], v[182:185], v[190:193], v[116:119]
	v_mfma_f32_16x16x32_bf16 v[104:107], v[174:177], v[208:211], v[104:107]
	v_mfma_f32_16x16x32_bf16 v[100:103], v[182:185], v[208:211], v[100:103]
	v_mfma_f32_16x16x32_bf16 v[88:91], v[174:177], v[216:219], v[88:91]
	v_mfma_f32_16x16x32_bf16 v[84:87], v[182:185], v[216:219], v[84:87]
	v_mfma_f32_16x16x32_bf16 v[72:75], v[174:177], v[224:227], v[72:75]
	v_mfma_f32_16x16x32_bf16 v[68:71], v[182:185], v[224:227], v[68:71]
	s_barrier
	s_add_i32 s4, s81, s16
	v_lshl_add_u64 v[148:149], v[148:149], 0, s[34:35]
	s_mov_b32 m0, s4
	ds_read_b128 v[186:189], v153 offset:49152
	ds_read_b128 v[190:193], v153 offset:50176
	ds_read_b128 v[204:207], v153 offset:51200
	ds_read_b128 v[208:211], v153 offset:52224
	ds_read_b128 v[212:215], v153 offset:53248
	ds_read_b128 v[216:219], v153 offset:54272
	ds_read_b128 v[220:223], v153 offset:55296
	ds_read_b128 v[224:227], v153 offset:56320
	global_load_lds_dwordx4 v[148:149], off
	s_add_i32 m0, s4, 0x2000
	s_add_u32 s4, s60, 0x40080
	v_lshl_add_u64 v[148:149], v[194:195], 0, s[34:35]
	s_addc_u32 s5, s61, 0
	s_add_i32 s60, s82, s16
	global_load_lds_dwordx4 v[148:149], off
	s_mov_b32 m0, s60
	v_lshl_add_u64 v[148:149], s[4:5], 0, v[136:137]
	global_load_lds_dwordx4 v[148:149], off
	s_add_i32 m0, s60, 0x2000
	v_lshl_add_u64 v[148:149], s[4:5], 0, v[132:133]
	global_load_lds_dwordx4 v[148:149], off
	s_mov_b32 m0, s74
	v_lshl_add_u64 v[148:149], s[12:13], 0, v[138:139]
	global_load_lds_dwordx4 v[148:149], off
	s_mov_b32 m0, s75
	v_lshl_add_u64 v[148:149], s[12:13], 0, v[134:135]
	global_load_lds_dwordx4 v[148:149], off
	s_waitcnt vmcnt(8)
	s_waitcnt lgkmcnt(0)
	s_barrier
	v_mfma_f32_16x16x32_bf16 v[64:67], v[154:157], v[186:189], v[64:67]
	v_mfma_f32_16x16x32_bf16 v[60:63], v[162:165], v[186:189], v[60:63]
	v_mfma_f32_16x16x32_bf16 v[48:51], v[154:157], v[204:207], v[48:51]
	v_mfma_f32_16x16x32_bf16 v[44:47], v[162:165], v[204:207], v[44:47]
	v_mfma_f32_16x16x32_bf16 v[32:35], v[154:157], v[212:215], v[32:35]
	v_mfma_f32_16x16x32_bf16 v[28:31], v[162:165], v[212:215], v[28:31]
	v_mfma_f32_16x16x32_bf16 v[16:19], v[154:157], v[220:223], v[16:19]
	v_mfma_f32_16x16x32_bf16 v[12:15], v[162:165], v[220:223], v[12:15]
	v_mfma_f32_16x16x32_bf16 v[64:67], v[158:161], v[190:193], v[64:67]
	v_mfma_f32_16x16x32_bf16 v[60:63], v[166:169], v[190:193], v[60:63]
	v_mfma_f32_16x16x32_bf16 v[48:51], v[158:161], v[208:211], v[48:51]
	v_mfma_f32_16x16x32_bf16 v[44:47], v[166:169], v[208:211], v[44:47]
	v_mfma_f32_16x16x32_bf16 v[32:35], v[158:161], v[216:219], v[32:35]
	v_mfma_f32_16x16x32_bf16 v[28:31], v[166:169], v[216:219], v[28:31]
	v_mfma_f32_16x16x32_bf16 v[16:19], v[158:161], v[224:227], v[16:19]
	v_mfma_f32_16x16x32_bf16 v[12:15], v[166:169], v[224:227], v[12:15]
	v_mfma_f32_16x16x32_bf16 v[56:59], v[170:173], v[186:189], v[56:59]
	v_mfma_f32_16x16x32_bf16 v[52:55], v[178:181], v[186:189], v[52:55]
	v_mfma_f32_16x16x32_bf16 v[40:43], v[170:173], v[204:207], v[40:43]
	v_mfma_f32_16x16x32_bf16 v[36:39], v[178:181], v[204:207], v[36:39]
	v_mfma_f32_16x16x32_bf16 v[24:27], v[170:173], v[212:215], v[24:27]
	v_mfma_f32_16x16x32_bf16 v[20:23], v[178:181], v[212:215], v[20:23]
	v_mfma_f32_16x16x32_bf16 v[8:11], v[170:173], v[220:223], v[8:11]
	v_mfma_f32_16x16x32_bf16 v[4:7], v[178:181], v[220:223], v[4:7]
	v_mfma_f32_16x16x32_bf16 v[56:59], v[174:177], v[190:193], v[56:59]
	v_mfma_f32_16x16x32_bf16 v[52:55], v[182:185], v[190:193], v[52:55]
	v_mfma_f32_16x16x32_bf16 v[40:43], v[174:177], v[208:211], v[40:43]
	v_mfma_f32_16x16x32_bf16 v[36:39], v[182:185], v[208:211], v[36:39]
	v_mfma_f32_16x16x32_bf16 v[24:27], v[174:177], v[216:219], v[24:27]
	v_mfma_f32_16x16x32_bf16 v[20:23], v[182:185], v[216:219], v[20:23]
	v_mfma_f32_16x16x32_bf16 v[8:11], v[174:177], v[224:227], v[8:11]
	v_mfma_f32_16x16x32_bf16 v[4:7], v[182:185], v[224:227], v[4:7]
	s_barrier
	s_add_i32 s80, s80, 2
	s_add_u32 s42, s42, 0x100
	s_addc_u32 s43, s43, 0
	s_cmp_gt_u32 s80, 13
	s_cbranch_scc0 .LBB0_211
	s_and_b64 vcc, exec, s[22:23]
	s_cbranch_vccz .LBB0_214
	s_barrier

.LBB0_288:
	s_ashr_i32 s41, s40, 31
	s_lshl_b64 s[4:5], s[40:41], 19
	s_add_u32 s42, s6, s4
	s_addc_u32 s43, s7, s5
	s_and_b64 s[4:5], s[22:23], exec
	s_cselect_b32 s41, s43, s37
	s_cselect_b32 s61, s42, s36
	s_ashr_i32 s39, s38, 31
	s_lshl_b64 s[4:5], s[38:39], 19
	s_add_u32 s44, s8, s4
	s_addc_u32 s45, s9, s5
	s_and_b64 s[4:5], s[22:23], exec
	s_cselect_b32 s39, s45, s49
	s_cselect_b32 s62, s44, s48
	s_add_u32 s63, s61, 0x80
	s_addc_u32 s64, s41, 0
	s_add_u32 s4, s36, 0x40080
	s_addc_u32 s5, s37, 0
	s_add_u32 s65, s48, 0x100
	v_lshl_add_u64 v[142:143], s[4:5], 0, v[138:139]
	v_lshl_add_u64 v[144:145], s[4:5], 0, v[140:141]
	s_addc_u32 s68, s49, 0
	s_mov_b32 s69, -2
	s_mov_b64 s[48:49], 0
	s_add_u32 s4, s36, s48
	s_addc_u32 s5, s37, s49
	s_add_u32 s70, s4, 0x100
	s_addc_u32 s71, s5, 0
	s_add_u32 s50, s65, s48
	s_addc_u32 s51, s68, s49
	s_add_u32 s4, s4, 0x180
	s_addc_u32 s5, s5, 0
	s_add_i32 s72, 0, 0x10000
	s_add_i32 s73, 0, 0x14000
	v_add_u32_e32 v160, s72, v146
	s_waitcnt vmcnt(0)
	v_add_u32_e32 v176, s73, v146
	ds_read_b128 v[148:151], v160
	ds_read_b128 v[152:155], v160 offset:1024
	ds_read_b128 v[156:159], v160 offset:2048
	ds_read_b128 v[160:163], v160 offset:3072
	ds_read_b128 v[164:167], v176
	ds_read_b128 v[168:171], v176 offset:1024
	ds_read_b128 v[172:175], v176 offset:2048
	ds_read_b128 v[176:179], v176 offset:3072
	s_cmpk_eq_i32 s48, 0x700
	s_cselect_b32 s13, s64, s5
	s_cselect_b32 s12, s63, s4
	s_cselect_b32 s51, s39, s51
	s_cselect_b32 s50, s62, s50
	s_cselect_b32 s5, s41, s71
	s_cselect_b32 s4, s61, s70
	v_lshl_add_u64 v[196:197], v[142:143], 0, s[48:49]
	s_add_i32 m0, s17, 0xc000
	ds_read_b128 v[180:183], v147
	ds_read_b128 v[184:187], v147 offset:1024
	ds_read_b128 v[188:191], v147 offset:2048
	ds_read_b128 v[192:195], v147 offset:3072
	ds_read_b128 v[204:207], v147 offset:4096
	ds_read_b128 v[208:211], v147 offset:5120
	ds_read_b128 v[212:215], v147 offset:6144
	ds_read_b128 v[216:219], v147 offset:7168
	global_load_lds_dwordx4 v[196:197], off
	s_add_i32 m0, s17, 0xe000
	v_lshl_add_u64 v[196:197], v[144:145], 0, s[48:49]
	global_load_lds_dwordx4 v[196:197], off
	s_waitcnt vmcnt(8)
	s_waitcnt lgkmcnt(0)
	s_barrier
	v_mfma_f32_16x16x32_bf16 v[128:131], v[148:151], v[180:183], 0
	v_mfma_f32_16x16x32_bf16 v[124:127], v[156:159], v[180:183], 0
	v_mfma_f32_16x16x32_bf16 v[120:123], v[148:151], v[188:191], 0
	v_mfma_f32_16x16x32_bf16 v[116:119], v[156:159], v[188:191], 0
	v_mfma_f32_16x16x32_bf16 v[104:107], v[148:151], v[204:207], 0
	v_mfma_f32_16x16x32_bf16 v[100:103], v[156:159], v[204:207], 0
	v_mfma_f32_16x16x32_bf16 v[88:91], v[148:151], v[212:215], 0
	v_mfma_f32_16x16x32_bf16 v[84:87], v[156:159], v[212:215], 0
	v_mfma_f32_16x16x32_bf16 v[128:131], v[152:155], v[184:187], v[128:131]
	v_mfma_f32_16x16x32_bf16 v[124:127], v[160:163], v[184:187], v[124:127]
	v_mfma_f32_16x16x32_bf16 v[120:123], v[152:155], v[192:195], v[120:123]
	v_mfma_f32_16x16x32_bf16 v[116:119], v[160:163], v[192:195], v[116:119]
	v_mfma_f32_16x16x32_bf16 v[104:107], v[152:155], v[208:211], v[104:107]
	v_mfma_f32_16x16x32_bf16 v[100:103], v[160:163], v[208:211], v[100:103]
	v_mfma_f32_16x16x32_bf16 v[88:91], v[152:155], v[216:219], v[88:91]
	v_mfma_f32_16x16x32_bf16 v[84:87], v[160:163], v[216:219], v[84:87]
	v_mfma_f32_16x16x32_bf16 v[112:115], v[164:167], v[180:183], 0
	v_mfma_f32_16x16x32_bf16 v[108:111], v[172:175], v[180:183], 0
	v_mfma_f32_16x16x32_bf16 v[96:99], v[164:167], v[188:191], 0
	v_mfma_f32_16x16x32_bf16 v[92:95], v[172:175], v[188:191], 0
	v_mfma_f32_16x16x32_bf16 v[80:83], v[164:167], v[204:207], 0
	v_mfma_f32_16x16x32_bf16 v[76:79], v[172:175], v[204:207], 0
	v_mfma_f32_16x16x32_bf16 v[72:75], v[164:167], v[212:215], 0
	v_mfma_f32_16x16x32_bf16 v[68:71], v[172:175], v[212:215], 0
	v_mfma_f32_16x16x32_bf16 v[112:115], v[168:171], v[184:187], v[112:115]
	v_mfma_f32_16x16x32_bf16 v[108:111], v[176:179], v[184:187], v[108:111]
	v_mfma_f32_16x16x32_bf16 v[96:99], v[168:171], v[192:195], v[96:99]
	v_mfma_f32_16x16x32_bf16 v[92:95], v[176:179], v[192:195], v[92:95]
	v_mfma_f32_16x16x32_bf16 v[80:83], v[168:171], v[208:211], v[80:83]
	v_mfma_f32_16x16x32_bf16 v[76:79], v[176:179], v[208:211], v[76:79]
	v_mfma_f32_16x16x32_bf16 v[72:75], v[168:171], v[216:219], v[72:75]
	v_mfma_f32_16x16x32_bf16 v[68:71], v[176:179], v[216:219], v[68:71]
	s_barrier
	s_add_i32 s70, s72, s16
	v_lshl_add_u64 v[196:197], s[50:51], 0, v[2:3]
	s_mov_b32 m0, s70
	ds_read_b128 v[180:183], v147 offset:16384
	ds_read_b128 v[184:187], v147 offset:17408
	ds_read_b128 v[188:191], v147 offset:18432
	ds_read_b128 v[192:195], v147 offset:19456
	ds_read_b128 v[204:207], v147 offset:20480
	ds_read_b128 v[208:211], v147 offset:21504
	ds_read_b128 v[212:215], v147 offset:22528
	ds_read_b128 v[216:219], v147 offset:23552
	global_load_lds_dwordx4 v[196:197], off
	s_add_i32 m0, s70, 0x2000
	s_add_u32 s70, s50, 0x40000
	v_lshl_add_u64 v[198:199], s[50:51], 0, v[136:137]
	s_addc_u32 s71, s51, 0
	s_add_i32 s72, s73, s16
	global_load_lds_dwordx4 v[198:199], off
	s_mov_b32 m0, s72
	v_lshl_add_u64 v[220:221], s[70:71], 0, v[2:3]
	global_load_lds_dwordx4 v[220:221], off
	s_add_i32 m0, s72, 0x2000
	v_lshl_add_u64 v[220:221], s[70:71], 0, v[136:137]
	global_load_lds_dwordx4 v[220:221], off
	s_mov_b32 m0, s17
	v_lshl_add_u64 v[220:221], s[4:5], 0, v[132:133]
	global_load_lds_dwordx4 v[220:221], off
	s_mov_b32 m0, s21
	v_lshl_add_u64 v[220:221], s[4:5], 0, v[134:135]
	global_load_lds_dwordx4 v[220:221], off
	s_waitcnt vmcnt(8)
	s_waitcnt lgkmcnt(0)
	s_barrier
	v_mfma_f32_16x16x32_bf16 v[64:67], v[148:151], v[180:183], 0
	v_mfma_f32_16x16x32_bf16 v[60:63], v[156:159], v[180:183], 0
	v_mfma_f32_16x16x32_bf16 v[56:59], v[148:151], v[188:191], 0
	v_mfma_f32_16x16x32_bf16 v[52:55], v[156:159], v[188:191], 0
	v_mfma_f32_16x16x32_bf16 v[40:43], v[148:151], v[204:207], 0
	v_mfma_f32_16x16x32_bf16 v[36:39], v[156:159], v[204:207], 0
	v_mfma_f32_16x16x32_bf16 v[24:27], v[148:151], v[212:215], 0
	v_mfma_f32_16x16x32_bf16 v[20:23], v[156:159], v[212:215], 0
	v_mfma_f32_16x16x32_bf16 v[64:67], v[152:155], v[184:187], v[64:67]
	v_mfma_f32_16x16x32_bf16 v[60:63], v[160:163], v[184:187], v[60:63]
	v_mfma_f32_16x16x32_bf16 v[56:59], v[152:155], v[192:195], v[56:59]
	v_mfma_f32_16x16x32_bf16 v[52:55], v[160:163], v[192:195], v[52:55]
	v_mfma_f32_16x16x32_bf16 v[40:43], v[152:155], v[208:211], v[40:43]
	v_mfma_f32_16x16x32_bf16 v[36:39], v[160:163], v[208:211], v[36:39]
	v_mfma_f32_16x16x32_bf16 v[24:27], v[152:155], v[216:219], v[24:27]
	v_mfma_f32_16x16x32_bf16 v[20:23], v[160:163], v[216:219], v[20:23]
	v_mfma_f32_16x16x32_bf16 v[48:51], v[164:167], v[180:183], 0
	v_mfma_f32_16x16x32_bf16 v[44:47], v[172:175], v[180:183], 0
	v_mfma_f32_16x16x32_bf16 v[32:35], v[164:167], v[188:191], 0
	v_mfma_f32_16x16x32_bf16 v[28:31], v[172:175], v[188:191], 0
	v_mfma_f32_16x16x32_bf16 v[16:19], v[164:167], v[204:207], 0
	v_mfma_f32_16x16x32_bf16 v[12:15], v[172:175], v[204:207], 0
	v_mfma_f32_16x16x32_bf16 v[8:11], v[164:167], v[212:215], 0
	v_mfma_f32_16x16x32_bf16 v[4:7], v[172:175], v[212:215], 0
	v_mfma_f32_16x16x32_bf16 v[48:51], v[168:171], v[184:187], v[48:51]
	v_mfma_f32_16x16x32_bf16 v[44:47], v[176:179], v[184:187], v[44:47]
	v_mfma_f32_16x16x32_bf16 v[32:35], v[168:171], v[192:195], v[32:35]
	v_mfma_f32_16x16x32_bf16 v[28:31], v[176:179], v[192:195], v[28:31]
	v_mfma_f32_16x16x32_bf16 v[16:19], v[168:171], v[208:211], v[16:19]
	v_mfma_f32_16x16x32_bf16 v[12:15], v[176:179], v[208:211], v[12:15]
	v_mfma_f32_16x16x32_bf16 v[8:11], v[168:171], v[216:219], v[8:11]
	v_mfma_f32_16x16x32_bf16 v[4:7], v[176:179], v[216:219], v[4:7]
	s_barrier
	s_add_i32 s70, 0, 0x18000
	s_add_i32 s71, 0, 0x1c000
	v_add_u32_e32 v160, s70, v146
	v_add_u32_e32 v176, s71, v146
	ds_read_b128 v[148:151], v160
	ds_read_b128 v[152:155], v160 offset:1024
	ds_read_b128 v[156:159], v160 offset:2048
	ds_read_b128 v[160:163], v160 offset:3072
	ds_read_b128 v[164:167], v176
	ds_read_b128 v[168:171], v176 offset:1024
	ds_read_b128 v[172:175], v176 offset:2048
	ds_read_b128 v[176:179], v176 offset:3072
	s_add_u32 s4, s4, 0x40000
	s_addc_u32 s5, s5, 0
	s_mov_b32 m0, s46
	v_lshl_add_u64 v[220:221], s[4:5], 0, v[132:133]
	ds_read_b128 v[180:183], v147 offset:32768
	ds_read_b128 v[184:187], v147 offset:33792
	ds_read_b128 v[188:191], v147 offset:34816
	ds_read_b128 v[192:195], v147 offset:35840
	ds_read_b128 v[204:207], v147 offset:36864
	ds_read_b128 v[208:211], v147 offset:37888
	ds_read_b128 v[212:215], v147 offset:38912
	ds_read_b128 v[216:219], v147 offset:39936
	global_load_lds_dwordx4 v[220:221], off
	s_mov_b32 m0, s47
	v_lshl_add_u64 v[220:221], s[4:5], 0, v[134:135]
	global_load_lds_dwordx4 v[220:221], off
	s_waitcnt vmcnt(8)
	s_waitcnt lgkmcnt(0)
	s_barrier
	v_mfma_f32_16x16x32_bf16 v[128:131], v[148:151], v[180:183], v[128:131]
	v_mfma_f32_16x16x32_bf16 v[124:127], v[156:159], v[180:183], v[124:127]
	v_mfma_f32_16x16x32_bf16 v[120:123], v[148:151], v[188:191], v[120:123]
	v_mfma_f32_16x16x32_bf16 v[116:119], v[156:159], v[188:191], v[116:119]
	v_mfma_f32_16x16x32_bf16 v[104:107], v[148:151], v[204:207], v[104:107]
	v_mfma_f32_16x16x32_bf16 v[100:103], v[156:159], v[204:207], v[100:103]
	v_mfma_f32_16x16x32_bf16 v[88:91], v[148:151], v[212:215], v[88:91]
	v_mfma_f32_16x16x32_bf16 v[84:87], v[156:159], v[212:215], v[84:87]
	v_mfma_f32_16x16x32_bf16 v[128:131], v[152:155], v[184:187], v[128:131]
	v_mfma_f32_16x16x32_bf16 v[124:127], v[160:163], v[184:187], v[124:127]
	v_mfma_f32_16x16x32_bf16 v[120:123], v[152:155], v[192:195], v[120:123]
	v_mfma_f32_16x16x32_bf16 v[116:119], v[160:163], v[192:195], v[116:119]
	v_mfma_f32_16x16x32_bf16 v[104:107], v[152:155], v[208:211], v[104:107]
	v_mfma_f32_16x16x32_bf16 v[100:103], v[160:163], v[208:211], v[100:103]
	v_mfma_f32_16x16x32_bf16 v[88:91], v[152:155], v[216:219], v[88:91]
	v_mfma_f32_16x16x32_bf16 v[84:87], v[160:163], v[216:219], v[84:87]
	v_mfma_f32_16x16x32_bf16 v[112:115], v[164:167], v[180:183], v[112:115]
	v_mfma_f32_16x16x32_bf16 v[108:111], v[172:175], v[180:183], v[108:111]
	v_mfma_f32_16x16x32_bf16 v[96:99], v[164:167], v[188:191], v[96:99]
	v_mfma_f32_16x16x32_bf16 v[92:95], v[172:175], v[188:191], v[92:95]
	v_mfma_f32_16x16x32_bf16 v[80:83], v[164:167], v[204:207], v[80:83]
	v_mfma_f32_16x16x32_bf16 v[76:79], v[172:175], v[204:207], v[76:79]
	v_mfma_f32_16x16x32_bf16 v[72:75], v[164:167], v[212:215], v[72:75]
	v_mfma_f32_16x16x32_bf16 v[68:71], v[172:175], v[212:215], v[68:71]
	v_mfma_f32_16x16x32_bf16 v[112:115], v[168:171], v[184:187], v[112:115]
	v_mfma_f32_16x16x32_bf16 v[108:111], v[176:179], v[184:187], v[108:111]
	v_mfma_f32_16x16x32_bf16 v[96:99], v[168:171], v[192:195], v[96:99]
	v_mfma_f32_16x16x32_bf16 v[92:95], v[176:179], v[192:195], v[92:95]
	v_mfma_f32_16x16x32_bf16 v[80:83], v[168:171], v[208:211], v[80:83]
	v_mfma_f32_16x16x32_bf16 v[76:79], v[176:179], v[208:211], v[76:79]
	v_mfma_f32_16x16x32_bf16 v[72:75], v[168:171], v[216:219], v[72:75]
	v_mfma_f32_16x16x32_bf16 v[68:71], v[176:179], v[216:219], v[68:71]
	s_barrier
	s_add_i32 s4, s70, s16
	v_lshl_add_u64 v[196:197], v[196:197], 0, s[34:35]
	s_mov_b32 m0, s4
	ds_read_b128 v[180:183], v147 offset:49152
	ds_read_b128 v[184:187], v147 offset:50176
	ds_read_b128 v[188:191], v147 offset:51200
	ds_read_b128 v[192:195], v147 offset:52224
	ds_read_b128 v[204:207], v147 offset:53248
	ds_read_b128 v[208:211], v147 offset:54272
	ds_read_b128 v[212:215], v147 offset:55296
	ds_read_b128 v[216:219], v147 offset:56320
	global_load_lds_dwordx4 v[196:197], off
	s_add_i32 m0, s4, 0x2000
	s_add_u32 s4, s50, 0x40080
	v_lshl_add_u64 v[196:197], v[198:199], 0, s[34:35]
	s_addc_u32 s5, s51, 0
	s_add_i32 s50, s71, s16
	global_load_lds_dwordx4 v[196:197], off
	s_mov_b32 m0, s50
	v_lshl_add_u64 v[196:197], s[4:5], 0, v[2:3]
	global_load_lds_dwordx4 v[196:197], off
	s_add_i32 m0, s50, 0x2000
	v_lshl_add_u64 v[196:197], s[4:5], 0, v[136:137]
	global_load_lds_dwordx4 v[196:197], off
	s_mov_b32 m0, s56
	v_lshl_add_u64 v[196:197], s[12:13], 0, v[132:133]
	global_load_lds_dwordx4 v[196:197], off
	s_mov_b32 m0, s58
	v_lshl_add_u64 v[196:197], s[12:13], 0, v[134:135]
	global_load_lds_dwordx4 v[196:197], off
	s_waitcnt vmcnt(8)
	s_waitcnt lgkmcnt(0)
	s_barrier
	v_mfma_f32_16x16x32_bf16 v[64:67], v[148:151], v[180:183], v[64:67]
	v_mfma_f32_16x16x32_bf16 v[60:63], v[156:159], v[180:183], v[60:63]
	v_mfma_f32_16x16x32_bf16 v[56:59], v[148:151], v[188:191], v[56:59]
	v_mfma_f32_16x16x32_bf16 v[52:55], v[156:159], v[188:191], v[52:55]
	v_mfma_f32_16x16x32_bf16 v[40:43], v[148:151], v[204:207], v[40:43]
	v_mfma_f32_16x16x32_bf16 v[36:39], v[156:159], v[204:207], v[36:39]
	v_mfma_f32_16x16x32_bf16 v[24:27], v[148:151], v[212:215], v[24:27]
	v_mfma_f32_16x16x32_bf16 v[20:23], v[156:159], v[212:215], v[20:23]
	v_mfma_f32_16x16x32_bf16 v[64:67], v[152:155], v[184:187], v[64:67]
	v_mfma_f32_16x16x32_bf16 v[60:63], v[160:163], v[184:187], v[60:63]
	v_mfma_f32_16x16x32_bf16 v[56:59], v[152:155], v[192:195], v[56:59]
	v_mfma_f32_16x16x32_bf16 v[52:55], v[160:163], v[192:195], v[52:55]
	v_mfma_f32_16x16x32_bf16 v[40:43], v[152:155], v[208:211], v[40:43]
	v_mfma_f32_16x16x32_bf16 v[36:39], v[160:163], v[208:211], v[36:39]
	v_mfma_f32_16x16x32_bf16 v[24:27], v[152:155], v[216:219], v[24:27]
	v_mfma_f32_16x16x32_bf16 v[20:23], v[160:163], v[216:219], v[20:23]
	v_mfma_f32_16x16x32_bf16 v[48:51], v[164:167], v[180:183], v[48:51]
	v_mfma_f32_16x16x32_bf16 v[44:47], v[172:175], v[180:183], v[44:47]
	v_mfma_f32_16x16x32_bf16 v[32:35], v[164:167], v[188:191], v[32:35]
	v_mfma_f32_16x16x32_bf16 v[28:31], v[172:175], v[188:191], v[28:31]
	v_mfma_f32_16x16x32_bf16 v[16:19], v[164:167], v[204:207], v[16:19]
	v_mfma_f32_16x16x32_bf16 v[12:15], v[172:175], v[204:207], v[12:15]
	v_mfma_f32_16x16x32_bf16 v[8:11], v[164:167], v[212:215], v[8:11]
	v_mfma_f32_16x16x32_bf16 v[4:7], v[172:175], v[212:215], v[4:7]
	v_mfma_f32_16x16x32_bf16 v[48:51], v[168:171], v[184:187], v[48:51]
	v_mfma_f32_16x16x32_bf16 v[44:47], v[176:179], v[184:187], v[44:47]
	v_mfma_f32_16x16x32_bf16 v[32:35], v[168:171], v[192:195], v[32:35]
	v_mfma_f32_16x16x32_bf16 v[28:31], v[176:179], v[192:195], v[28:31]
	v_mfma_f32_16x16x32_bf16 v[16:19], v[168:171], v[208:211], v[16:19]
	v_mfma_f32_16x16x32_bf16 v[12:15], v[176:179], v[208:211], v[12:15]
	v_mfma_f32_16x16x32_bf16 v[8:11], v[168:171], v[216:219], v[8:11]
	v_mfma_f32_16x16x32_bf16 v[4:7], v[176:179], v[216:219], v[4:7]
	s_barrier
	s_add_i32 s69, s69, 2
	s_add_u32 s48, s48, 0x100
	s_addc_u32 s49, s49, 0
	s_cmp_gt_u32 s69, 13
.LBB0_289:
	s_add_u32 s4, s36, s48
	s_addc_u32 s5, s37, s49
	s_add_u32 s70, s4, 0x100
	s_addc_u32 s71, s5, 0
	s_add_u32 s50, s65, s48
	s_addc_u32 s51, s68, s49
	s_add_u32 s4, s4, 0x180
	s_addc_u32 s5, s5, 0
	s_add_i32 s72, 0, 0x10000
	s_add_i32 s73, 0, 0x14000
	v_add_u32_e32 v160, s72, v146
	s_waitcnt vmcnt(0)
	v_add_u32_e32 v176, s73, v146
	ds_read_b128 v[148:151], v160
	ds_read_b128 v[152:155], v160 offset:1024
	ds_read_b128 v[156:159], v160 offset:2048
	ds_read_b128 v[160:163], v160 offset:3072
	ds_read_b128 v[164:167], v176
	ds_read_b128 v[168:171], v176 offset:1024
	ds_read_b128 v[172:175], v176 offset:2048
	ds_read_b128 v[176:179], v176 offset:3072
	s_cmpk_eq_i32 s48, 0x700
	s_cselect_b32 s13, s64, s5
	s_cselect_b32 s12, s63, s4
	s_cselect_b32 s51, s39, s51
	s_cselect_b32 s50, s62, s50
	s_cselect_b32 s5, s41, s71
	s_cselect_b32 s4, s61, s70
	v_lshl_add_u64 v[196:197], v[142:143], 0, s[48:49]
	s_add_i32 m0, s17, 0xc000
	ds_read_b128 v[180:183], v147
	ds_read_b128 v[184:187], v147 offset:1024
	ds_read_b128 v[188:191], v147 offset:2048
	ds_read_b128 v[192:195], v147 offset:3072
	ds_read_b128 v[204:207], v147 offset:4096
	ds_read_b128 v[208:211], v147 offset:5120
	ds_read_b128 v[212:215], v147 offset:6144
	ds_read_b128 v[216:219], v147 offset:7168
	global_load_lds_dwordx4 v[196:197], off
	s_add_i32 m0, s17, 0xe000
	v_lshl_add_u64 v[196:197], v[144:145], 0, s[48:49]
	global_load_lds_dwordx4 v[196:197], off
	s_waitcnt vmcnt(8)
	s_waitcnt lgkmcnt(0)
	s_barrier
	v_mfma_f32_16x16x32_bf16 v[128:131], v[148:151], v[180:183], v[128:131]
	v_mfma_f32_16x16x32_bf16 v[124:127], v[156:159], v[180:183], v[124:127]
	v_mfma_f32_16x16x32_bf16 v[120:123], v[148:151], v[188:191], v[120:123]
	v_mfma_f32_16x16x32_bf16 v[116:119], v[156:159], v[188:191], v[116:119]
	v_mfma_f32_16x16x32_bf16 v[104:107], v[148:151], v[204:207], v[104:107]
	v_mfma_f32_16x16x32_bf16 v[100:103], v[156:159], v[204:207], v[100:103]
	v_mfma_f32_16x16x32_bf16 v[88:91], v[148:151], v[212:215], v[88:91]
	v_mfma_f32_16x16x32_bf16 v[84:87], v[156:159], v[212:215], v[84:87]
	v_mfma_f32_16x16x32_bf16 v[128:131], v[152:155], v[184:187], v[128:131]
	v_mfma_f32_16x16x32_bf16 v[124:127], v[160:163], v[184:187], v[124:127]
	v_mfma_f32_16x16x32_bf16 v[120:123], v[152:155], v[192:195], v[120:123]
	v_mfma_f32_16x16x32_bf16 v[116:119], v[160:163], v[192:195], v[116:119]
	v_mfma_f32_16x16x32_bf16 v[104:107], v[152:155], v[208:211], v[104:107]
	v_mfma_f32_16x16x32_bf16 v[100:103], v[160:163], v[208:211], v[100:103]
	v_mfma_f32_16x16x32_bf16 v[88:91], v[152:155], v[216:219], v[88:91]
	v_mfma_f32_16x16x32_bf16 v[84:87], v[160:163], v[216:219], v[84:87]
	v_mfma_f32_16x16x32_bf16 v[112:115], v[164:167], v[180:183], v[112:115]
	v_mfma_f32_16x16x32_bf16 v[108:111], v[172:175], v[180:183], v[108:111]
	v_mfma_f32_16x16x32_bf16 v[96:99], v[164:167], v[188:191], v[96:99]
	v_mfma_f32_16x16x32_bf16 v[92:95], v[172:175], v[188:191], v[92:95]
	v_mfma_f32_16x16x32_bf16 v[80:83], v[164:167], v[204:207], v[80:83]
	v_mfma_f32_16x16x32_bf16 v[76:79], v[172:175], v[204:207], v[76:79]
	v_mfma_f32_16x16x32_bf16 v[72:75], v[164:167], v[212:215], v[72:75]
	v_mfma_f32_16x16x32_bf16 v[68:71], v[172:175], v[212:215], v[68:71]
	v_mfma_f32_16x16x32_bf16 v[112:115], v[168:171], v[184:187], v[112:115]
	v_mfma_f32_16x16x32_bf16 v[108:111], v[176:179], v[184:187], v[108:111]
	v_mfma_f32_16x16x32_bf16 v[96:99], v[168:171], v[192:195], v[96:99]
	v_mfma_f32_16x16x32_bf16 v[92:95], v[176:179], v[192:195], v[92:95]
	v_mfma_f32_16x16x32_bf16 v[80:83], v[168:171], v[208:211], v[80:83]
	v_mfma_f32_16x16x32_bf16 v[76:79], v[176:179], v[208:211], v[76:79]
	v_mfma_f32_16x16x32_bf16 v[72:75], v[168:171], v[216:219], v[72:75]
	v_mfma_f32_16x16x32_bf16 v[68:71], v[176:179], v[216:219], v[68:71]
	s_barrier
	s_add_i32 s70, s72, s16
	v_lshl_add_u64 v[196:197], s[50:51], 0, v[2:3]
	s_mov_b32 m0, s70
	ds_read_b128 v[180:183], v147 offset:16384
	ds_read_b128 v[184:187], v147 offset:17408
	ds_read_b128 v[188:191], v147 offset:18432
	ds_read_b128 v[192:195], v147 offset:19456
	ds_read_b128 v[204:207], v147 offset:20480
	ds_read_b128 v[208:211], v147 offset:21504
	ds_read_b128 v[212:215], v147 offset:22528
	ds_read_b128 v[216:219], v147 offset:23552
	global_load_lds_dwordx4 v[196:197], off
	s_add_i32 m0, s70, 0x2000
	s_add_u32 s70, s50, 0x40000
	v_lshl_add_u64 v[198:199], s[50:51], 0, v[136:137]
	s_addc_u32 s71, s51, 0
	s_add_i32 s72, s73, s16
	global_load_lds_dwordx4 v[198:199], off
	s_mov_b32 m0, s72
	v_lshl_add_u64 v[220:221], s[70:71], 0, v[2:3]
	global_load_lds_dwordx4 v[220:221], off
	s_add_i32 m0, s72, 0x2000
	v_lshl_add_u64 v[220:221], s[70:71], 0, v[136:137]
	global_load_lds_dwordx4 v[220:221], off
	s_mov_b32 m0, s17
	v_lshl_add_u64 v[220:221], s[4:5], 0, v[132:133]
	global_load_lds_dwordx4 v[220:221], off
	s_mov_b32 m0, s21
	v_lshl_add_u64 v[220:221], s[4:5], 0, v[134:135]
	global_load_lds_dwordx4 v[220:221], off
	s_waitcnt vmcnt(8)
	s_waitcnt lgkmcnt(0)
	s_barrier
	v_mfma_f32_16x16x32_bf16 v[64:67], v[148:151], v[180:183], v[64:67]
	v_mfma_f32_16x16x32_bf16 v[60:63], v[156:159], v[180:183], v[60:63]
	v_mfma_f32_16x16x32_bf16 v[56:59], v[148:151], v[188:191], v[56:59]
	v_mfma_f32_16x16x32_bf16 v[52:55], v[156:159], v[188:191], v[52:55]
	v_mfma_f32_16x16x32_bf16 v[40:43], v[148:151], v[204:207], v[40:43]
	v_mfma_f32_16x16x32_bf16 v[36:39], v[156:159], v[204:207], v[36:39]
	v_mfma_f32_16x16x32_bf16 v[24:27], v[148:151], v[212:215], v[24:27]
	v_mfma_f32_16x16x32_bf16 v[20:23], v[156:159], v[212:215], v[20:23]
	v_mfma_f32_16x16x32_bf16 v[64:67], v[152:155], v[184:187], v[64:67]
	v_mfma_f32_16x16x32_bf16 v[60:63], v[160:163], v[184:187], v[60:63]
	v_mfma_f32_16x16x32_bf16 v[56:59], v[152:155], v[192:195], v[56:59]
	v_mfma_f32_16x16x32_bf16 v[52:55], v[160:163], v[192:195], v[52:55]
	v_mfma_f32_16x16x32_bf16 v[40:43], v[152:155], v[208:211], v[40:43]
	v_mfma_f32_16x16x32_bf16 v[36:39], v[160:163], v[208:211], v[36:39]
	v_mfma_f32_16x16x32_bf16 v[24:27], v[152:155], v[216:219], v[24:27]
	v_mfma_f32_16x16x32_bf16 v[20:23], v[160:163], v[216:219], v[20:23]
	v_mfma_f32_16x16x32_bf16 v[48:51], v[164:167], v[180:183], v[48:51]
	v_mfma_f32_16x16x32_bf16 v[44:47], v[172:175], v[180:183], v[44:47]
	v_mfma_f32_16x16x32_bf16 v[32:35], v[164:167], v[188:191], v[32:35]
	v_mfma_f32_16x16x32_bf16 v[28:31], v[172:175], v[188:191], v[28:31]
	v_mfma_f32_16x16x32_bf16 v[16:19], v[164:167], v[204:207], v[16:19]
	v_mfma_f32_16x16x32_bf16 v[12:15], v[172:175], v[204:207], v[12:15]
	v_mfma_f32_16x16x32_bf16 v[8:11], v[164:167], v[212:215], v[8:11]
	v_mfma_f32_16x16x32_bf16 v[4:7], v[172:175], v[212:215], v[4:7]
	v_mfma_f32_16x16x32_bf16 v[48:51], v[168:171], v[184:187], v[48:51]
	v_mfma_f32_16x16x32_bf16 v[44:47], v[176:179], v[184:187], v[44:47]
	v_mfma_f32_16x16x32_bf16 v[32:35], v[168:171], v[192:195], v[32:35]
	v_mfma_f32_16x16x32_bf16 v[28:31], v[176:179], v[192:195], v[28:31]
	v_mfma_f32_16x16x32_bf16 v[16:19], v[168:171], v[208:211], v[16:19]
	v_mfma_f32_16x16x32_bf16 v[12:15], v[176:179], v[208:211], v[12:15]
	v_mfma_f32_16x16x32_bf16 v[8:11], v[168:171], v[216:219], v[8:11]
	v_mfma_f32_16x16x32_bf16 v[4:7], v[176:179], v[216:219], v[4:7]
	s_barrier
	s_add_i32 s70, 0, 0x18000
	s_add_i32 s71, 0, 0x1c000
	v_add_u32_e32 v160, s70, v146
	v_add_u32_e32 v176, s71, v146
	ds_read_b128 v[148:151], v160
	ds_read_b128 v[152:155], v160 offset:1024
	ds_read_b128 v[156:159], v160 offset:2048
	ds_read_b128 v[160:163], v160 offset:3072
	ds_read_b128 v[164:167], v176
	ds_read_b128 v[168:171], v176 offset:1024
	ds_read_b128 v[172:175], v176 offset:2048
	ds_read_b128 v[176:179], v176 offset:3072
	s_add_u32 s4, s4, 0x40000
	s_addc_u32 s5, s5, 0
	s_mov_b32 m0, s46
	v_lshl_add_u64 v[220:221], s[4:5], 0, v[132:133]
	ds_read_b128 v[180:183], v147 offset:32768
	ds_read_b128 v[184:187], v147 offset:33792
	ds_read_b128 v[188:191], v147 offset:34816
	ds_read_b128 v[192:195], v147 offset:35840
	ds_read_b128 v[204:207], v147 offset:36864
	ds_read_b128 v[208:211], v147 offset:37888
	ds_read_b128 v[212:215], v147 offset:38912
	ds_read_b128 v[216:219], v147 offset:39936
	global_load_lds_dwordx4 v[220:221], off
	s_mov_b32 m0, s47
	v_lshl_add_u64 v[220:221], s[4:5], 0, v[134:135]
	global_load_lds_dwordx4 v[220:221], off
	s_waitcnt vmcnt(8)
	s_waitcnt lgkmcnt(0)
	s_barrier
	v_mfma_f32_16x16x32_bf16 v[128:131], v[148:151], v[180:183], v[128:131]
	v_mfma_f32_16x16x32_bf16 v[124:127], v[156:159], v[180:183], v[124:127]
	v_mfma_f32_16x16x32_bf16 v[120:123], v[148:151], v[188:191], v[120:123]
	v_mfma_f32_16x16x32_bf16 v[116:119], v[156:159], v[188:191], v[116:119]
	v_mfma_f32_16x16x32_bf16 v[104:107], v[148:151], v[204:207], v[104:107]
	v_mfma_f32_16x16x32_bf16 v[100:103], v[156:159], v[204:207], v[100:103]
	v_mfma_f32_16x16x32_bf16 v[88:91], v[148:151], v[212:215], v[88:91]
	v_mfma_f32_16x16x32_bf16 v[84:87], v[156:159], v[212:215], v[84:87]
	v_mfma_f32_16x16x32_bf16 v[128:131], v[152:155], v[184:187], v[128:131]
	v_mfma_f32_16x16x32_bf16 v[124:127], v[160:163], v[184:187], v[124:127]
	v_mfma_f32_16x16x32_bf16 v[120:123], v[152:155], v[192:195], v[120:123]
	v_mfma_f32_16x16x32_bf16 v[116:119], v[160:163], v[192:195], v[116:119]
	v_mfma_f32_16x16x32_bf16 v[104:107], v[152:155], v[208:211], v[104:107]
	v_mfma_f32_16x16x32_bf16 v[100:103], v[160:163], v[208:211], v[100:103]
	v_mfma_f32_16x16x32_bf16 v[88:91], v[152:155], v[216:219], v[88:91]
	v_mfma_f32_16x16x32_bf16 v[84:87], v[160:163], v[216:219], v[84:87]
	v_mfma_f32_16x16x32_bf16 v[112:115], v[164:167], v[180:183], v[112:115]
	v_mfma_f32_16x16x32_bf16 v[108:111], v[172:175], v[180:183], v[108:111]
	v_mfma_f32_16x16x32_bf16 v[96:99], v[164:167], v[188:191], v[96:99]
	v_mfma_f32_16x16x32_bf16 v[92:95], v[172:175], v[188:191], v[92:95]
	v_mfma_f32_16x16x32_bf16 v[80:83], v[164:167], v[204:207], v[80:83]
	v_mfma_f32_16x16x32_bf16 v[76:79], v[172:175], v[204:207], v[76:79]
	v_mfma_f32_16x16x32_bf16 v[72:75], v[164:167], v[212:215], v[72:75]
	v_mfma_f32_16x16x32_bf16 v[68:71], v[172:175], v[212:215], v[68:71]
	v_mfma_f32_16x16x32_bf16 v[112:115], v[168:171], v[184:187], v[112:115]
	v_mfma_f32_16x16x32_bf16 v[108:111], v[176:179], v[184:187], v[108:111]
	v_mfma_f32_16x16x32_bf16 v[96:99], v[168:171], v[192:195], v[96:99]
	v_mfma_f32_16x16x32_bf16 v[92:95], v[176:179], v[192:195], v[92:95]
	v_mfma_f32_16x16x32_bf16 v[80:83], v[168:171], v[208:211], v[80:83]
	v_mfma_f32_16x16x32_bf16 v[76:79], v[176:179], v[208:211], v[76:79]
	v_mfma_f32_16x16x32_bf16 v[72:75], v[168:171], v[216:219], v[72:75]
	v_mfma_f32_16x16x32_bf16 v[68:71], v[176:179], v[216:219], v[68:71]
	s_barrier
	s_add_i32 s4, s70, s16
	v_lshl_add_u64 v[196:197], v[196:197], 0, s[34:35]
	s_mov_b32 m0, s4
	ds_read_b128 v[180:183], v147 offset:49152
	ds_read_b128 v[184:187], v147 offset:50176
	ds_read_b128 v[188:191], v147 offset:51200
	ds_read_b128 v[192:195], v147 offset:52224
	ds_read_b128 v[204:207], v147 offset:53248
	ds_read_b128 v[208:211], v147 offset:54272
	ds_read_b128 v[212:215], v147 offset:55296
	ds_read_b128 v[216:219], v147 offset:56320
	global_load_lds_dwordx4 v[196:197], off
	s_add_i32 m0, s4, 0x2000
	s_add_u32 s4, s50, 0x40080
	v_lshl_add_u64 v[196:197], v[198:199], 0, s[34:35]
	s_addc_u32 s5, s51, 0
	s_add_i32 s50, s71, s16
	global_load_lds_dwordx4 v[196:197], off
	s_mov_b32 m0, s50
	v_lshl_add_u64 v[196:197], s[4:5], 0, v[2:3]
	global_load_lds_dwordx4 v[196:197], off
	s_add_i32 m0, s50, 0x2000
	v_lshl_add_u64 v[196:197], s[4:5], 0, v[136:137]
	global_load_lds_dwordx4 v[196:197], off
	s_mov_b32 m0, s56
	v_lshl_add_u64 v[196:197], s[12:13], 0, v[132:133]
	global_load_lds_dwordx4 v[196:197], off
	s_mov_b32 m0, s58
	v_lshl_add_u64 v[196:197], s[12:13], 0, v[134:135]
	global_load_lds_dwordx4 v[196:197], off
	s_waitcnt vmcnt(8)
	s_waitcnt lgkmcnt(0)
	s_barrier
	v_mfma_f32_16x16x32_bf16 v[64:67], v[148:151], v[180:183], v[64:67]
	v_mfma_f32_16x16x32_bf16 v[60:63], v[156:159], v[180:183], v[60:63]
	v_mfma_f32_16x16x32_bf16 v[56:59], v[148:151], v[188:191], v[56:59]
	v_mfma_f32_16x16x32_bf16 v[52:55], v[156:159], v[188:191], v[52:55]
	v_mfma_f32_16x16x32_bf16 v[40:43], v[148:151], v[204:207], v[40:43]
	v_mfma_f32_16x16x32_bf16 v[36:39], v[156:159], v[204:207], v[36:39]
	v_mfma_f32_16x16x32_bf16 v[24:27], v[148:151], v[212:215], v[24:27]
	v_mfma_f32_16x16x32_bf16 v[20:23], v[156:159], v[212:215], v[20:23]
	v_mfma_f32_16x16x32_bf16 v[64:67], v[152:155], v[184:187], v[64:67]
	v_mfma_f32_16x16x32_bf16 v[60:63], v[160:163], v[184:187], v[60:63]
	v_mfma_f32_16x16x32_bf16 v[56:59], v[152:155], v[192:195], v[56:59]
	v_mfma_f32_16x16x32_bf16 v[52:55], v[160:163], v[192:195], v[52:55]
	v_mfma_f32_16x16x32_bf16 v[40:43], v[152:155], v[208:211], v[40:43]
	v_mfma_f32_16x16x32_bf16 v[36:39], v[160:163], v[208:211], v[36:39]
	v_mfma_f32_16x16x32_bf16 v[24:27], v[152:155], v[216:219], v[24:27]
	v_mfma_f32_16x16x32_bf16 v[20:23], v[160:163], v[216:219], v[20:23]
	v_mfma_f32_16x16x32_bf16 v[48:51], v[164:167], v[180:183], v[48:51]
	v_mfma_f32_16x16x32_bf16 v[44:47], v[172:175], v[180:183], v[44:47]
	v_mfma_f32_16x16x32_bf16 v[32:35], v[164:167], v[188:191], v[32:35]
	v_mfma_f32_16x16x32_bf16 v[28:31], v[172:175], v[188:191], v[28:31]
	v_mfma_f32_16x16x32_bf16 v[16:19], v[164:167], v[204:207], v[16:19]
	v_mfma_f32_16x16x32_bf16 v[12:15], v[172:175], v[204:207], v[12:15]
	v_mfma_f32_16x16x32_bf16 v[8:11], v[164:167], v[212:215], v[8:11]
	v_mfma_f32_16x16x32_bf16 v[4:7], v[172:175], v[212:215], v[4:7]
	v_mfma_f32_16x16x32_bf16 v[48:51], v[168:171], v[184:187], v[48:51]
	v_mfma_f32_16x16x32_bf16 v[44:47], v[176:179], v[184:187], v[44:47]
	v_mfma_f32_16x16x32_bf16 v[32:35], v[168:171], v[192:195], v[32:35]
	v_mfma_f32_16x16x32_bf16 v[28:31], v[176:179], v[192:195], v[28:31]
	v_mfma_f32_16x16x32_bf16 v[16:19], v[168:171], v[208:211], v[16:19]
	v_mfma_f32_16x16x32_bf16 v[12:15], v[176:179], v[208:211], v[12:15]
	v_mfma_f32_16x16x32_bf16 v[8:11], v[168:171], v[216:219], v[8:11]
	v_mfma_f32_16x16x32_bf16 v[4:7], v[176:179], v[216:219], v[4:7]
	s_barrier
	s_add_i32 s69, s69, 2
	s_add_u32 s48, s48, 0x100
	s_addc_u32 s49, s49, 0
	s_cmp_gt_u32 s69, 13
	s_cbranch_scc0 .LBB0_289
	s_and_b64 vcc, exec, s[18:19]
	s_mov_b32 s62, 0x18000
	s_mov_b32 s63, 0x1a000
	s_cbranch_vccz .LBB0_292
	s_barrier

.LBB0_310:
	s_ashr_i32 s41, s40, 31
	s_lshl_b64 s[4:5], s[40:41], 19
	s_add_u32 s42, s6, s4
	s_addc_u32 s43, s7, s5
	s_and_b64 s[4:5], s[22:23], exec
	s_cselect_b32 s41, s43, s39
	s_cselect_b32 s60, s42, s38
	s_ashr_i32 s37, s36, 31
	s_lshl_b64 s[4:5], s[36:37], 19
	s_add_u32 s44, s8, s4
	s_addc_u32 s45, s9, s5
	s_and_b64 s[4:5], s[22:23], exec
	s_cselect_b32 s37, s45, s49
	s_cselect_b32 s61, s44, s48
	s_add_u32 s62, s60, 0x80
	s_addc_u32 s63, s41, 0
	s_add_u32 s4, s38, 0x40080
	s_addc_u32 s5, s39, 0
	s_add_u32 s64, s48, 0x100
	v_lshl_add_u64 v[144:145], s[4:5], 0, v[140:141]
	v_lshl_add_u64 v[146:147], s[4:5], 0, v[142:143]
	s_addc_u32 s65, s49, 0
	s_mov_b32 s68, -2
	s_mov_b64 s[48:49], 0
	s_add_u32 s4, s38, s48
	s_addc_u32 s5, s39, s49
	s_add_u32 s69, s4, 0x100
	s_addc_u32 s70, s5, 0
	s_add_u32 s50, s64, s48
	s_addc_u32 s51, s65, s49
	s_add_u32 s4, s4, 0x180
	s_addc_u32 s5, s5, 0
	s_add_i32 s71, 0, 0x10000
	s_add_i32 s72, 0, 0x14000
	v_add_u32_e32 v2, s71, v149
	ds_read_b128 v[152:155], v2
	s_waitcnt vmcnt(0)
	ds_read_b128 v[156:159], v2 offset:1024
	ds_read_b128 v[160:163], v2 offset:2048
	ds_read_b128 v[164:167], v2 offset:3072
	v_add_u32_e32 v2, s72, v149
	ds_read_b128 v[168:171], v2
	ds_read_b128 v[172:175], v2 offset:1024
	ds_read_b128 v[176:179], v2 offset:2048
	ds_read_b128 v[180:183], v2 offset:3072
	s_cmpk_eq_i32 s48, 0x700
	s_cselect_b32 s13, s63, s5
	s_cselect_b32 s12, s62, s4
	s_cselect_b32 s51, s37, s51
	s_cselect_b32 s50, s61, s50
	s_cselect_b32 s5, s41, s70
	s_cselect_b32 s4, s60, s69
	v_lshl_add_u64 v[196:197], v[144:145], 0, s[48:49]
	s_add_i32 m0, s17, 0xc000
	ds_read_b128 v[184:187], v151
	ds_read_b128 v[188:191], v151 offset:1024
	ds_read_b128 v[192:195], v151 offset:2048
	ds_read_b128 v[204:207], v151 offset:3072
	ds_read_b128 v[208:211], v151 offset:4096
	ds_read_b128 v[212:215], v151 offset:5120
	ds_read_b128 v[216:219], v151 offset:6144
	ds_read_b128 v[220:223], v151 offset:7168
	global_load_lds_dwordx4 v[196:197], off
	s_add_i32 m0, s17, 0xe000
	v_lshl_add_u64 v[196:197], v[146:147], 0, s[48:49]
	global_load_lds_dwordx4 v[196:197], off
	s_waitcnt vmcnt(8)
	s_waitcnt lgkmcnt(0)
	s_barrier
	v_mfma_f32_16x16x32_bf16 v[128:131], v[152:155], v[184:187], 0
	v_mfma_f32_16x16x32_bf16 v[124:127], v[160:163], v[184:187], 0
	v_mfma_f32_16x16x32_bf16 v[120:123], v[152:155], v[192:195], 0
	v_mfma_f32_16x16x32_bf16 v[116:119], v[160:163], v[192:195], 0
	v_mfma_f32_16x16x32_bf16 v[104:107], v[152:155], v[208:211], 0
	v_mfma_f32_16x16x32_bf16 v[100:103], v[160:163], v[208:211], 0
	v_mfma_f32_16x16x32_bf16 v[88:91], v[152:155], v[216:219], 0
	v_mfma_f32_16x16x32_bf16 v[84:87], v[160:163], v[216:219], 0
	v_mfma_f32_16x16x32_bf16 v[128:131], v[156:159], v[188:191], v[128:131]
	v_mfma_f32_16x16x32_bf16 v[124:127], v[164:167], v[188:191], v[124:127]
	v_mfma_f32_16x16x32_bf16 v[120:123], v[156:159], v[204:207], v[120:123]
	v_mfma_f32_16x16x32_bf16 v[116:119], v[164:167], v[204:207], v[116:119]
	v_mfma_f32_16x16x32_bf16 v[104:107], v[156:159], v[212:215], v[104:107]
	v_mfma_f32_16x16x32_bf16 v[100:103], v[164:167], v[212:215], v[100:103]
	v_mfma_f32_16x16x32_bf16 v[88:91], v[156:159], v[220:223], v[88:91]
	v_mfma_f32_16x16x32_bf16 v[84:87], v[164:167], v[220:223], v[84:87]
	v_mfma_f32_16x16x32_bf16 v[112:115], v[168:171], v[184:187], 0
	v_mfma_f32_16x16x32_bf16 v[108:111], v[176:179], v[184:187], 0
	v_mfma_f32_16x16x32_bf16 v[96:99], v[168:171], v[192:195], 0
	v_mfma_f32_16x16x32_bf16 v[92:95], v[176:179], v[192:195], 0
	v_mfma_f32_16x16x32_bf16 v[80:83], v[168:171], v[208:211], 0
	v_mfma_f32_16x16x32_bf16 v[76:79], v[176:179], v[208:211], 0
	v_mfma_f32_16x16x32_bf16 v[72:75], v[168:171], v[216:219], 0
	v_mfma_f32_16x16x32_bf16 v[68:71], v[176:179], v[216:219], 0
	v_mfma_f32_16x16x32_bf16 v[112:115], v[172:175], v[188:191], v[112:115]
	v_mfma_f32_16x16x32_bf16 v[108:111], v[180:183], v[188:191], v[108:111]
	v_mfma_f32_16x16x32_bf16 v[96:99], v[172:175], v[204:207], v[96:99]
	v_mfma_f32_16x16x32_bf16 v[92:95], v[180:183], v[204:207], v[92:95]
	v_mfma_f32_16x16x32_bf16 v[80:83], v[172:175], v[212:215], v[80:83]
	v_mfma_f32_16x16x32_bf16 v[76:79], v[180:183], v[212:215], v[76:79]
	v_mfma_f32_16x16x32_bf16 v[72:75], v[172:175], v[220:223], v[72:75]
	v_mfma_f32_16x16x32_bf16 v[68:71], v[180:183], v[220:223], v[68:71]
	s_barrier
	s_add_i32 s69, s71, s16
	v_lshl_add_u64 v[196:197], s[50:51], 0, v[134:135]
	s_mov_b32 m0, s69
	ds_read_b128 v[184:187], v151 offset:16384
	ds_read_b128 v[188:191], v151 offset:17408
	ds_read_b128 v[192:195], v151 offset:18432
	ds_read_b128 v[204:207], v151 offset:19456
	ds_read_b128 v[208:211], v151 offset:20480
	ds_read_b128 v[212:215], v151 offset:21504
	ds_read_b128 v[216:219], v151 offset:22528
	ds_read_b128 v[220:223], v151 offset:23552
	global_load_lds_dwordx4 v[196:197], off
	s_add_i32 m0, s69, 0x2000
	s_add_u32 s70, s50, 0x40000
	v_lshl_add_u64 v[198:199], s[50:51], 0, v[138:139]
	s_addc_u32 s71, s51, 0
	s_add_i32 s69, s72, s16
	global_load_lds_dwordx4 v[198:199], off
	s_mov_b32 m0, s69
	v_lshl_add_u64 v[224:225], s[70:71], 0, v[134:135]
	global_load_lds_dwordx4 v[224:225], off
	s_add_i32 m0, s69, 0x2000
	v_lshl_add_u64 v[224:225], s[70:71], 0, v[138:139]
	global_load_lds_dwordx4 v[224:225], off
	s_mov_b32 m0, s17
	v_lshl_add_u64 v[224:225], s[4:5], 0, v[132:133]
	global_load_lds_dwordx4 v[224:225], off
	s_mov_b32 m0, s21
	v_lshl_add_u64 v[224:225], s[4:5], 0, v[136:137]
	global_load_lds_dwordx4 v[224:225], off
	s_waitcnt vmcnt(8)
	s_waitcnt lgkmcnt(0)
	s_barrier
	v_mfma_f32_16x16x32_bf16 v[64:67], v[152:155], v[184:187], 0
	v_mfma_f32_16x16x32_bf16 v[60:63], v[160:163], v[184:187], 0
	v_mfma_f32_16x16x32_bf16 v[56:59], v[152:155], v[192:195], 0
	v_mfma_f32_16x16x32_bf16 v[52:55], v[160:163], v[192:195], 0
	v_mfma_f32_16x16x32_bf16 v[40:43], v[152:155], v[208:211], 0
	v_mfma_f32_16x16x32_bf16 v[36:39], v[160:163], v[208:211], 0
	v_mfma_f32_16x16x32_bf16 v[24:27], v[152:155], v[216:219], 0
	v_mfma_f32_16x16x32_bf16 v[20:23], v[160:163], v[216:219], 0
	v_mfma_f32_16x16x32_bf16 v[64:67], v[156:159], v[188:191], v[64:67]
	v_mfma_f32_16x16x32_bf16 v[60:63], v[164:167], v[188:191], v[60:63]
	v_mfma_f32_16x16x32_bf16 v[56:59], v[156:159], v[204:207], v[56:59]
	v_mfma_f32_16x16x32_bf16 v[52:55], v[164:167], v[204:207], v[52:55]
	v_mfma_f32_16x16x32_bf16 v[40:43], v[156:159], v[212:215], v[40:43]
	v_mfma_f32_16x16x32_bf16 v[36:39], v[164:167], v[212:215], v[36:39]
	v_mfma_f32_16x16x32_bf16 v[24:27], v[156:159], v[220:223], v[24:27]
	v_mfma_f32_16x16x32_bf16 v[20:23], v[164:167], v[220:223], v[20:23]
	v_mfma_f32_16x16x32_bf16 v[48:51], v[168:171], v[184:187], 0
	v_mfma_f32_16x16x32_bf16 v[44:47], v[176:179], v[184:187], 0
	v_mfma_f32_16x16x32_bf16 v[32:35], v[168:171], v[192:195], 0
	v_mfma_f32_16x16x32_bf16 v[28:31], v[176:179], v[192:195], 0
	v_mfma_f32_16x16x32_bf16 v[16:19], v[168:171], v[208:211], 0
	v_mfma_f32_16x16x32_bf16 v[12:15], v[176:179], v[208:211], 0
	v_mfma_f32_16x16x32_bf16 v[8:11], v[168:171], v[216:219], 0
	v_mfma_f32_16x16x32_bf16 v[4:7], v[176:179], v[216:219], 0
	v_mfma_f32_16x16x32_bf16 v[48:51], v[172:175], v[188:191], v[48:51]
	v_mfma_f32_16x16x32_bf16 v[44:47], v[180:183], v[188:191], v[44:47]
	v_mfma_f32_16x16x32_bf16 v[32:35], v[172:175], v[204:207], v[32:35]
	v_mfma_f32_16x16x32_bf16 v[28:31], v[180:183], v[204:207], v[28:31]
	v_mfma_f32_16x16x32_bf16 v[16:19], v[172:175], v[212:215], v[16:19]
	v_mfma_f32_16x16x32_bf16 v[12:15], v[180:183], v[212:215], v[12:15]
	v_mfma_f32_16x16x32_bf16 v[8:11], v[172:175], v[220:223], v[8:11]
	v_mfma_f32_16x16x32_bf16 v[4:7], v[180:183], v[220:223], v[4:7]
	s_barrier
	s_add_i32 s69, 0, 0x18000
	v_add_u32_e32 v2, s69, v149
	s_add_i32 s70, 0, 0x1c000
	ds_read_b128 v[152:155], v2
	ds_read_b128 v[156:159], v2 offset:1024
	ds_read_b128 v[160:163], v2 offset:2048
	ds_read_b128 v[164:167], v2 offset:3072
	v_add_u32_e32 v2, s70, v149
	ds_read_b128 v[168:171], v2
	ds_read_b128 v[172:175], v2 offset:1024
	ds_read_b128 v[176:179], v2 offset:2048
	ds_read_b128 v[180:183], v2 offset:3072
	s_add_u32 s4, s4, 0x40000
	s_addc_u32 s5, s5, 0
	s_mov_b32 m0, s46
	v_lshl_add_u64 v[224:225], s[4:5], 0, v[132:133]
	ds_read_b128 v[184:187], v151 offset:32768
	ds_read_b128 v[188:191], v151 offset:33792
	ds_read_b128 v[192:195], v151 offset:34816
	ds_read_b128 v[204:207], v151 offset:35840
	ds_read_b128 v[208:211], v151 offset:36864
	ds_read_b128 v[212:215], v151 offset:37888
	ds_read_b128 v[216:219], v151 offset:38912
	ds_read_b128 v[220:223], v151 offset:39936
	global_load_lds_dwordx4 v[224:225], off
	s_mov_b32 m0, s47
	v_lshl_add_u64 v[224:225], s[4:5], 0, v[136:137]
	global_load_lds_dwordx4 v[224:225], off
	s_waitcnt vmcnt(8)
	s_waitcnt lgkmcnt(0)
	s_barrier
	v_mfma_f32_16x16x32_bf16 v[128:131], v[152:155], v[184:187], v[128:131]
	v_mfma_f32_16x16x32_bf16 v[124:127], v[160:163], v[184:187], v[124:127]
	v_mfma_f32_16x16x32_bf16 v[120:123], v[152:155], v[192:195], v[120:123]
	v_mfma_f32_16x16x32_bf16 v[116:119], v[160:163], v[192:195], v[116:119]
	v_mfma_f32_16x16x32_bf16 v[104:107], v[152:155], v[208:211], v[104:107]
	v_mfma_f32_16x16x32_bf16 v[100:103], v[160:163], v[208:211], v[100:103]
	v_mfma_f32_16x16x32_bf16 v[88:91], v[152:155], v[216:219], v[88:91]
	v_mfma_f32_16x16x32_bf16 v[84:87], v[160:163], v[216:219], v[84:87]
	v_mfma_f32_16x16x32_bf16 v[128:131], v[156:159], v[188:191], v[128:131]
	v_mfma_f32_16x16x32_bf16 v[124:127], v[164:167], v[188:191], v[124:127]
	v_mfma_f32_16x16x32_bf16 v[120:123], v[156:159], v[204:207], v[120:123]
	v_mfma_f32_16x16x32_bf16 v[116:119], v[164:167], v[204:207], v[116:119]
	v_mfma_f32_16x16x32_bf16 v[104:107], v[156:159], v[212:215], v[104:107]
	v_mfma_f32_16x16x32_bf16 v[100:103], v[164:167], v[212:215], v[100:103]
	v_mfma_f32_16x16x32_bf16 v[88:91], v[156:159], v[220:223], v[88:91]
	v_mfma_f32_16x16x32_bf16 v[84:87], v[164:167], v[220:223], v[84:87]
	v_mfma_f32_16x16x32_bf16 v[112:115], v[168:171], v[184:187], v[112:115]
	v_mfma_f32_16x16x32_bf16 v[108:111], v[176:179], v[184:187], v[108:111]
	v_mfma_f32_16x16x32_bf16 v[96:99], v[168:171], v[192:195], v[96:99]
	v_mfma_f32_16x16x32_bf16 v[92:95], v[176:179], v[192:195], v[92:95]
	v_mfma_f32_16x16x32_bf16 v[80:83], v[168:171], v[208:211], v[80:83]
	v_mfma_f32_16x16x32_bf16 v[76:79], v[176:179], v[208:211], v[76:79]
	v_mfma_f32_16x16x32_bf16 v[72:75], v[168:171], v[216:219], v[72:75]
	v_mfma_f32_16x16x32_bf16 v[68:71], v[176:179], v[216:219], v[68:71]
	v_mfma_f32_16x16x32_bf16 v[112:115], v[172:175], v[188:191], v[112:115]
	v_mfma_f32_16x16x32_bf16 v[108:111], v[180:183], v[188:191], v[108:111]
	v_mfma_f32_16x16x32_bf16 v[96:99], v[172:175], v[204:207], v[96:99]
	v_mfma_f32_16x16x32_bf16 v[92:95], v[180:183], v[204:207], v[92:95]
	v_mfma_f32_16x16x32_bf16 v[80:83], v[172:175], v[212:215], v[80:83]
	v_mfma_f32_16x16x32_bf16 v[76:79], v[180:183], v[212:215], v[76:79]
	v_mfma_f32_16x16x32_bf16 v[72:75], v[172:175], v[220:223], v[72:75]
	v_mfma_f32_16x16x32_bf16 v[68:71], v[180:183], v[220:223], v[68:71]
	s_barrier
	s_add_i32 s4, s69, s16
	v_lshl_add_u64 v[196:197], v[196:197], 0, s[34:35]
	s_mov_b32 m0, s4
	ds_read_b128 v[184:187], v151 offset:49152
	ds_read_b128 v[188:191], v151 offset:50176
	ds_read_b128 v[192:195], v151 offset:51200
	ds_read_b128 v[204:207], v151 offset:52224
	ds_read_b128 v[208:211], v151 offset:53248
	ds_read_b128 v[212:215], v151 offset:54272
	ds_read_b128 v[216:219], v151 offset:55296
	ds_read_b128 v[220:223], v151 offset:56320
	global_load_lds_dwordx4 v[196:197], off
	s_add_i32 m0, s4, 0x2000
	s_add_u32 s4, s50, 0x40080
	v_lshl_add_u64 v[196:197], v[198:199], 0, s[34:35]
	s_addc_u32 s5, s51, 0
	s_add_i32 s50, s70, s16
	global_load_lds_dwordx4 v[196:197], off
	s_mov_b32 m0, s50
	v_lshl_add_u64 v[196:197], s[4:5], 0, v[134:135]
	global_load_lds_dwordx4 v[196:197], off
	s_add_i32 m0, s50, 0x2000
	v_lshl_add_u64 v[196:197], s[4:5], 0, v[138:139]
	global_load_lds_dwordx4 v[196:197], off
	s_mov_b32 m0, s53
	v_lshl_add_u64 v[196:197], s[12:13], 0, v[132:133]
	global_load_lds_dwordx4 v[196:197], off
	s_mov_b32 m0, s56
	v_lshl_add_u64 v[196:197], s[12:13], 0, v[136:137]
	global_load_lds_dwordx4 v[196:197], off
	s_waitcnt vmcnt(8)
	s_waitcnt lgkmcnt(0)
	s_barrier
	v_mfma_f32_16x16x32_bf16 v[64:67], v[152:155], v[184:187], v[64:67]
	v_mfma_f32_16x16x32_bf16 v[60:63], v[160:163], v[184:187], v[60:63]
	v_mfma_f32_16x16x32_bf16 v[56:59], v[152:155], v[192:195], v[56:59]
	v_mfma_f32_16x16x32_bf16 v[52:55], v[160:163], v[192:195], v[52:55]
	v_mfma_f32_16x16x32_bf16 v[40:43], v[152:155], v[208:211], v[40:43]
	v_mfma_f32_16x16x32_bf16 v[36:39], v[160:163], v[208:211], v[36:39]
	v_mfma_f32_16x16x32_bf16 v[24:27], v[152:155], v[216:219], v[24:27]
	v_mfma_f32_16x16x32_bf16 v[20:23], v[160:163], v[216:219], v[20:23]
	v_mfma_f32_16x16x32_bf16 v[64:67], v[156:159], v[188:191], v[64:67]
	v_mfma_f32_16x16x32_bf16 v[60:63], v[164:167], v[188:191], v[60:63]
	v_mfma_f32_16x16x32_bf16 v[56:59], v[156:159], v[204:207], v[56:59]
	v_mfma_f32_16x16x32_bf16 v[52:55], v[164:167], v[204:207], v[52:55]
	v_mfma_f32_16x16x32_bf16 v[40:43], v[156:159], v[212:215], v[40:43]
	v_mfma_f32_16x16x32_bf16 v[36:39], v[164:167], v[212:215], v[36:39]
	v_mfma_f32_16x16x32_bf16 v[24:27], v[156:159], v[220:223], v[24:27]
	v_mfma_f32_16x16x32_bf16 v[20:23], v[164:167], v[220:223], v[20:23]
	v_mfma_f32_16x16x32_bf16 v[48:51], v[168:171], v[184:187], v[48:51]
	v_mfma_f32_16x16x32_bf16 v[44:47], v[176:179], v[184:187], v[44:47]
	v_mfma_f32_16x16x32_bf16 v[32:35], v[168:171], v[192:195], v[32:35]
	v_mfma_f32_16x16x32_bf16 v[28:31], v[176:179], v[192:195], v[28:31]
	v_mfma_f32_16x16x32_bf16 v[16:19], v[168:171], v[208:211], v[16:19]
	v_mfma_f32_16x16x32_bf16 v[12:15], v[176:179], v[208:211], v[12:15]
	v_mfma_f32_16x16x32_bf16 v[8:11], v[168:171], v[216:219], v[8:11]
	v_mfma_f32_16x16x32_bf16 v[4:7], v[176:179], v[216:219], v[4:7]
	v_mfma_f32_16x16x32_bf16 v[48:51], v[172:175], v[188:191], v[48:51]
	v_mfma_f32_16x16x32_bf16 v[44:47], v[180:183], v[188:191], v[44:47]
	v_mfma_f32_16x16x32_bf16 v[32:35], v[172:175], v[204:207], v[32:35]
	v_mfma_f32_16x16x32_bf16 v[28:31], v[180:183], v[204:207], v[28:31]
	v_mfma_f32_16x16x32_bf16 v[16:19], v[172:175], v[212:215], v[16:19]
	v_mfma_f32_16x16x32_bf16 v[12:15], v[180:183], v[212:215], v[12:15]
	v_mfma_f32_16x16x32_bf16 v[8:11], v[172:175], v[220:223], v[8:11]
	v_mfma_f32_16x16x32_bf16 v[4:7], v[180:183], v[220:223], v[4:7]
	s_barrier
	s_add_i32 s68, s68, 2
	s_add_u32 s48, s48, 0x100
	s_addc_u32 s49, s49, 0
	s_cmp_gt_u32 s68, 13
.LBB0_311:
	s_add_u32 s4, s38, s48
	s_addc_u32 s5, s39, s49
	s_add_u32 s69, s4, 0x100
	s_addc_u32 s70, s5, 0
	s_add_u32 s50, s64, s48
	s_addc_u32 s51, s65, s49
	s_add_u32 s4, s4, 0x180
	s_addc_u32 s5, s5, 0
	s_add_i32 s71, 0, 0x10000
	s_add_i32 s72, 0, 0x14000
	v_add_u32_e32 v2, s71, v149
	ds_read_b128 v[152:155], v2
	s_waitcnt vmcnt(0)
	ds_read_b128 v[156:159], v2 offset:1024
	ds_read_b128 v[160:163], v2 offset:2048
	ds_read_b128 v[164:167], v2 offset:3072
	v_add_u32_e32 v2, s72, v149
	ds_read_b128 v[168:171], v2
	ds_read_b128 v[172:175], v2 offset:1024
	ds_read_b128 v[176:179], v2 offset:2048
	ds_read_b128 v[180:183], v2 offset:3072
	s_cmpk_eq_i32 s48, 0x700
	s_cselect_b32 s13, s63, s5
	s_cselect_b32 s12, s62, s4
	s_cselect_b32 s51, s37, s51
	s_cselect_b32 s50, s61, s50
	s_cselect_b32 s5, s41, s70
	s_cselect_b32 s4, s60, s69
	v_lshl_add_u64 v[196:197], v[144:145], 0, s[48:49]
	s_add_i32 m0, s17, 0xc000
	ds_read_b128 v[184:187], v151
	ds_read_b128 v[188:191], v151 offset:1024
	ds_read_b128 v[192:195], v151 offset:2048
	ds_read_b128 v[204:207], v151 offset:3072
	ds_read_b128 v[208:211], v151 offset:4096
	ds_read_b128 v[212:215], v151 offset:5120
	ds_read_b128 v[216:219], v151 offset:6144
	ds_read_b128 v[220:223], v151 offset:7168
	global_load_lds_dwordx4 v[196:197], off
	s_add_i32 m0, s17, 0xe000
	v_lshl_add_u64 v[196:197], v[146:147], 0, s[48:49]
	global_load_lds_dwordx4 v[196:197], off
	s_waitcnt vmcnt(8)
	s_waitcnt lgkmcnt(0)
	s_barrier
	v_mfma_f32_16x16x32_bf16 v[128:131], v[152:155], v[184:187], v[128:131]
	v_mfma_f32_16x16x32_bf16 v[124:127], v[160:163], v[184:187], v[124:127]
	v_mfma_f32_16x16x32_bf16 v[120:123], v[152:155], v[192:195], v[120:123]
	v_mfma_f32_16x16x32_bf16 v[116:119], v[160:163], v[192:195], v[116:119]
	v_mfma_f32_16x16x32_bf16 v[104:107], v[152:155], v[208:211], v[104:107]
	v_mfma_f32_16x16x32_bf16 v[100:103], v[160:163], v[208:211], v[100:103]
	v_mfma_f32_16x16x32_bf16 v[88:91], v[152:155], v[216:219], v[88:91]
	v_mfma_f32_16x16x32_bf16 v[84:87], v[160:163], v[216:219], v[84:87]
	v_mfma_f32_16x16x32_bf16 v[128:131], v[156:159], v[188:191], v[128:131]
	v_mfma_f32_16x16x32_bf16 v[124:127], v[164:167], v[188:191], v[124:127]
	v_mfma_f32_16x16x32_bf16 v[120:123], v[156:159], v[204:207], v[120:123]
	v_mfma_f32_16x16x32_bf16 v[116:119], v[164:167], v[204:207], v[116:119]
	v_mfma_f32_16x16x32_bf16 v[104:107], v[156:159], v[212:215], v[104:107]
	v_mfma_f32_16x16x32_bf16 v[100:103], v[164:167], v[212:215], v[100:103]
	v_mfma_f32_16x16x32_bf16 v[88:91], v[156:159], v[220:223], v[88:91]
	v_mfma_f32_16x16x32_bf16 v[84:87], v[164:167], v[220:223], v[84:87]
	v_mfma_f32_16x16x32_bf16 v[112:115], v[168:171], v[184:187], v[112:115]
	v_mfma_f32_16x16x32_bf16 v[108:111], v[176:179], v[184:187], v[108:111]
	v_mfma_f32_16x16x32_bf16 v[96:99], v[168:171], v[192:195], v[96:99]
	v_mfma_f32_16x16x32_bf16 v[92:95], v[176:179], v[192:195], v[92:95]
	v_mfma_f32_16x16x32_bf16 v[80:83], v[168:171], v[208:211], v[80:83]
	v_mfma_f32_16x16x32_bf16 v[76:79], v[176:179], v[208:211], v[76:79]
	v_mfma_f32_16x16x32_bf16 v[72:75], v[168:171], v[216:219], v[72:75]
	v_mfma_f32_16x16x32_bf16 v[68:71], v[176:179], v[216:219], v[68:71]
	v_mfma_f32_16x16x32_bf16 v[112:115], v[172:175], v[188:191], v[112:115]
	v_mfma_f32_16x16x32_bf16 v[108:111], v[180:183], v[188:191], v[108:111]
	v_mfma_f32_16x16x32_bf16 v[96:99], v[172:175], v[204:207], v[96:99]
	v_mfma_f32_16x16x32_bf16 v[92:95], v[180:183], v[204:207], v[92:95]
	v_mfma_f32_16x16x32_bf16 v[80:83], v[172:175], v[212:215], v[80:83]
	v_mfma_f32_16x16x32_bf16 v[76:79], v[180:183], v[212:215], v[76:79]
	v_mfma_f32_16x16x32_bf16 v[72:75], v[172:175], v[220:223], v[72:75]
	v_mfma_f32_16x16x32_bf16 v[68:71], v[180:183], v[220:223], v[68:71]
	s_barrier
	s_add_i32 s69, s71, s16
	v_lshl_add_u64 v[196:197], s[50:51], 0, v[134:135]
	s_mov_b32 m0, s69
	ds_read_b128 v[184:187], v151 offset:16384
	ds_read_b128 v[188:191], v151 offset:17408
	ds_read_b128 v[192:195], v151 offset:18432
	ds_read_b128 v[204:207], v151 offset:19456
	ds_read_b128 v[208:211], v151 offset:20480
	ds_read_b128 v[212:215], v151 offset:21504
	ds_read_b128 v[216:219], v151 offset:22528
	ds_read_b128 v[220:223], v151 offset:23552
	global_load_lds_dwordx4 v[196:197], off
	s_add_i32 m0, s69, 0x2000
	s_add_u32 s70, s50, 0x40000
	v_lshl_add_u64 v[198:199], s[50:51], 0, v[138:139]
	s_addc_u32 s71, s51, 0
	s_add_i32 s69, s72, s16
	global_load_lds_dwordx4 v[198:199], off
	s_mov_b32 m0, s69
	v_lshl_add_u64 v[224:225], s[70:71], 0, v[134:135]
	global_load_lds_dwordx4 v[224:225], off
	s_add_i32 m0, s69, 0x2000
	v_lshl_add_u64 v[224:225], s[70:71], 0, v[138:139]
	global_load_lds_dwordx4 v[224:225], off
	s_mov_b32 m0, s17
	v_lshl_add_u64 v[224:225], s[4:5], 0, v[132:133]
	global_load_lds_dwordx4 v[224:225], off
	s_mov_b32 m0, s21
	v_lshl_add_u64 v[224:225], s[4:5], 0, v[136:137]
	global_load_lds_dwordx4 v[224:225], off
	s_waitcnt vmcnt(8)
	s_waitcnt lgkmcnt(0)
	s_barrier
	v_mfma_f32_16x16x32_bf16 v[64:67], v[152:155], v[184:187], v[64:67]
	v_mfma_f32_16x16x32_bf16 v[60:63], v[160:163], v[184:187], v[60:63]
	v_mfma_f32_16x16x32_bf16 v[56:59], v[152:155], v[192:195], v[56:59]
	v_mfma_f32_16x16x32_bf16 v[52:55], v[160:163], v[192:195], v[52:55]
	v_mfma_f32_16x16x32_bf16 v[40:43], v[152:155], v[208:211], v[40:43]
	v_mfma_f32_16x16x32_bf16 v[36:39], v[160:163], v[208:211], v[36:39]
	v_mfma_f32_16x16x32_bf16 v[24:27], v[152:155], v[216:219], v[24:27]
	v_mfma_f32_16x16x32_bf16 v[20:23], v[160:163], v[216:219], v[20:23]
	v_mfma_f32_16x16x32_bf16 v[64:67], v[156:159], v[188:191], v[64:67]
	v_mfma_f32_16x16x32_bf16 v[60:63], v[164:167], v[188:191], v[60:63]
	v_mfma_f32_16x16x32_bf16 v[56:59], v[156:159], v[204:207], v[56:59]
	v_mfma_f32_16x16x32_bf16 v[52:55], v[164:167], v[204:207], v[52:55]
	v_mfma_f32_16x16x32_bf16 v[40:43], v[156:159], v[212:215], v[40:43]
	v_mfma_f32_16x16x32_bf16 v[36:39], v[164:167], v[212:215], v[36:39]
	v_mfma_f32_16x16x32_bf16 v[24:27], v[156:159], v[220:223], v[24:27]
	v_mfma_f32_16x16x32_bf16 v[20:23], v[164:167], v[220:223], v[20:23]
	v_mfma_f32_16x16x32_bf16 v[48:51], v[168:171], v[184:187], v[48:51]
	v_mfma_f32_16x16x32_bf16 v[44:47], v[176:179], v[184:187], v[44:47]
	v_mfma_f32_16x16x32_bf16 v[32:35], v[168:171], v[192:195], v[32:35]
	v_mfma_f32_16x16x32_bf16 v[28:31], v[176:179], v[192:195], v[28:31]
	v_mfma_f32_16x16x32_bf16 v[16:19], v[168:171], v[208:211], v[16:19]
	v_mfma_f32_16x16x32_bf16 v[12:15], v[176:179], v[208:211], v[12:15]
	v_mfma_f32_16x16x32_bf16 v[8:11], v[168:171], v[216:219], v[8:11]
	v_mfma_f32_16x16x32_bf16 v[4:7], v[176:179], v[216:219], v[4:7]
	v_mfma_f32_16x16x32_bf16 v[48:51], v[172:175], v[188:191], v[48:51]
	v_mfma_f32_16x16x32_bf16 v[44:47], v[180:183], v[188:191], v[44:47]
	v_mfma_f32_16x16x32_bf16 v[32:35], v[172:175], v[204:207], v[32:35]
	v_mfma_f32_16x16x32_bf16 v[28:31], v[180:183], v[204:207], v[28:31]
	v_mfma_f32_16x16x32_bf16 v[16:19], v[172:175], v[212:215], v[16:19]
	v_mfma_f32_16x16x32_bf16 v[12:15], v[180:183], v[212:215], v[12:15]
	v_mfma_f32_16x16x32_bf16 v[8:11], v[172:175], v[220:223], v[8:11]
	v_mfma_f32_16x16x32_bf16 v[4:7], v[180:183], v[220:223], v[4:7]
	s_barrier
	s_add_i32 s69, 0, 0x18000
	v_add_u32_e32 v2, s69, v149
	s_add_i32 s70, 0, 0x1c000
	ds_read_b128 v[152:155], v2
	ds_read_b128 v[156:159], v2 offset:1024
	ds_read_b128 v[160:163], v2 offset:2048
	ds_read_b128 v[164:167], v2 offset:3072
	v_add_u32_e32 v2, s70, v149
	ds_read_b128 v[168:171], v2
	ds_read_b128 v[172:175], v2 offset:1024
	ds_read_b128 v[176:179], v2 offset:2048
	ds_read_b128 v[180:183], v2 offset:3072
	s_add_u32 s4, s4, 0x40000
	s_addc_u32 s5, s5, 0
	s_mov_b32 m0, s46
	v_lshl_add_u64 v[224:225], s[4:5], 0, v[132:133]
	ds_read_b128 v[184:187], v151 offset:32768
	ds_read_b128 v[188:191], v151 offset:33792
	ds_read_b128 v[192:195], v151 offset:34816
	ds_read_b128 v[204:207], v151 offset:35840
	ds_read_b128 v[208:211], v151 offset:36864
	ds_read_b128 v[212:215], v151 offset:37888
	ds_read_b128 v[216:219], v151 offset:38912
	ds_read_b128 v[220:223], v151 offset:39936
	global_load_lds_dwordx4 v[224:225], off
	s_mov_b32 m0, s47
	v_lshl_add_u64 v[224:225], s[4:5], 0, v[136:137]
	global_load_lds_dwordx4 v[224:225], off
	s_waitcnt vmcnt(8)
	s_waitcnt lgkmcnt(0)
	s_barrier
	v_mfma_f32_16x16x32_bf16 v[128:131], v[152:155], v[184:187], v[128:131]
	v_mfma_f32_16x16x32_bf16 v[124:127], v[160:163], v[184:187], v[124:127]
	v_mfma_f32_16x16x32_bf16 v[120:123], v[152:155], v[192:195], v[120:123]
	v_mfma_f32_16x16x32_bf16 v[116:119], v[160:163], v[192:195], v[116:119]
	v_mfma_f32_16x16x32_bf16 v[104:107], v[152:155], v[208:211], v[104:107]
	v_mfma_f32_16x16x32_bf16 v[100:103], v[160:163], v[208:211], v[100:103]
	v_mfma_f32_16x16x32_bf16 v[88:91], v[152:155], v[216:219], v[88:91]
	v_mfma_f32_16x16x32_bf16 v[84:87], v[160:163], v[216:219], v[84:87]
	v_mfma_f32_16x16x32_bf16 v[128:131], v[156:159], v[188:191], v[128:131]
	v_mfma_f32_16x16x32_bf16 v[124:127], v[164:167], v[188:191], v[124:127]
	v_mfma_f32_16x16x32_bf16 v[120:123], v[156:159], v[204:207], v[120:123]
	v_mfma_f32_16x16x32_bf16 v[116:119], v[164:167], v[204:207], v[116:119]
	v_mfma_f32_16x16x32_bf16 v[104:107], v[156:159], v[212:215], v[104:107]
	v_mfma_f32_16x16x32_bf16 v[100:103], v[164:167], v[212:215], v[100:103]
	v_mfma_f32_16x16x32_bf16 v[88:91], v[156:159], v[220:223], v[88:91]
	v_mfma_f32_16x16x32_bf16 v[84:87], v[164:167], v[220:223], v[84:87]
	v_mfma_f32_16x16x32_bf16 v[112:115], v[168:171], v[184:187], v[112:115]
	v_mfma_f32_16x16x32_bf16 v[108:111], v[176:179], v[184:187], v[108:111]
	v_mfma_f32_16x16x32_bf16 v[96:99], v[168:171], v[192:195], v[96:99]
	v_mfma_f32_16x16x32_bf16 v[92:95], v[176:179], v[192:195], v[92:95]
	v_mfma_f32_16x16x32_bf16 v[80:83], v[168:171], v[208:211], v[80:83]
	v_mfma_f32_16x16x32_bf16 v[76:79], v[176:179], v[208:211], v[76:79]
	v_mfma_f32_16x16x32_bf16 v[72:75], v[168:171], v[216:219], v[72:75]
	v_mfma_f32_16x16x32_bf16 v[68:71], v[176:179], v[216:219], v[68:71]
	v_mfma_f32_16x16x32_bf16 v[112:115], v[172:175], v[188:191], v[112:115]
	v_mfma_f32_16x16x32_bf16 v[108:111], v[180:183], v[188:191], v[108:111]
	v_mfma_f32_16x16x32_bf16 v[96:99], v[172:175], v[204:207], v[96:99]
	v_mfma_f32_16x16x32_bf16 v[92:95], v[180:183], v[204:207], v[92:95]
	v_mfma_f32_16x16x32_bf16 v[80:83], v[172:175], v[212:215], v[80:83]
	v_mfma_f32_16x16x32_bf16 v[76:79], v[180:183], v[212:215], v[76:79]
	v_mfma_f32_16x16x32_bf16 v[72:75], v[172:175], v[220:223], v[72:75]
	v_mfma_f32_16x16x32_bf16 v[68:71], v[180:183], v[220:223], v[68:71]
	s_barrier
	s_add_i32 s4, s69, s16
	v_lshl_add_u64 v[196:197], v[196:197], 0, s[34:35]
	s_mov_b32 m0, s4
	ds_read_b128 v[184:187], v151 offset:49152
	ds_read_b128 v[188:191], v151 offset:50176
	ds_read_b128 v[192:195], v151 offset:51200
	ds_read_b128 v[204:207], v151 offset:52224
	ds_read_b128 v[208:211], v151 offset:53248
	ds_read_b128 v[212:215], v151 offset:54272
	ds_read_b128 v[216:219], v151 offset:55296
	ds_read_b128 v[220:223], v151 offset:56320
	global_load_lds_dwordx4 v[196:197], off
	s_add_i32 m0, s4, 0x2000
	s_add_u32 s4, s50, 0x40080
	v_lshl_add_u64 v[196:197], v[198:199], 0, s[34:35]
	s_addc_u32 s5, s51, 0
	s_add_i32 s50, s70, s16
	global_load_lds_dwordx4 v[196:197], off
	s_mov_b32 m0, s50
	v_lshl_add_u64 v[196:197], s[4:5], 0, v[134:135]
	global_load_lds_dwordx4 v[196:197], off
	s_add_i32 m0, s50, 0x2000
	v_lshl_add_u64 v[196:197], s[4:5], 0, v[138:139]
	global_load_lds_dwordx4 v[196:197], off
	s_mov_b32 m0, s53
	v_lshl_add_u64 v[196:197], s[12:13], 0, v[132:133]
	global_load_lds_dwordx4 v[196:197], off
	s_mov_b32 m0, s56
	v_lshl_add_u64 v[196:197], s[12:13], 0, v[136:137]
	global_load_lds_dwordx4 v[196:197], off
	s_waitcnt vmcnt(8)
	s_waitcnt lgkmcnt(0)
	s_barrier
	v_mfma_f32_16x16x32_bf16 v[64:67], v[152:155], v[184:187], v[64:67]
	v_mfma_f32_16x16x32_bf16 v[60:63], v[160:163], v[184:187], v[60:63]
	v_mfma_f32_16x16x32_bf16 v[56:59], v[152:155], v[192:195], v[56:59]
	v_mfma_f32_16x16x32_bf16 v[52:55], v[160:163], v[192:195], v[52:55]
	v_mfma_f32_16x16x32_bf16 v[40:43], v[152:155], v[208:211], v[40:43]
	v_mfma_f32_16x16x32_bf16 v[36:39], v[160:163], v[208:211], v[36:39]
	v_mfma_f32_16x16x32_bf16 v[24:27], v[152:155], v[216:219], v[24:27]
	v_mfma_f32_16x16x32_bf16 v[20:23], v[160:163], v[216:219], v[20:23]
	v_mfma_f32_16x16x32_bf16 v[64:67], v[156:159], v[188:191], v[64:67]
	v_mfma_f32_16x16x32_bf16 v[60:63], v[164:167], v[188:191], v[60:63]
	v_mfma_f32_16x16x32_bf16 v[56:59], v[156:159], v[204:207], v[56:59]
	v_mfma_f32_16x16x32_bf16 v[52:55], v[164:167], v[204:207], v[52:55]
	v_mfma_f32_16x16x32_bf16 v[40:43], v[156:159], v[212:215], v[40:43]
	v_mfma_f32_16x16x32_bf16 v[36:39], v[164:167], v[212:215], v[36:39]
	v_mfma_f32_16x16x32_bf16 v[24:27], v[156:159], v[220:223], v[24:27]
	v_mfma_f32_16x16x32_bf16 v[20:23], v[164:167], v[220:223], v[20:23]
	v_mfma_f32_16x16x32_bf16 v[48:51], v[168:171], v[184:187], v[48:51]
	v_mfma_f32_16x16x32_bf16 v[44:47], v[176:179], v[184:187], v[44:47]
	v_mfma_f32_16x16x32_bf16 v[32:35], v[168:171], v[192:195], v[32:35]
	v_mfma_f32_16x16x32_bf16 v[28:31], v[176:179], v[192:195], v[28:31]
	v_mfma_f32_16x16x32_bf16 v[16:19], v[168:171], v[208:211], v[16:19]
	v_mfma_f32_16x16x32_bf16 v[12:15], v[176:179], v[208:211], v[12:15]
	v_mfma_f32_16x16x32_bf16 v[8:11], v[168:171], v[216:219], v[8:11]
	v_mfma_f32_16x16x32_bf16 v[4:7], v[176:179], v[216:219], v[4:7]
	v_mfma_f32_16x16x32_bf16 v[48:51], v[172:175], v[188:191], v[48:51]
	v_mfma_f32_16x16x32_bf16 v[44:47], v[180:183], v[188:191], v[44:47]
	v_mfma_f32_16x16x32_bf16 v[32:35], v[172:175], v[204:207], v[32:35]
	v_mfma_f32_16x16x32_bf16 v[28:31], v[180:183], v[204:207], v[28:31]
	v_mfma_f32_16x16x32_bf16 v[16:19], v[172:175], v[212:215], v[16:19]
	v_mfma_f32_16x16x32_bf16 v[12:15], v[180:183], v[212:215], v[12:15]
	v_mfma_f32_16x16x32_bf16 v[8:11], v[172:175], v[220:223], v[8:11]
	v_mfma_f32_16x16x32_bf16 v[4:7], v[180:183], v[220:223], v[4:7]
	s_barrier
	s_add_i32 s68, s68, 2
	s_add_u32 s48, s48, 0x100
	s_addc_u32 s49, s49, 0
	s_cmp_gt_u32 s68, 13
	s_cbranch_scc0 .LBB0_311
	s_and_b64 vcc, exec, s[18:19]
	s_mov_b32 s62, 0x18000
	s_mov_b32 s63, 0x1a000
	s_cbranch_vccz .LBB0_314
	s_barrier

.LBB0_382:
	s_ashr_i32 s51, s50, 31
	s_lshl_b64 s[4:5], s[50:51], 19
	s_add_u32 s64, s8, s4
	s_addc_u32 s65, s9, s5
	s_and_b64 s[4:5], s[38:39], exec
	s_cselect_b32 s51, s65, s41
	s_cselect_b32 s71, s64, s40
	s_ashr_i32 s11, s10, 31
	s_lshl_b64 s[4:5], s[10:11], 18
	s_add_u32 s36, s16, s4
	s_addc_u32 s37, s17, s5
	s_and_b64 s[4:5], s[38:39], exec
	s_cselect_b32 s11, s37, s43
	s_cselect_b32 s74, s36, s42
	s_add_u32 s75, s71, 0x80
	s_addc_u32 s76, s51, 0
	s_add_u32 s4, s40, 0x40080
	s_addc_u32 s5, s41, 0
	s_add_u32 s77, s42, 0x100
	v_lshl_add_u64 v[100:101], s[4:5], 0, v[176:177]
	v_lshl_add_u64 v[102:103], s[4:5], 0, v[178:179]
	s_addc_u32 s78, s43, 0
	s_mov_b32 s79, -2
	s_mov_b64 s[42:43], 0
	s_add_u32 s4, s40, s42
	s_addc_u32 s5, s41, s43
	s_add_u32 s80, s4, 0x100
	s_addc_u32 s81, s5, 0
	s_add_u32 s48, s77, s42
	s_addc_u32 s49, s78, s43
	s_add_u32 s4, s4, 0x180
	s_addc_u32 s5, s5, 0
	s_add_i32 s82, 0, 0x10000
	s_add_i32 s83, 0, 0x14000
	v_add_u32_e32 v2, s82, v203
	ds_read_b128 v[104:107], v2
	ds_read_b128 v[124:127], v2 offset:1024
	ds_read_b128 v[128:131], v2 offset:2048
	ds_read_b128 v[148:151], v2 offset:3072
	v_add_u32_e32 v2, s83, v203
	ds_read_b128 v[152:155], v2
	ds_read_b128 v[156:159], v2 offset:1024
	ds_read_b128 v[160:163], v2 offset:2048
	ds_read_b128 v[164:167], v2 offset:3072
	s_cmpk_eq_i32 s42, 0x300
	s_cselect_b32 s45, s76, s5
	s_cselect_b32 s44, s75, s4
	s_cselect_b32 s49, s11, s49
	s_cselect_b32 s48, s74, s48
	s_cselect_b32 s5, s51, s81
	s_cselect_b32 s4, s71, s80
	v_lshl_add_u64 v[196:197], v[100:101], 0, s[42:43]
	s_add_i32 m0, s47, 0xc000
	ds_read_b128 v[180:183], v210
	ds_read_b128 v[184:187], v210 offset:1024
	ds_read_b128 v[188:191], v210 offset:2048
	ds_read_b128 v[192:195], v210 offset:3072
	ds_read_b128 v[204:207], v210 offset:4096
	ds_read_b128 v[212:215], v210 offset:5120
	ds_read_b128 v[216:219], v210 offset:6144
	ds_read_b128 v[220:223], v210 offset:7168
	global_load_lds_dwordx4 v[196:197], off
	s_add_i32 m0, s47, 0xe000
	v_lshl_add_u64 v[196:197], v[102:103], 0, s[42:43]
	global_load_lds_dwordx4 v[196:197], off
	s_waitcnt vmcnt(8)
	s_waitcnt lgkmcnt(0)
	s_barrier
	v_mfma_f32_16x16x32_bf16 v[144:147], v[104:107], v[180:183], 0
	v_mfma_f32_16x16x32_bf16 v[140:143], v[128:131], v[180:183], 0
	v_mfma_f32_16x16x32_bf16 v[120:123], v[104:107], v[188:191], 0
	v_mfma_f32_16x16x32_bf16 v[116:119], v[128:131], v[188:191], 0
	v_mfma_f32_16x16x32_bf16 v[96:99], v[104:107], v[204:207], 0
	v_mfma_f32_16x16x32_bf16 v[92:95], v[128:131], v[204:207], 0
	v_mfma_f32_16x16x32_bf16 v[80:83], v[104:107], v[216:219], 0
	v_mfma_f32_16x16x32_bf16 v[76:79], v[128:131], v[216:219], 0
	v_mfma_f32_16x16x32_bf16 v[144:147], v[124:127], v[184:187], v[144:147]
	v_mfma_f32_16x16x32_bf16 v[140:143], v[148:151], v[184:187], v[140:143]
	v_mfma_f32_16x16x32_bf16 v[120:123], v[124:127], v[192:195], v[120:123]
	v_mfma_f32_16x16x32_bf16 v[116:119], v[148:151], v[192:195], v[116:119]
	v_mfma_f32_16x16x32_bf16 v[96:99], v[124:127], v[212:215], v[96:99]
	v_mfma_f32_16x16x32_bf16 v[92:95], v[148:151], v[212:215], v[92:95]
	v_mfma_f32_16x16x32_bf16 v[80:83], v[124:127], v[220:223], v[80:83]
	v_mfma_f32_16x16x32_bf16 v[76:79], v[148:151], v[220:223], v[76:79]
	v_mfma_f32_16x16x32_bf16 v[136:139], v[152:155], v[180:183], 0
	v_mfma_f32_16x16x32_bf16 v[132:135], v[160:163], v[180:183], 0
	v_mfma_f32_16x16x32_bf16 v[112:115], v[152:155], v[188:191], 0
	v_mfma_f32_16x16x32_bf16 v[108:111], v[160:163], v[188:191], 0
	v_mfma_f32_16x16x32_bf16 v[88:91], v[152:155], v[204:207], 0
	v_mfma_f32_16x16x32_bf16 v[84:87], v[160:163], v[204:207], 0
	v_mfma_f32_16x16x32_bf16 v[72:75], v[152:155], v[216:219], 0
	v_mfma_f32_16x16x32_bf16 v[68:71], v[160:163], v[216:219], 0
	v_mfma_f32_16x16x32_bf16 v[136:139], v[156:159], v[184:187], v[136:139]
	v_mfma_f32_16x16x32_bf16 v[132:135], v[164:167], v[184:187], v[132:135]
	v_mfma_f32_16x16x32_bf16 v[112:115], v[156:159], v[192:195], v[112:115]
	v_mfma_f32_16x16x32_bf16 v[108:111], v[164:167], v[192:195], v[108:111]
	v_mfma_f32_16x16x32_bf16 v[88:91], v[156:159], v[212:215], v[88:91]
	v_mfma_f32_16x16x32_bf16 v[84:87], v[164:167], v[212:215], v[84:87]
	v_mfma_f32_16x16x32_bf16 v[72:75], v[156:159], v[220:223], v[72:75]
	v_mfma_f32_16x16x32_bf16 v[68:71], v[164:167], v[220:223], v[68:71]
	s_barrier
	s_add_i32 s80, s82, s46
	v_lshl_add_u64 v[196:197], s[48:49], 0, v[172:173]
	s_mov_b32 m0, s80
	ds_read_b128 v[180:183], v210 offset:16384
	ds_read_b128 v[184:187], v210 offset:17408
	ds_read_b128 v[188:191], v210 offset:18432
	ds_read_b128 v[192:195], v210 offset:19456
	ds_read_b128 v[204:207], v210 offset:20480
	ds_read_b128 v[212:215], v210 offset:21504
	ds_read_b128 v[216:219], v210 offset:22528
	ds_read_b128 v[220:223], v210 offset:23552
	global_load_lds_dwordx4 v[196:197], off
	s_add_i32 m0, s80, 0x2000
	s_add_u32 s80, s48, 0x20000
	v_lshl_add_u64 v[198:199], s[48:49], 0, v[168:169]
	s_addc_u32 s81, s49, 0
	s_add_i32 s82, s83, s46
	global_load_lds_dwordx4 v[198:199], off
	s_mov_b32 m0, s82
	v_lshl_add_u64 v[208:209], s[80:81], 0, v[172:173]
	global_load_lds_dwordx4 v[208:209], off
	s_add_i32 m0, s82, 0x2000
	v_lshl_add_u64 v[208:209], s[80:81], 0, v[168:169]
	global_load_lds_dwordx4 v[208:209], off
	s_mov_b32 m0, s47
	v_lshl_add_u64 v[208:209], s[4:5], 0, v[174:175]
	global_load_lds_dwordx4 v[208:209], off
	s_mov_b32 m0, s56
	v_lshl_add_u64 v[208:209], s[4:5], 0, v[170:171]
	global_load_lds_dwordx4 v[208:209], off
	s_waitcnt vmcnt(8)
	s_waitcnt lgkmcnt(0)
	s_barrier
	v_mfma_f32_16x16x32_bf16 v[64:67], v[104:107], v[180:183], 0
	v_mfma_f32_16x16x32_bf16 v[60:63], v[128:131], v[180:183], 0
	v_mfma_f32_16x16x32_bf16 v[48:51], v[104:107], v[188:191], 0
	v_mfma_f32_16x16x32_bf16 v[44:47], v[128:131], v[188:191], 0
	v_mfma_f32_16x16x32_bf16 v[32:35], v[104:107], v[204:207], 0
	v_mfma_f32_16x16x32_bf16 v[28:31], v[128:131], v[204:207], 0
	v_mfma_f32_16x16x32_bf16 v[16:19], v[104:107], v[216:219], 0
	v_mfma_f32_16x16x32_bf16 v[12:15], v[128:131], v[216:219], 0
	v_mfma_f32_16x16x32_bf16 v[64:67], v[124:127], v[184:187], v[64:67]
	v_mfma_f32_16x16x32_bf16 v[60:63], v[148:151], v[184:187], v[60:63]
	v_mfma_f32_16x16x32_bf16 v[48:51], v[124:127], v[192:195], v[48:51]
	v_mfma_f32_16x16x32_bf16 v[44:47], v[148:151], v[192:195], v[44:47]
	v_mfma_f32_16x16x32_bf16 v[32:35], v[124:127], v[212:215], v[32:35]
	v_mfma_f32_16x16x32_bf16 v[28:31], v[148:151], v[212:215], v[28:31]
	v_mfma_f32_16x16x32_bf16 v[16:19], v[124:127], v[220:223], v[16:19]
	v_mfma_f32_16x16x32_bf16 v[12:15], v[148:151], v[220:223], v[12:15]
	v_mfma_f32_16x16x32_bf16 v[56:59], v[152:155], v[180:183], 0
	v_mfma_f32_16x16x32_bf16 v[52:55], v[160:163], v[180:183], 0
	v_mfma_f32_16x16x32_bf16 v[40:43], v[152:155], v[188:191], 0
	v_mfma_f32_16x16x32_bf16 v[36:39], v[160:163], v[188:191], 0
	v_mfma_f32_16x16x32_bf16 v[24:27], v[152:155], v[204:207], 0
	v_mfma_f32_16x16x32_bf16 v[20:23], v[160:163], v[204:207], 0
	v_mfma_f32_16x16x32_bf16 v[8:11], v[152:155], v[216:219], 0
	v_mfma_f32_16x16x32_bf16 v[4:7], v[160:163], v[216:219], 0
	v_mfma_f32_16x16x32_bf16 v[56:59], v[156:159], v[184:187], v[56:59]
	v_mfma_f32_16x16x32_bf16 v[52:55], v[164:167], v[184:187], v[52:55]
	v_mfma_f32_16x16x32_bf16 v[40:43], v[156:159], v[192:195], v[40:43]
	v_mfma_f32_16x16x32_bf16 v[36:39], v[164:167], v[192:195], v[36:39]
	v_mfma_f32_16x16x32_bf16 v[24:27], v[156:159], v[212:215], v[24:27]
	v_mfma_f32_16x16x32_bf16 v[20:23], v[164:167], v[212:215], v[20:23]
	v_mfma_f32_16x16x32_bf16 v[8:11], v[156:159], v[220:223], v[8:11]
	v_mfma_f32_16x16x32_bf16 v[4:7], v[164:167], v[220:223], v[4:7]
	s_barrier
	s_add_i32 s80, 0, 0x18000
	v_add_u32_e32 v2, s80, v203
	s_add_i32 s81, 0, 0x1c000
	ds_read_b128 v[104:107], v2
	ds_read_b128 v[124:127], v2 offset:1024
	ds_read_b128 v[128:131], v2 offset:2048
	ds_read_b128 v[148:151], v2 offset:3072
	v_add_u32_e32 v2, s81, v203
	ds_read_b128 v[152:155], v2
	ds_read_b128 v[156:159], v2 offset:1024
	ds_read_b128 v[160:163], v2 offset:2048
	ds_read_b128 v[164:167], v2 offset:3072
	s_add_u32 s4, s4, 0x40000
	s_addc_u32 s5, s5, 0
	s_mov_b32 m0, s58
	v_lshl_add_u64 v[208:209], s[4:5], 0, v[174:175]
	ds_read_b128 v[180:183], v210 offset:32768
	ds_read_b128 v[184:187], v210 offset:33792
	ds_read_b128 v[188:191], v210 offset:34816
	ds_read_b128 v[192:195], v210 offset:35840
	ds_read_b128 v[204:207], v210 offset:36864
	ds_read_b128 v[212:215], v210 offset:37888
	ds_read_b128 v[216:219], v210 offset:38912
	ds_read_b128 v[220:223], v210 offset:39936
	global_load_lds_dwordx4 v[208:209], off
	s_mov_b32 m0, s59
	v_lshl_add_u64 v[208:209], s[4:5], 0, v[170:171]
	global_load_lds_dwordx4 v[208:209], off
	s_waitcnt vmcnt(8)
	s_waitcnt lgkmcnt(0)
	s_barrier
	v_mfma_f32_16x16x32_bf16 v[144:147], v[104:107], v[180:183], v[144:147]
	v_mfma_f32_16x16x32_bf16 v[140:143], v[128:131], v[180:183], v[140:143]
	v_mfma_f32_16x16x32_bf16 v[120:123], v[104:107], v[188:191], v[120:123]
	v_mfma_f32_16x16x32_bf16 v[116:119], v[128:131], v[188:191], v[116:119]
	v_mfma_f32_16x16x32_bf16 v[96:99], v[104:107], v[204:207], v[96:99]
	v_mfma_f32_16x16x32_bf16 v[92:95], v[128:131], v[204:207], v[92:95]
	v_mfma_f32_16x16x32_bf16 v[80:83], v[104:107], v[216:219], v[80:83]
	v_mfma_f32_16x16x32_bf16 v[76:79], v[128:131], v[216:219], v[76:79]
	v_mfma_f32_16x16x32_bf16 v[144:147], v[124:127], v[184:187], v[144:147]
	v_mfma_f32_16x16x32_bf16 v[140:143], v[148:151], v[184:187], v[140:143]
	v_mfma_f32_16x16x32_bf16 v[120:123], v[124:127], v[192:195], v[120:123]
	v_mfma_f32_16x16x32_bf16 v[116:119], v[148:151], v[192:195], v[116:119]
	v_mfma_f32_16x16x32_bf16 v[96:99], v[124:127], v[212:215], v[96:99]
	v_mfma_f32_16x16x32_bf16 v[92:95], v[148:151], v[212:215], v[92:95]
	v_mfma_f32_16x16x32_bf16 v[80:83], v[124:127], v[220:223], v[80:83]
	v_mfma_f32_16x16x32_bf16 v[76:79], v[148:151], v[220:223], v[76:79]
	v_mfma_f32_16x16x32_bf16 v[136:139], v[152:155], v[180:183], v[136:139]
	v_mfma_f32_16x16x32_bf16 v[132:135], v[160:163], v[180:183], v[132:135]
	v_mfma_f32_16x16x32_bf16 v[112:115], v[152:155], v[188:191], v[112:115]
	v_mfma_f32_16x16x32_bf16 v[108:111], v[160:163], v[188:191], v[108:111]
	v_mfma_f32_16x16x32_bf16 v[88:91], v[152:155], v[204:207], v[88:91]
	v_mfma_f32_16x16x32_bf16 v[84:87], v[160:163], v[204:207], v[84:87]
	v_mfma_f32_16x16x32_bf16 v[72:75], v[152:155], v[216:219], v[72:75]
	v_mfma_f32_16x16x32_bf16 v[68:71], v[160:163], v[216:219], v[68:71]
	v_mfma_f32_16x16x32_bf16 v[136:139], v[156:159], v[184:187], v[136:139]
	v_mfma_f32_16x16x32_bf16 v[132:135], v[164:167], v[184:187], v[132:135]
	v_mfma_f32_16x16x32_bf16 v[112:115], v[156:159], v[192:195], v[112:115]
	v_mfma_f32_16x16x32_bf16 v[108:111], v[164:167], v[192:195], v[108:111]
	v_mfma_f32_16x16x32_bf16 v[88:91], v[156:159], v[212:215], v[88:91]
	v_mfma_f32_16x16x32_bf16 v[84:87], v[164:167], v[212:215], v[84:87]
	v_mfma_f32_16x16x32_bf16 v[72:75], v[156:159], v[220:223], v[72:75]
	v_mfma_f32_16x16x32_bf16 v[68:71], v[164:167], v[220:223], v[68:71]
	s_barrier
	s_add_i32 s4, s80, s46
	v_lshl_add_u64 v[196:197], v[196:197], 0, s[34:35]
	s_mov_b32 m0, s4
	ds_read_b128 v[180:183], v210 offset:49152
	ds_read_b128 v[184:187], v210 offset:50176
	ds_read_b128 v[188:191], v210 offset:51200
	ds_read_b128 v[192:195], v210 offset:52224
	ds_read_b128 v[204:207], v210 offset:53248
	ds_read_b128 v[212:215], v210 offset:54272
	ds_read_b128 v[216:219], v210 offset:55296
	ds_read_b128 v[220:223], v210 offset:56320
	global_load_lds_dwordx4 v[196:197], off
	s_add_i32 m0, s4, 0x2000
	s_add_u32 s4, s48, 0x20080
	v_lshl_add_u64 v[196:197], v[198:199], 0, s[34:35]
	s_addc_u32 s5, s49, 0
	s_add_i32 s48, s81, s46
	global_load_lds_dwordx4 v[196:197], off
	s_mov_b32 m0, s48
	v_lshl_add_u64 v[196:197], s[4:5], 0, v[172:173]
	global_load_lds_dwordx4 v[196:197], off
	s_add_i32 m0, s48, 0x2000
	v_lshl_add_u64 v[196:197], s[4:5], 0, v[168:169]
	global_load_lds_dwordx4 v[196:197], off
	s_mov_b32 m0, s68
	v_lshl_add_u64 v[196:197], s[44:45], 0, v[174:175]
	global_load_lds_dwordx4 v[196:197], off
	s_mov_b32 m0, s69
	v_lshl_add_u64 v[196:197], s[44:45], 0, v[170:171]
	global_load_lds_dwordx4 v[196:197], off
	s_waitcnt vmcnt(8)
	s_waitcnt lgkmcnt(0)
	s_barrier
	v_mfma_f32_16x16x32_bf16 v[64:67], v[104:107], v[180:183], v[64:67]
	v_mfma_f32_16x16x32_bf16 v[60:63], v[128:131], v[180:183], v[60:63]
	v_mfma_f32_16x16x32_bf16 v[48:51], v[104:107], v[188:191], v[48:51]
	v_mfma_f32_16x16x32_bf16 v[44:47], v[128:131], v[188:191], v[44:47]
	v_mfma_f32_16x16x32_bf16 v[32:35], v[104:107], v[204:207], v[32:35]
	v_mfma_f32_16x16x32_bf16 v[28:31], v[128:131], v[204:207], v[28:31]
	v_mfma_f32_16x16x32_bf16 v[16:19], v[104:107], v[216:219], v[16:19]
	v_mfma_f32_16x16x32_bf16 v[12:15], v[128:131], v[216:219], v[12:15]
	v_mfma_f32_16x16x32_bf16 v[64:67], v[124:127], v[184:187], v[64:67]
	v_mfma_f32_16x16x32_bf16 v[60:63], v[148:151], v[184:187], v[60:63]
	v_mfma_f32_16x16x32_bf16 v[48:51], v[124:127], v[192:195], v[48:51]
	v_mfma_f32_16x16x32_bf16 v[44:47], v[148:151], v[192:195], v[44:47]
	v_mfma_f32_16x16x32_bf16 v[32:35], v[124:127], v[212:215], v[32:35]
	v_mfma_f32_16x16x32_bf16 v[28:31], v[148:151], v[212:215], v[28:31]
	v_mfma_f32_16x16x32_bf16 v[16:19], v[124:127], v[220:223], v[16:19]
	v_mfma_f32_16x16x32_bf16 v[12:15], v[148:151], v[220:223], v[12:15]
	v_mfma_f32_16x16x32_bf16 v[56:59], v[152:155], v[180:183], v[56:59]
	v_mfma_f32_16x16x32_bf16 v[52:55], v[160:163], v[180:183], v[52:55]
	v_mfma_f32_16x16x32_bf16 v[40:43], v[152:155], v[188:191], v[40:43]
	v_mfma_f32_16x16x32_bf16 v[36:39], v[160:163], v[188:191], v[36:39]
	v_mfma_f32_16x16x32_bf16 v[24:27], v[152:155], v[204:207], v[24:27]
	v_mfma_f32_16x16x32_bf16 v[20:23], v[160:163], v[204:207], v[20:23]
	v_mfma_f32_16x16x32_bf16 v[8:11], v[152:155], v[216:219], v[8:11]
	v_mfma_f32_16x16x32_bf16 v[4:7], v[160:163], v[216:219], v[4:7]
	v_mfma_f32_16x16x32_bf16 v[56:59], v[156:159], v[184:187], v[56:59]
	v_mfma_f32_16x16x32_bf16 v[52:55], v[164:167], v[184:187], v[52:55]
	v_mfma_f32_16x16x32_bf16 v[40:43], v[156:159], v[192:195], v[40:43]
	v_mfma_f32_16x16x32_bf16 v[36:39], v[164:167], v[192:195], v[36:39]
	v_mfma_f32_16x16x32_bf16 v[24:27], v[156:159], v[212:215], v[24:27]
	v_mfma_f32_16x16x32_bf16 v[20:23], v[164:167], v[212:215], v[20:23]
	v_mfma_f32_16x16x32_bf16 v[8:11], v[156:159], v[220:223], v[8:11]
	v_mfma_f32_16x16x32_bf16 v[4:7], v[164:167], v[220:223], v[4:7]
	s_barrier
	s_add_i32 s79, s79, 2
	s_add_u32 s42, s42, 0x100
	s_addc_u32 s43, s43, 0
	s_cmp_gt_u32 s79, 5
.LBB0_383:
	s_add_u32 s4, s40, s42
	s_addc_u32 s5, s41, s43
	s_add_u32 s80, s4, 0x100
	s_addc_u32 s81, s5, 0
	s_add_u32 s48, s77, s42
	s_addc_u32 s49, s78, s43
	s_add_u32 s4, s4, 0x180
	s_addc_u32 s5, s5, 0
	s_add_i32 s82, 0, 0x10000
	s_add_i32 s83, 0, 0x14000
	v_add_u32_e32 v2, s82, v203
	ds_read_b128 v[104:107], v2
	ds_read_b128 v[124:127], v2 offset:1024
	ds_read_b128 v[128:131], v2 offset:2048
	ds_read_b128 v[148:151], v2 offset:3072
	v_add_u32_e32 v2, s83, v203
	ds_read_b128 v[152:155], v2
	ds_read_b128 v[156:159], v2 offset:1024
	ds_read_b128 v[160:163], v2 offset:2048
	ds_read_b128 v[164:167], v2 offset:3072
	s_cmpk_eq_i32 s42, 0x300
	s_cselect_b32 s45, s76, s5
	s_cselect_b32 s44, s75, s4
	s_cselect_b32 s49, s11, s49
	s_cselect_b32 s48, s74, s48
	s_cselect_b32 s5, s51, s81
	s_cselect_b32 s4, s71, s80
	v_lshl_add_u64 v[196:197], v[100:101], 0, s[42:43]
	s_add_i32 m0, s47, 0xc000
	ds_read_b128 v[180:183], v210
	ds_read_b128 v[184:187], v210 offset:1024
	ds_read_b128 v[188:191], v210 offset:2048
	ds_read_b128 v[192:195], v210 offset:3072
	ds_read_b128 v[204:207], v210 offset:4096
	ds_read_b128 v[212:215], v210 offset:5120
	ds_read_b128 v[216:219], v210 offset:6144
	ds_read_b128 v[220:223], v210 offset:7168
	global_load_lds_dwordx4 v[196:197], off
	s_add_i32 m0, s47, 0xe000
	v_lshl_add_u64 v[196:197], v[102:103], 0, s[42:43]
	global_load_lds_dwordx4 v[196:197], off
	s_waitcnt vmcnt(8)
	s_waitcnt lgkmcnt(0)
	s_barrier
	v_mfma_f32_16x16x32_bf16 v[144:147], v[104:107], v[180:183], v[144:147]
	v_mfma_f32_16x16x32_bf16 v[140:143], v[128:131], v[180:183], v[140:143]
	v_mfma_f32_16x16x32_bf16 v[120:123], v[104:107], v[188:191], v[120:123]
	v_mfma_f32_16x16x32_bf16 v[116:119], v[128:131], v[188:191], v[116:119]
	v_mfma_f32_16x16x32_bf16 v[96:99], v[104:107], v[204:207], v[96:99]
	v_mfma_f32_16x16x32_bf16 v[92:95], v[128:131], v[204:207], v[92:95]
	v_mfma_f32_16x16x32_bf16 v[80:83], v[104:107], v[216:219], v[80:83]
	v_mfma_f32_16x16x32_bf16 v[76:79], v[128:131], v[216:219], v[76:79]
	v_mfma_f32_16x16x32_bf16 v[144:147], v[124:127], v[184:187], v[144:147]
	v_mfma_f32_16x16x32_bf16 v[140:143], v[148:151], v[184:187], v[140:143]
	v_mfma_f32_16x16x32_bf16 v[120:123], v[124:127], v[192:195], v[120:123]
	v_mfma_f32_16x16x32_bf16 v[116:119], v[148:151], v[192:195], v[116:119]
	v_mfma_f32_16x16x32_bf16 v[96:99], v[124:127], v[212:215], v[96:99]
	v_mfma_f32_16x16x32_bf16 v[92:95], v[148:151], v[212:215], v[92:95]
	v_mfma_f32_16x16x32_bf16 v[80:83], v[124:127], v[220:223], v[80:83]
	v_mfma_f32_16x16x32_bf16 v[76:79], v[148:151], v[220:223], v[76:79]
	v_mfma_f32_16x16x32_bf16 v[136:139], v[152:155], v[180:183], v[136:139]
	v_mfma_f32_16x16x32_bf16 v[132:135], v[160:163], v[180:183], v[132:135]
	v_mfma_f32_16x16x32_bf16 v[112:115], v[152:155], v[188:191], v[112:115]
	v_mfma_f32_16x16x32_bf16 v[108:111], v[160:163], v[188:191], v[108:111]
	v_mfma_f32_16x16x32_bf16 v[88:91], v[152:155], v[204:207], v[88:91]
	v_mfma_f32_16x16x32_bf16 v[84:87], v[160:163], v[204:207], v[84:87]
	v_mfma_f32_16x16x32_bf16 v[72:75], v[152:155], v[216:219], v[72:75]
	v_mfma_f32_16x16x32_bf16 v[68:71], v[160:163], v[216:219], v[68:71]
	v_mfma_f32_16x16x32_bf16 v[136:139], v[156:159], v[184:187], v[136:139]
	v_mfma_f32_16x16x32_bf16 v[132:135], v[164:167], v[184:187], v[132:135]
	v_mfma_f32_16x16x32_bf16 v[112:115], v[156:159], v[192:195], v[112:115]
	v_mfma_f32_16x16x32_bf16 v[108:111], v[164:167], v[192:195], v[108:111]
	v_mfma_f32_16x16x32_bf16 v[88:91], v[156:159], v[212:215], v[88:91]
	v_mfma_f32_16x16x32_bf16 v[84:87], v[164:167], v[212:215], v[84:87]
	v_mfma_f32_16x16x32_bf16 v[72:75], v[156:159], v[220:223], v[72:75]
	v_mfma_f32_16x16x32_bf16 v[68:71], v[164:167], v[220:223], v[68:71]
	s_barrier
	s_add_i32 s80, s82, s46
	v_lshl_add_u64 v[196:197], s[48:49], 0, v[172:173]
	s_mov_b32 m0, s80
	ds_read_b128 v[180:183], v210 offset:16384
	ds_read_b128 v[184:187], v210 offset:17408
	ds_read_b128 v[188:191], v210 offset:18432
	ds_read_b128 v[192:195], v210 offset:19456
	ds_read_b128 v[204:207], v210 offset:20480
	ds_read_b128 v[212:215], v210 offset:21504
	ds_read_b128 v[216:219], v210 offset:22528
	ds_read_b128 v[220:223], v210 offset:23552
	global_load_lds_dwordx4 v[196:197], off
	s_add_i32 m0, s80, 0x2000
	s_add_u32 s80, s48, 0x20000
	v_lshl_add_u64 v[198:199], s[48:49], 0, v[168:169]
	s_addc_u32 s81, s49, 0
	s_add_i32 s82, s83, s46
	global_load_lds_dwordx4 v[198:199], off
	s_mov_b32 m0, s82
	v_lshl_add_u64 v[208:209], s[80:81], 0, v[172:173]
	global_load_lds_dwordx4 v[208:209], off
	s_add_i32 m0, s82, 0x2000
	v_lshl_add_u64 v[208:209], s[80:81], 0, v[168:169]
	global_load_lds_dwordx4 v[208:209], off
	s_mov_b32 m0, s47
	v_lshl_add_u64 v[208:209], s[4:5], 0, v[174:175]
	global_load_lds_dwordx4 v[208:209], off
	s_mov_b32 m0, s56
	v_lshl_add_u64 v[208:209], s[4:5], 0, v[170:171]
	global_load_lds_dwordx4 v[208:209], off
	s_waitcnt vmcnt(8)
	s_waitcnt lgkmcnt(0)
	s_barrier
	v_mfma_f32_16x16x32_bf16 v[64:67], v[104:107], v[180:183], v[64:67]
	v_mfma_f32_16x16x32_bf16 v[60:63], v[128:131], v[180:183], v[60:63]
	v_mfma_f32_16x16x32_bf16 v[48:51], v[104:107], v[188:191], v[48:51]
	v_mfma_f32_16x16x32_bf16 v[44:47], v[128:131], v[188:191], v[44:47]
	v_mfma_f32_16x16x32_bf16 v[32:35], v[104:107], v[204:207], v[32:35]
	v_mfma_f32_16x16x32_bf16 v[28:31], v[128:131], v[204:207], v[28:31]
	v_mfma_f32_16x16x32_bf16 v[16:19], v[104:107], v[216:219], v[16:19]
	v_mfma_f32_16x16x32_bf16 v[12:15], v[128:131], v[216:219], v[12:15]
	v_mfma_f32_16x16x32_bf16 v[64:67], v[124:127], v[184:187], v[64:67]
	v_mfma_f32_16x16x32_bf16 v[60:63], v[148:151], v[184:187], v[60:63]
	v_mfma_f32_16x16x32_bf16 v[48:51], v[124:127], v[192:195], v[48:51]
	v_mfma_f32_16x16x32_bf16 v[44:47], v[148:151], v[192:195], v[44:47]
	v_mfma_f32_16x16x32_bf16 v[32:35], v[124:127], v[212:215], v[32:35]
	v_mfma_f32_16x16x32_bf16 v[28:31], v[148:151], v[212:215], v[28:31]
	v_mfma_f32_16x16x32_bf16 v[16:19], v[124:127], v[220:223], v[16:19]
	v_mfma_f32_16x16x32_bf16 v[12:15], v[148:151], v[220:223], v[12:15]
	v_mfma_f32_16x16x32_bf16 v[56:59], v[152:155], v[180:183], v[56:59]
	v_mfma_f32_16x16x32_bf16 v[52:55], v[160:163], v[180:183], v[52:55]
	v_mfma_f32_16x16x32_bf16 v[40:43], v[152:155], v[188:191], v[40:43]
	v_mfma_f32_16x16x32_bf16 v[36:39], v[160:163], v[188:191], v[36:39]
	v_mfma_f32_16x16x32_bf16 v[24:27], v[152:155], v[204:207], v[24:27]
	v_mfma_f32_16x16x32_bf16 v[20:23], v[160:163], v[204:207], v[20:23]
	v_mfma_f32_16x16x32_bf16 v[8:11], v[152:155], v[216:219], v[8:11]
	v_mfma_f32_16x16x32_bf16 v[4:7], v[160:163], v[216:219], v[4:7]
	v_mfma_f32_16x16x32_bf16 v[56:59], v[156:159], v[184:187], v[56:59]
	v_mfma_f32_16x16x32_bf16 v[52:55], v[164:167], v[184:187], v[52:55]
	v_mfma_f32_16x16x32_bf16 v[40:43], v[156:159], v[192:195], v[40:43]
	v_mfma_f32_16x16x32_bf16 v[36:39], v[164:167], v[192:195], v[36:39]
	v_mfma_f32_16x16x32_bf16 v[24:27], v[156:159], v[212:215], v[24:27]
	v_mfma_f32_16x16x32_bf16 v[20:23], v[164:167], v[212:215], v[20:23]
	v_mfma_f32_16x16x32_bf16 v[8:11], v[156:159], v[220:223], v[8:11]
	v_mfma_f32_16x16x32_bf16 v[4:7], v[164:167], v[220:223], v[4:7]
	s_barrier
	s_add_i32 s80, 0, 0x18000
	v_add_u32_e32 v2, s80, v203
	s_add_i32 s81, 0, 0x1c000
	ds_read_b128 v[104:107], v2
	ds_read_b128 v[124:127], v2 offset:1024
	ds_read_b128 v[128:131], v2 offset:2048
	ds_read_b128 v[148:151], v2 offset:3072
	v_add_u32_e32 v2, s81, v203
	ds_read_b128 v[152:155], v2
	ds_read_b128 v[156:159], v2 offset:1024
	ds_read_b128 v[160:163], v2 offset:2048
	ds_read_b128 v[164:167], v2 offset:3072
	s_add_u32 s4, s4, 0x40000
	s_addc_u32 s5, s5, 0
	s_mov_b32 m0, s58
	v_lshl_add_u64 v[208:209], s[4:5], 0, v[174:175]
	ds_read_b128 v[180:183], v210 offset:32768
	ds_read_b128 v[184:187], v210 offset:33792
	ds_read_b128 v[188:191], v210 offset:34816
	ds_read_b128 v[192:195], v210 offset:35840
	ds_read_b128 v[204:207], v210 offset:36864
	ds_read_b128 v[212:215], v210 offset:37888
	ds_read_b128 v[216:219], v210 offset:38912
	ds_read_b128 v[220:223], v210 offset:39936
	global_load_lds_dwordx4 v[208:209], off
	s_mov_b32 m0, s59
	v_lshl_add_u64 v[208:209], s[4:5], 0, v[170:171]
	global_load_lds_dwordx4 v[208:209], off
	s_waitcnt vmcnt(8)
	s_waitcnt lgkmcnt(0)
	s_barrier
	v_mfma_f32_16x16x32_bf16 v[144:147], v[104:107], v[180:183], v[144:147]
	v_mfma_f32_16x16x32_bf16 v[140:143], v[128:131], v[180:183], v[140:143]
	v_mfma_f32_16x16x32_bf16 v[120:123], v[104:107], v[188:191], v[120:123]
	v_mfma_f32_16x16x32_bf16 v[116:119], v[128:131], v[188:191], v[116:119]
	v_mfma_f32_16x16x32_bf16 v[96:99], v[104:107], v[204:207], v[96:99]
	v_mfma_f32_16x16x32_bf16 v[92:95], v[128:131], v[204:207], v[92:95]
	v_mfma_f32_16x16x32_bf16 v[80:83], v[104:107], v[216:219], v[80:83]
	v_mfma_f32_16x16x32_bf16 v[76:79], v[128:131], v[216:219], v[76:79]
	v_mfma_f32_16x16x32_bf16 v[144:147], v[124:127], v[184:187], v[144:147]
	v_mfma_f32_16x16x32_bf16 v[140:143], v[148:151], v[184:187], v[140:143]
	v_mfma_f32_16x16x32_bf16 v[120:123], v[124:127], v[192:195], v[120:123]
	v_mfma_f32_16x16x32_bf16 v[116:119], v[148:151], v[192:195], v[116:119]
	v_mfma_f32_16x16x32_bf16 v[96:99], v[124:127], v[212:215], v[96:99]
	v_mfma_f32_16x16x32_bf16 v[92:95], v[148:151], v[212:215], v[92:95]
	v_mfma_f32_16x16x32_bf16 v[80:83], v[124:127], v[220:223], v[80:83]
	v_mfma_f32_16x16x32_bf16 v[76:79], v[148:151], v[220:223], v[76:79]
	v_mfma_f32_16x16x32_bf16 v[136:139], v[152:155], v[180:183], v[136:139]
	v_mfma_f32_16x16x32_bf16 v[132:135], v[160:163], v[180:183], v[132:135]
	v_mfma_f32_16x16x32_bf16 v[112:115], v[152:155], v[188:191], v[112:115]
	v_mfma_f32_16x16x32_bf16 v[108:111], v[160:163], v[188:191], v[108:111]
	v_mfma_f32_16x16x32_bf16 v[88:91], v[152:155], v[204:207], v[88:91]
	v_mfma_f32_16x16x32_bf16 v[84:87], v[160:163], v[204:207], v[84:87]
	v_mfma_f32_16x16x32_bf16 v[72:75], v[152:155], v[216:219], v[72:75]
	v_mfma_f32_16x16x32_bf16 v[68:71], v[160:163], v[216:219], v[68:71]
	v_mfma_f32_16x16x32_bf16 v[136:139], v[156:159], v[184:187], v[136:139]
	v_mfma_f32_16x16x32_bf16 v[132:135], v[164:167], v[184:187], v[132:135]
	v_mfma_f32_16x16x32_bf16 v[112:115], v[156:159], v[192:195], v[112:115]
	v_mfma_f32_16x16x32_bf16 v[108:111], v[164:167], v[192:195], v[108:111]
	v_mfma_f32_16x16x32_bf16 v[88:91], v[156:159], v[212:215], v[88:91]
	v_mfma_f32_16x16x32_bf16 v[84:87], v[164:167], v[212:215], v[84:87]
	v_mfma_f32_16x16x32_bf16 v[72:75], v[156:159], v[220:223], v[72:75]
	v_mfma_f32_16x16x32_bf16 v[68:71], v[164:167], v[220:223], v[68:71]
	s_barrier
	s_add_i32 s4, s80, s46
	v_lshl_add_u64 v[196:197], v[196:197], 0, s[34:35]
	s_mov_b32 m0, s4
	ds_read_b128 v[180:183], v210 offset:49152
	ds_read_b128 v[184:187], v210 offset:50176
	ds_read_b128 v[188:191], v210 offset:51200
	ds_read_b128 v[192:195], v210 offset:52224
	ds_read_b128 v[204:207], v210 offset:53248
	ds_read_b128 v[212:215], v210 offset:54272
	ds_read_b128 v[216:219], v210 offset:55296
	ds_read_b128 v[220:223], v210 offset:56320
	global_load_lds_dwordx4 v[196:197], off
	s_add_i32 m0, s4, 0x2000
	s_add_u32 s4, s48, 0x20080
	v_lshl_add_u64 v[196:197], v[198:199], 0, s[34:35]
	s_addc_u32 s5, s49, 0
	s_add_i32 s48, s81, s46
	global_load_lds_dwordx4 v[196:197], off
	s_mov_b32 m0, s48
	v_lshl_add_u64 v[196:197], s[4:5], 0, v[172:173]
	global_load_lds_dwordx4 v[196:197], off
	s_add_i32 m0, s48, 0x2000
	v_lshl_add_u64 v[196:197], s[4:5], 0, v[168:169]
	global_load_lds_dwordx4 v[196:197], off
	s_mov_b32 m0, s68
	v_lshl_add_u64 v[196:197], s[44:45], 0, v[174:175]
	global_load_lds_dwordx4 v[196:197], off
	s_mov_b32 m0, s69
	v_lshl_add_u64 v[196:197], s[44:45], 0, v[170:171]
	global_load_lds_dwordx4 v[196:197], off
	s_waitcnt vmcnt(8)
	s_waitcnt lgkmcnt(0)
	s_barrier
	v_mfma_f32_16x16x32_bf16 v[64:67], v[104:107], v[180:183], v[64:67]
	v_mfma_f32_16x16x32_bf16 v[60:63], v[128:131], v[180:183], v[60:63]
	v_mfma_f32_16x16x32_bf16 v[48:51], v[104:107], v[188:191], v[48:51]
	v_mfma_f32_16x16x32_bf16 v[44:47], v[128:131], v[188:191], v[44:47]
	v_mfma_f32_16x16x32_bf16 v[32:35], v[104:107], v[204:207], v[32:35]
	v_mfma_f32_16x16x32_bf16 v[28:31], v[128:131], v[204:207], v[28:31]
	v_mfma_f32_16x16x32_bf16 v[16:19], v[104:107], v[216:219], v[16:19]
	v_mfma_f32_16x16x32_bf16 v[12:15], v[128:131], v[216:219], v[12:15]
	v_mfma_f32_16x16x32_bf16 v[64:67], v[124:127], v[184:187], v[64:67]
	v_mfma_f32_16x16x32_bf16 v[60:63], v[148:151], v[184:187], v[60:63]
	v_mfma_f32_16x16x32_bf16 v[48:51], v[124:127], v[192:195], v[48:51]
	v_mfma_f32_16x16x32_bf16 v[44:47], v[148:151], v[192:195], v[44:47]
	v_mfma_f32_16x16x32_bf16 v[32:35], v[124:127], v[212:215], v[32:35]
	v_mfma_f32_16x16x32_bf16 v[28:31], v[148:151], v[212:215], v[28:31]
	v_mfma_f32_16x16x32_bf16 v[16:19], v[124:127], v[220:223], v[16:19]
	v_mfma_f32_16x16x32_bf16 v[12:15], v[148:151], v[220:223], v[12:15]
	v_mfma_f32_16x16x32_bf16 v[56:59], v[152:155], v[180:183], v[56:59]
	v_mfma_f32_16x16x32_bf16 v[52:55], v[160:163], v[180:183], v[52:55]
	v_mfma_f32_16x16x32_bf16 v[40:43], v[152:155], v[188:191], v[40:43]
	v_mfma_f32_16x16x32_bf16 v[36:39], v[160:163], v[188:191], v[36:39]
	v_mfma_f32_16x16x32_bf16 v[24:27], v[152:155], v[204:207], v[24:27]
	v_mfma_f32_16x16x32_bf16 v[20:23], v[160:163], v[204:207], v[20:23]
	v_mfma_f32_16x16x32_bf16 v[8:11], v[152:155], v[216:219], v[8:11]
	v_mfma_f32_16x16x32_bf16 v[4:7], v[160:163], v[216:219], v[4:7]
	v_mfma_f32_16x16x32_bf16 v[56:59], v[156:159], v[184:187], v[56:59]
	v_mfma_f32_16x16x32_bf16 v[52:55], v[164:167], v[184:187], v[52:55]
	v_mfma_f32_16x16x32_bf16 v[40:43], v[156:159], v[192:195], v[40:43]
	v_mfma_f32_16x16x32_bf16 v[36:39], v[164:167], v[192:195], v[36:39]
	v_mfma_f32_16x16x32_bf16 v[24:27], v[156:159], v[212:215], v[24:27]
	v_mfma_f32_16x16x32_bf16 v[20:23], v[164:167], v[212:215], v[20:23]
	v_mfma_f32_16x16x32_bf16 v[8:11], v[156:159], v[220:223], v[8:11]
	v_mfma_f32_16x16x32_bf16 v[4:7], v[164:167], v[220:223], v[4:7]
	s_barrier
	s_add_i32 s79, s79, 2
	s_add_u32 s42, s42, 0x100
	s_addc_u32 s43, s43, 0
	s_cmp_gt_u32 s79, 5
	s_cbranch_scc0 .LBB0_383
	s_and_b64 vcc, exec, s[72:73]
	s_cbranch_vccz .LBB0_386
	s_barrier

.LBB0_1043:
	s_ashr_i32 s41, s40, 31
	s_lshl_b64 s[4:5], s[40:41], 19
	s_add_u32 s42, s6, s4
	s_addc_u32 s43, s7, s5
	s_and_b64 s[4:5], s[38:39], exec
	s_cselect_b32 s41, s43, s49
	s_cselect_b32 s65, s42, s48
	s_ashr_i32 s37, s36, 31
	s_lshl_b64 s[4:5], s[36:37], 19
	s_add_u32 s44, s8, s4
	s_addc_u32 s45, s9, s5
	s_and_b64 s[4:5], s[38:39], exec
	s_cselect_b32 s37, s45, s51
	s_cselect_b32 s68, s44, s50
	s_add_u32 s69, s65, 0x80
	s_addc_u32 s70, s41, 0
	s_add_u32 s4, s48, 0x40080
	s_addc_u32 s5, s49, 0
	s_add_u32 s71, s50, 0x100
	v_lshl_add_u64 v[140:141], s[4:5], 0, v[136:137]
	v_lshl_add_u64 v[142:143], s[4:5], 0, v[138:139]
	s_addc_u32 s72, s51, 0
	s_mov_b32 s73, -2
	s_mov_b64 s[50:51], 0
	s_waitcnt vmcnt(0)
	s_add_u32 s4, s48, s50
	s_addc_u32 s5, s49, s51
	s_add_u32 s74, s4, 0x100
	s_addc_u32 s75, s5, 0
	s_add_u32 s52, s71, s50
	s_addc_u32 s53, s72, s51
	s_add_u32 s4, s4, 0x180
	s_addc_u32 s5, s5, 0
	s_add_i32 s76, 0, 0x10000
	s_add_i32 s77, 0, 0x14000
	v_add_u32_e32 v2, s76, v203
	ds_read_b128 v[144:147], v2
	ds_read_b128 v[148:151], v2 offset:1024
	ds_read_b128 v[152:155], v2 offset:2048
	ds_read_b128 v[156:159], v2 offset:3072
	v_add_u32_e32 v2, s77, v203
	ds_read_b128 v[160:163], v2
	ds_read_b128 v[164:167], v2 offset:1024
	ds_read_b128 v[168:171], v2 offset:2048
	ds_read_b128 v[172:175], v2 offset:3072
	s_cmpk_eq_i32 s50, 0x700
	s_cselect_b32 s13, s70, s5
	s_cselect_b32 s12, s69, s4
	s_cselect_b32 s53, s37, s53
	s_cselect_b32 s52, s68, s52
	s_cselect_b32 s5, s41, s75
	s_cselect_b32 s4, s65, s74
	v_lshl_add_u64 v[212:213], v[140:141], 0, s[50:51]
	s_add_i32 m0, s17, 0xc000
	ds_read_b128 v[176:179], v224
	ds_read_b128 v[180:183], v224 offset:1024
	ds_read_b128 v[184:187], v224 offset:2048
	ds_read_b128 v[188:191], v224 offset:3072
	ds_read_b128 v[192:195], v224 offset:4096
	ds_read_b128 v[196:199], v224 offset:5120
	ds_read_b128 v[204:207], v224 offset:6144
	ds_read_b128 v[208:211], v224 offset:7168
	global_load_lds_dwordx4 v[212:213], off
	s_add_i32 m0, s17, 0xe000
	v_lshl_add_u64 v[212:213], v[142:143], 0, s[50:51]
	global_load_lds_dwordx4 v[212:213], off
	s_waitcnt vmcnt(8)
	s_waitcnt lgkmcnt(0)
	s_barrier
	v_mfma_f32_16x16x32_bf16 v[128:131], v[144:147], v[176:179], 0
	v_mfma_f32_16x16x32_bf16 v[124:127], v[152:155], v[176:179], 0
	v_mfma_f32_16x16x32_bf16 v[112:115], v[144:147], v[184:187], 0
	v_mfma_f32_16x16x32_bf16 v[108:111], v[152:155], v[184:187], 0
	v_mfma_f32_16x16x32_bf16 v[96:99], v[144:147], v[192:195], 0
	v_mfma_f32_16x16x32_bf16 v[92:95], v[152:155], v[192:195], 0
	v_mfma_f32_16x16x32_bf16 v[80:83], v[144:147], v[204:207], 0
	v_mfma_f32_16x16x32_bf16 v[76:79], v[152:155], v[204:207], 0
	v_mfma_f32_16x16x32_bf16 v[128:131], v[148:151], v[180:183], v[128:131]
	v_mfma_f32_16x16x32_bf16 v[124:127], v[156:159], v[180:183], v[124:127]
	v_mfma_f32_16x16x32_bf16 v[112:115], v[148:151], v[188:191], v[112:115]
	v_mfma_f32_16x16x32_bf16 v[108:111], v[156:159], v[188:191], v[108:111]
	v_mfma_f32_16x16x32_bf16 v[96:99], v[148:151], v[196:199], v[96:99]
	v_mfma_f32_16x16x32_bf16 v[92:95], v[156:159], v[196:199], v[92:95]
	v_mfma_f32_16x16x32_bf16 v[80:83], v[148:151], v[208:211], v[80:83]
	v_mfma_f32_16x16x32_bf16 v[76:79], v[156:159], v[208:211], v[76:79]
	v_mfma_f32_16x16x32_bf16 v[120:123], v[160:163], v[176:179], 0
	v_mfma_f32_16x16x32_bf16 v[116:119], v[168:171], v[176:179], 0
	v_mfma_f32_16x16x32_bf16 v[104:107], v[160:163], v[184:187], 0
	v_mfma_f32_16x16x32_bf16 v[100:103], v[168:171], v[184:187], 0
	v_mfma_f32_16x16x32_bf16 v[88:91], v[160:163], v[192:195], 0
	v_mfma_f32_16x16x32_bf16 v[84:87], v[168:171], v[192:195], 0
	v_mfma_f32_16x16x32_bf16 v[72:75], v[160:163], v[204:207], 0
	v_mfma_f32_16x16x32_bf16 v[68:71], v[168:171], v[204:207], 0
	v_mfma_f32_16x16x32_bf16 v[120:123], v[164:167], v[180:183], v[120:123]
	v_mfma_f32_16x16x32_bf16 v[116:119], v[172:175], v[180:183], v[116:119]
	v_mfma_f32_16x16x32_bf16 v[104:107], v[164:167], v[188:191], v[104:107]
	v_mfma_f32_16x16x32_bf16 v[100:103], v[172:175], v[188:191], v[100:103]
	v_mfma_f32_16x16x32_bf16 v[88:91], v[164:167], v[196:199], v[88:91]
	v_mfma_f32_16x16x32_bf16 v[84:87], v[172:175], v[196:199], v[84:87]
	v_mfma_f32_16x16x32_bf16 v[72:75], v[164:167], v[208:211], v[72:75]
	v_mfma_f32_16x16x32_bf16 v[68:71], v[172:175], v[208:211], v[68:71]
	s_barrier
	s_add_i32 s74, s76, s16
	v_lshl_add_u64 v[212:213], s[52:53], 0, v[134:135]
	s_mov_b32 m0, s74
	ds_read_b128 v[176:179], v224 offset:16384
	ds_read_b128 v[180:183], v224 offset:17408
	ds_read_b128 v[184:187], v224 offset:18432
	ds_read_b128 v[188:191], v224 offset:19456
	ds_read_b128 v[192:195], v224 offset:20480
	ds_read_b128 v[196:199], v224 offset:21504
	ds_read_b128 v[204:207], v224 offset:22528
	ds_read_b128 v[208:211], v224 offset:23552
	global_load_lds_dwordx4 v[212:213], off
	s_add_i32 m0, s74, 0x2000
	s_add_u32 s74, s52, 0x40000
	v_lshl_add_u64 v[214:215], s[52:53], 0, v[132:133]
	s_addc_u32 s75, s53, 0
	s_add_i32 s76, s77, s16
	global_load_lds_dwordx4 v[214:215], off
	s_mov_b32 m0, s76
	v_lshl_add_u64 v[216:217], s[74:75], 0, v[134:135]
	global_load_lds_dwordx4 v[216:217], off
	s_add_i32 m0, s76, 0x2000
	v_lshl_add_u64 v[216:217], s[74:75], 0, v[132:133]
	global_load_lds_dwordx4 v[216:217], off
	s_mov_b32 m0, s17
	v_lshl_add_u64 v[216:217], s[4:5], 0, v[134:135]
	global_load_lds_dwordx4 v[216:217], off
	s_mov_b32 m0, s46
	v_lshl_add_u64 v[216:217], s[4:5], 0, v[132:133]
	global_load_lds_dwordx4 v[216:217], off
	s_waitcnt vmcnt(8)
	s_waitcnt lgkmcnt(0)
	s_barrier
	v_mfma_f32_16x16x32_bf16 v[64:67], v[144:147], v[176:179], 0
	v_mfma_f32_16x16x32_bf16 v[60:63], v[152:155], v[176:179], 0
	v_mfma_f32_16x16x32_bf16 v[48:51], v[144:147], v[184:187], 0
	v_mfma_f32_16x16x32_bf16 v[44:47], v[152:155], v[184:187], 0
	v_mfma_f32_16x16x32_bf16 v[32:35], v[144:147], v[192:195], 0
	v_mfma_f32_16x16x32_bf16 v[28:31], v[152:155], v[192:195], 0
	v_mfma_f32_16x16x32_bf16 v[16:19], v[144:147], v[204:207], 0
	v_mfma_f32_16x16x32_bf16 v[12:15], v[152:155], v[204:207], 0
	v_mfma_f32_16x16x32_bf16 v[64:67], v[148:151], v[180:183], v[64:67]
	v_mfma_f32_16x16x32_bf16 v[60:63], v[156:159], v[180:183], v[60:63]
	v_mfma_f32_16x16x32_bf16 v[48:51], v[148:151], v[188:191], v[48:51]
	v_mfma_f32_16x16x32_bf16 v[44:47], v[156:159], v[188:191], v[44:47]
	v_mfma_f32_16x16x32_bf16 v[32:35], v[148:151], v[196:199], v[32:35]
	v_mfma_f32_16x16x32_bf16 v[28:31], v[156:159], v[196:199], v[28:31]
	v_mfma_f32_16x16x32_bf16 v[16:19], v[148:151], v[208:211], v[16:19]
	v_mfma_f32_16x16x32_bf16 v[12:15], v[156:159], v[208:211], v[12:15]
	v_mfma_f32_16x16x32_bf16 v[56:59], v[160:163], v[176:179], 0
	v_mfma_f32_16x16x32_bf16 v[52:55], v[168:171], v[176:179], 0
	v_mfma_f32_16x16x32_bf16 v[40:43], v[160:163], v[184:187], 0
	v_mfma_f32_16x16x32_bf16 v[36:39], v[168:171], v[184:187], 0
	v_mfma_f32_16x16x32_bf16 v[24:27], v[160:163], v[192:195], 0
	v_mfma_f32_16x16x32_bf16 v[20:23], v[168:171], v[192:195], 0
	v_mfma_f32_16x16x32_bf16 v[8:11], v[160:163], v[204:207], 0
	v_mfma_f32_16x16x32_bf16 v[4:7], v[168:171], v[204:207], 0
	v_mfma_f32_16x16x32_bf16 v[56:59], v[164:167], v[180:183], v[56:59]
	v_mfma_f32_16x16x32_bf16 v[52:55], v[172:175], v[180:183], v[52:55]
	v_mfma_f32_16x16x32_bf16 v[40:43], v[164:167], v[188:191], v[40:43]
	v_mfma_f32_16x16x32_bf16 v[36:39], v[172:175], v[188:191], v[36:39]
	v_mfma_f32_16x16x32_bf16 v[24:27], v[164:167], v[196:199], v[24:27]
	v_mfma_f32_16x16x32_bf16 v[20:23], v[172:175], v[196:199], v[20:23]
	v_mfma_f32_16x16x32_bf16 v[8:11], v[164:167], v[208:211], v[8:11]
	v_mfma_f32_16x16x32_bf16 v[4:7], v[172:175], v[208:211], v[4:7]
	s_barrier
	s_add_i32 s74, 0, 0x18000
	v_add_u32_e32 v2, s74, v203
	s_add_i32 s75, 0, 0x1c000
	ds_read_b128 v[144:147], v2
	ds_read_b128 v[148:151], v2 offset:1024
	ds_read_b128 v[152:155], v2 offset:2048
	ds_read_b128 v[156:159], v2 offset:3072
	v_add_u32_e32 v2, s75, v203
	ds_read_b128 v[160:163], v2
	ds_read_b128 v[164:167], v2 offset:1024
	ds_read_b128 v[168:171], v2 offset:2048
	ds_read_b128 v[172:175], v2 offset:3072
	s_add_u32 s4, s4, 0x40000
	s_addc_u32 s5, s5, 0
	s_mov_b32 m0, s47
	v_lshl_add_u64 v[216:217], s[4:5], 0, v[134:135]
	ds_read_b128 v[176:179], v224 offset:32768
	ds_read_b128 v[180:183], v224 offset:33792
	ds_read_b128 v[184:187], v224 offset:34816
	ds_read_b128 v[188:191], v224 offset:35840
	ds_read_b128 v[192:195], v224 offset:36864
	ds_read_b128 v[196:199], v224 offset:37888
	ds_read_b128 v[204:207], v224 offset:38912
	ds_read_b128 v[208:211], v224 offset:39936
	global_load_lds_dwordx4 v[216:217], off
	s_mov_b32 m0, s56
	v_lshl_add_u64 v[216:217], s[4:5], 0, v[132:133]
	global_load_lds_dwordx4 v[216:217], off
	s_waitcnt vmcnt(8)
	s_waitcnt lgkmcnt(0)
	s_barrier
	v_mfma_f32_16x16x32_bf16 v[128:131], v[144:147], v[176:179], v[128:131]
	v_mfma_f32_16x16x32_bf16 v[124:127], v[152:155], v[176:179], v[124:127]
	v_mfma_f32_16x16x32_bf16 v[112:115], v[144:147], v[184:187], v[112:115]
	v_mfma_f32_16x16x32_bf16 v[108:111], v[152:155], v[184:187], v[108:111]
	v_mfma_f32_16x16x32_bf16 v[96:99], v[144:147], v[192:195], v[96:99]
	v_mfma_f32_16x16x32_bf16 v[92:95], v[152:155], v[192:195], v[92:95]
	v_mfma_f32_16x16x32_bf16 v[80:83], v[144:147], v[204:207], v[80:83]
	v_mfma_f32_16x16x32_bf16 v[76:79], v[152:155], v[204:207], v[76:79]
	v_mfma_f32_16x16x32_bf16 v[128:131], v[148:151], v[180:183], v[128:131]
	v_mfma_f32_16x16x32_bf16 v[124:127], v[156:159], v[180:183], v[124:127]
	v_mfma_f32_16x16x32_bf16 v[112:115], v[148:151], v[188:191], v[112:115]
	v_mfma_f32_16x16x32_bf16 v[108:111], v[156:159], v[188:191], v[108:111]
	v_mfma_f32_16x16x32_bf16 v[96:99], v[148:151], v[196:199], v[96:99]
	v_mfma_f32_16x16x32_bf16 v[92:95], v[156:159], v[196:199], v[92:95]
	v_mfma_f32_16x16x32_bf16 v[80:83], v[148:151], v[208:211], v[80:83]
	v_mfma_f32_16x16x32_bf16 v[76:79], v[156:159], v[208:211], v[76:79]
	v_mfma_f32_16x16x32_bf16 v[120:123], v[160:163], v[176:179], v[120:123]
	v_mfma_f32_16x16x32_bf16 v[116:119], v[168:171], v[176:179], v[116:119]
	v_mfma_f32_16x16x32_bf16 v[104:107], v[160:163], v[184:187], v[104:107]
	v_mfma_f32_16x16x32_bf16 v[100:103], v[168:171], v[184:187], v[100:103]
	v_mfma_f32_16x16x32_bf16 v[88:91], v[160:163], v[192:195], v[88:91]
	v_mfma_f32_16x16x32_bf16 v[84:87], v[168:171], v[192:195], v[84:87]
	v_mfma_f32_16x16x32_bf16 v[72:75], v[160:163], v[204:207], v[72:75]
	v_mfma_f32_16x16x32_bf16 v[68:71], v[168:171], v[204:207], v[68:71]
	v_mfma_f32_16x16x32_bf16 v[120:123], v[164:167], v[180:183], v[120:123]
	v_mfma_f32_16x16x32_bf16 v[116:119], v[172:175], v[180:183], v[116:119]
	v_mfma_f32_16x16x32_bf16 v[104:107], v[164:167], v[188:191], v[104:107]
	v_mfma_f32_16x16x32_bf16 v[100:103], v[172:175], v[188:191], v[100:103]
	v_mfma_f32_16x16x32_bf16 v[88:91], v[164:167], v[196:199], v[88:91]
	v_mfma_f32_16x16x32_bf16 v[84:87], v[172:175], v[196:199], v[84:87]
	v_mfma_f32_16x16x32_bf16 v[72:75], v[164:167], v[208:211], v[72:75]
	v_mfma_f32_16x16x32_bf16 v[68:71], v[172:175], v[208:211], v[68:71]
	s_barrier
	s_add_i32 s4, s74, s16
	v_lshl_add_u64 v[212:213], v[212:213], 0, s[34:35]
	s_mov_b32 m0, s4
	ds_read_b128 v[176:179], v224 offset:49152
	ds_read_b128 v[180:183], v224 offset:50176
	ds_read_b128 v[184:187], v224 offset:51200
	ds_read_b128 v[188:191], v224 offset:52224
	ds_read_b128 v[192:195], v224 offset:53248
	ds_read_b128 v[196:199], v224 offset:54272
	ds_read_b128 v[204:207], v224 offset:55296
	ds_read_b128 v[208:211], v224 offset:56320
	global_load_lds_dwordx4 v[212:213], off
	s_add_i32 m0, s4, 0x2000
	s_add_u32 s4, s52, 0x40080
	v_lshl_add_u64 v[212:213], v[214:215], 0, s[34:35]
	s_addc_u32 s5, s53, 0
	s_add_i32 s52, s75, s16
	global_load_lds_dwordx4 v[212:213], off
	s_mov_b32 m0, s52
	v_lshl_add_u64 v[212:213], s[4:5], 0, v[134:135]
	global_load_lds_dwordx4 v[212:213], off
	s_add_i32 m0, s52, 0x2000
	v_lshl_add_u64 v[212:213], s[4:5], 0, v[132:133]
	global_load_lds_dwordx4 v[212:213], off
	s_mov_b32 m0, s59
	v_lshl_add_u64 v[212:213], s[12:13], 0, v[134:135]
	global_load_lds_dwordx4 v[212:213], off
	s_mov_b32 m0, s60
	v_lshl_add_u64 v[212:213], s[12:13], 0, v[132:133]
	global_load_lds_dwordx4 v[212:213], off
	s_waitcnt vmcnt(8)
	s_waitcnt lgkmcnt(0)
	s_barrier
	v_mfma_f32_16x16x32_bf16 v[64:67], v[144:147], v[176:179], v[64:67]
	v_mfma_f32_16x16x32_bf16 v[60:63], v[152:155], v[176:179], v[60:63]
	v_mfma_f32_16x16x32_bf16 v[48:51], v[144:147], v[184:187], v[48:51]
	v_mfma_f32_16x16x32_bf16 v[44:47], v[152:155], v[184:187], v[44:47]
	v_mfma_f32_16x16x32_bf16 v[32:35], v[144:147], v[192:195], v[32:35]
	v_mfma_f32_16x16x32_bf16 v[28:31], v[152:155], v[192:195], v[28:31]
	v_mfma_f32_16x16x32_bf16 v[16:19], v[144:147], v[204:207], v[16:19]
	v_mfma_f32_16x16x32_bf16 v[12:15], v[152:155], v[204:207], v[12:15]
	v_mfma_f32_16x16x32_bf16 v[64:67], v[148:151], v[180:183], v[64:67]
	v_mfma_f32_16x16x32_bf16 v[60:63], v[156:159], v[180:183], v[60:63]
	v_mfma_f32_16x16x32_bf16 v[48:51], v[148:151], v[188:191], v[48:51]
	v_mfma_f32_16x16x32_bf16 v[44:47], v[156:159], v[188:191], v[44:47]
	v_mfma_f32_16x16x32_bf16 v[32:35], v[148:151], v[196:199], v[32:35]
	v_mfma_f32_16x16x32_bf16 v[28:31], v[156:159], v[196:199], v[28:31]
	v_mfma_f32_16x16x32_bf16 v[16:19], v[148:151], v[208:211], v[16:19]
	v_mfma_f32_16x16x32_bf16 v[12:15], v[156:159], v[208:211], v[12:15]
	v_mfma_f32_16x16x32_bf16 v[56:59], v[160:163], v[176:179], v[56:59]
	v_mfma_f32_16x16x32_bf16 v[52:55], v[168:171], v[176:179], v[52:55]
	v_mfma_f32_16x16x32_bf16 v[40:43], v[160:163], v[184:187], v[40:43]
	v_mfma_f32_16x16x32_bf16 v[36:39], v[168:171], v[184:187], v[36:39]
	v_mfma_f32_16x16x32_bf16 v[24:27], v[160:163], v[192:195], v[24:27]
	v_mfma_f32_16x16x32_bf16 v[20:23], v[168:171], v[192:195], v[20:23]
	v_mfma_f32_16x16x32_bf16 v[8:11], v[160:163], v[204:207], v[8:11]
	v_mfma_f32_16x16x32_bf16 v[4:7], v[168:171], v[204:207], v[4:7]
	v_mfma_f32_16x16x32_bf16 v[56:59], v[164:167], v[180:183], v[56:59]
	v_mfma_f32_16x16x32_bf16 v[52:55], v[172:175], v[180:183], v[52:55]
	v_mfma_f32_16x16x32_bf16 v[40:43], v[164:167], v[188:191], v[40:43]
	v_mfma_f32_16x16x32_bf16 v[36:39], v[172:175], v[188:191], v[36:39]
	v_mfma_f32_16x16x32_bf16 v[24:27], v[164:167], v[196:199], v[24:27]
	v_mfma_f32_16x16x32_bf16 v[20:23], v[172:175], v[196:199], v[20:23]
	v_mfma_f32_16x16x32_bf16 v[8:11], v[164:167], v[208:211], v[8:11]
	v_mfma_f32_16x16x32_bf16 v[4:7], v[172:175], v[208:211], v[4:7]
	s_barrier
	s_add_i32 s73, s73, 2
	s_add_u32 s50, s50, 0x100
	s_addc_u32 s51, s51, 0
	s_cmp_gt_u32 s73, 13
.LBB0_1044:
	s_add_u32 s4, s48, s50
	s_addc_u32 s5, s49, s51
	s_add_u32 s74, s4, 0x100
	s_addc_u32 s75, s5, 0
	s_add_u32 s52, s71, s50
	s_addc_u32 s53, s72, s51
	s_add_u32 s4, s4, 0x180
	s_addc_u32 s5, s5, 0
	s_add_i32 s76, 0, 0x10000
	s_add_i32 s77, 0, 0x14000
	v_add_u32_e32 v2, s76, v203
	ds_read_b128 v[144:147], v2
	ds_read_b128 v[148:151], v2 offset:1024
	ds_read_b128 v[152:155], v2 offset:2048
	ds_read_b128 v[156:159], v2 offset:3072
	v_add_u32_e32 v2, s77, v203
	ds_read_b128 v[160:163], v2
	ds_read_b128 v[164:167], v2 offset:1024
	ds_read_b128 v[168:171], v2 offset:2048
	ds_read_b128 v[172:175], v2 offset:3072
	s_cmpk_eq_i32 s50, 0x700
	s_cselect_b32 s13, s70, s5
	s_cselect_b32 s12, s69, s4
	s_cselect_b32 s53, s37, s53
	s_cselect_b32 s52, s68, s52
	s_cselect_b32 s5, s41, s75
	s_cselect_b32 s4, s65, s74
	v_lshl_add_u64 v[212:213], v[140:141], 0, s[50:51]
	s_add_i32 m0, s17, 0xc000
	ds_read_b128 v[176:179], v224
	ds_read_b128 v[180:183], v224 offset:1024
	ds_read_b128 v[184:187], v224 offset:2048
	ds_read_b128 v[188:191], v224 offset:3072
	ds_read_b128 v[192:195], v224 offset:4096
	ds_read_b128 v[196:199], v224 offset:5120
	ds_read_b128 v[204:207], v224 offset:6144
	ds_read_b128 v[208:211], v224 offset:7168
	global_load_lds_dwordx4 v[212:213], off
	s_add_i32 m0, s17, 0xe000
	v_lshl_add_u64 v[212:213], v[142:143], 0, s[50:51]
	global_load_lds_dwordx4 v[212:213], off
	s_waitcnt vmcnt(8)
	s_waitcnt lgkmcnt(0)
	s_barrier
	v_mfma_f32_16x16x32_bf16 v[128:131], v[144:147], v[176:179], v[128:131]
	v_mfma_f32_16x16x32_bf16 v[124:127], v[152:155], v[176:179], v[124:127]
	v_mfma_f32_16x16x32_bf16 v[112:115], v[144:147], v[184:187], v[112:115]
	v_mfma_f32_16x16x32_bf16 v[108:111], v[152:155], v[184:187], v[108:111]
	v_mfma_f32_16x16x32_bf16 v[96:99], v[144:147], v[192:195], v[96:99]
	v_mfma_f32_16x16x32_bf16 v[92:95], v[152:155], v[192:195], v[92:95]
	v_mfma_f32_16x16x32_bf16 v[80:83], v[144:147], v[204:207], v[80:83]
	v_mfma_f32_16x16x32_bf16 v[76:79], v[152:155], v[204:207], v[76:79]
	v_mfma_f32_16x16x32_bf16 v[128:131], v[148:151], v[180:183], v[128:131]
	v_mfma_f32_16x16x32_bf16 v[124:127], v[156:159], v[180:183], v[124:127]
	v_mfma_f32_16x16x32_bf16 v[112:115], v[148:151], v[188:191], v[112:115]
	v_mfma_f32_16x16x32_bf16 v[108:111], v[156:159], v[188:191], v[108:111]
	v_mfma_f32_16x16x32_bf16 v[96:99], v[148:151], v[196:199], v[96:99]
	v_mfma_f32_16x16x32_bf16 v[92:95], v[156:159], v[196:199], v[92:95]
	v_mfma_f32_16x16x32_bf16 v[80:83], v[148:151], v[208:211], v[80:83]
	v_mfma_f32_16x16x32_bf16 v[76:79], v[156:159], v[208:211], v[76:79]
	v_mfma_f32_16x16x32_bf16 v[120:123], v[160:163], v[176:179], v[120:123]
	v_mfma_f32_16x16x32_bf16 v[116:119], v[168:171], v[176:179], v[116:119]
	v_mfma_f32_16x16x32_bf16 v[104:107], v[160:163], v[184:187], v[104:107]
	v_mfma_f32_16x16x32_bf16 v[100:103], v[168:171], v[184:187], v[100:103]
	v_mfma_f32_16x16x32_bf16 v[88:91], v[160:163], v[192:195], v[88:91]
	v_mfma_f32_16x16x32_bf16 v[84:87], v[168:171], v[192:195], v[84:87]
	v_mfma_f32_16x16x32_bf16 v[72:75], v[160:163], v[204:207], v[72:75]
	v_mfma_f32_16x16x32_bf16 v[68:71], v[168:171], v[204:207], v[68:71]
	v_mfma_f32_16x16x32_bf16 v[120:123], v[164:167], v[180:183], v[120:123]
	v_mfma_f32_16x16x32_bf16 v[116:119], v[172:175], v[180:183], v[116:119]
	v_mfma_f32_16x16x32_bf16 v[104:107], v[164:167], v[188:191], v[104:107]
	v_mfma_f32_16x16x32_bf16 v[100:103], v[172:175], v[188:191], v[100:103]
	v_mfma_f32_16x16x32_bf16 v[88:91], v[164:167], v[196:199], v[88:91]
	v_mfma_f32_16x16x32_bf16 v[84:87], v[172:175], v[196:199], v[84:87]
	v_mfma_f32_16x16x32_bf16 v[72:75], v[164:167], v[208:211], v[72:75]
	v_mfma_f32_16x16x32_bf16 v[68:71], v[172:175], v[208:211], v[68:71]
	s_barrier
	s_add_i32 s74, s76, s16
	v_lshl_add_u64 v[212:213], s[52:53], 0, v[134:135]
	s_mov_b32 m0, s74
	ds_read_b128 v[176:179], v224 offset:16384
	ds_read_b128 v[180:183], v224 offset:17408
	ds_read_b128 v[184:187], v224 offset:18432
	ds_read_b128 v[188:191], v224 offset:19456
	ds_read_b128 v[192:195], v224 offset:20480
	ds_read_b128 v[196:199], v224 offset:21504
	ds_read_b128 v[204:207], v224 offset:22528
	ds_read_b128 v[208:211], v224 offset:23552
	global_load_lds_dwordx4 v[212:213], off
	s_add_i32 m0, s74, 0x2000
	s_add_u32 s74, s52, 0x40000
	v_lshl_add_u64 v[214:215], s[52:53], 0, v[132:133]
	s_addc_u32 s75, s53, 0
	s_add_i32 s76, s77, s16
	global_load_lds_dwordx4 v[214:215], off
	s_mov_b32 m0, s76
	v_lshl_add_u64 v[216:217], s[74:75], 0, v[134:135]
	global_load_lds_dwordx4 v[216:217], off
	s_add_i32 m0, s76, 0x2000
	v_lshl_add_u64 v[216:217], s[74:75], 0, v[132:133]
	global_load_lds_dwordx4 v[216:217], off
	s_mov_b32 m0, s17
	v_lshl_add_u64 v[216:217], s[4:5], 0, v[134:135]
	global_load_lds_dwordx4 v[216:217], off
	s_mov_b32 m0, s46
	v_lshl_add_u64 v[216:217], s[4:5], 0, v[132:133]
	global_load_lds_dwordx4 v[216:217], off
	s_waitcnt vmcnt(8)
	s_waitcnt lgkmcnt(0)
	s_barrier
	v_mfma_f32_16x16x32_bf16 v[64:67], v[144:147], v[176:179], v[64:67]
	v_mfma_f32_16x16x32_bf16 v[60:63], v[152:155], v[176:179], v[60:63]
	v_mfma_f32_16x16x32_bf16 v[48:51], v[144:147], v[184:187], v[48:51]
	v_mfma_f32_16x16x32_bf16 v[44:47], v[152:155], v[184:187], v[44:47]
	v_mfma_f32_16x16x32_bf16 v[32:35], v[144:147], v[192:195], v[32:35]
	v_mfma_f32_16x16x32_bf16 v[28:31], v[152:155], v[192:195], v[28:31]
	v_mfma_f32_16x16x32_bf16 v[16:19], v[144:147], v[204:207], v[16:19]
	v_mfma_f32_16x16x32_bf16 v[12:15], v[152:155], v[204:207], v[12:15]
	v_mfma_f32_16x16x32_bf16 v[64:67], v[148:151], v[180:183], v[64:67]
	v_mfma_f32_16x16x32_bf16 v[60:63], v[156:159], v[180:183], v[60:63]
	v_mfma_f32_16x16x32_bf16 v[48:51], v[148:151], v[188:191], v[48:51]
	v_mfma_f32_16x16x32_bf16 v[44:47], v[156:159], v[188:191], v[44:47]
	v_mfma_f32_16x16x32_bf16 v[32:35], v[148:151], v[196:199], v[32:35]
	v_mfma_f32_16x16x32_bf16 v[28:31], v[156:159], v[196:199], v[28:31]
	v_mfma_f32_16x16x32_bf16 v[16:19], v[148:151], v[208:211], v[16:19]
	v_mfma_f32_16x16x32_bf16 v[12:15], v[156:159], v[208:211], v[12:15]
	v_mfma_f32_16x16x32_bf16 v[56:59], v[160:163], v[176:179], v[56:59]
	v_mfma_f32_16x16x32_bf16 v[52:55], v[168:171], v[176:179], v[52:55]
	v_mfma_f32_16x16x32_bf16 v[40:43], v[160:163], v[184:187], v[40:43]
	v_mfma_f32_16x16x32_bf16 v[36:39], v[168:171], v[184:187], v[36:39]
	v_mfma_f32_16x16x32_bf16 v[24:27], v[160:163], v[192:195], v[24:27]
	v_mfma_f32_16x16x32_bf16 v[20:23], v[168:171], v[192:195], v[20:23]
	v_mfma_f32_16x16x32_bf16 v[8:11], v[160:163], v[204:207], v[8:11]
	v_mfma_f32_16x16x32_bf16 v[4:7], v[168:171], v[204:207], v[4:7]
	v_mfma_f32_16x16x32_bf16 v[56:59], v[164:167], v[180:183], v[56:59]
	v_mfma_f32_16x16x32_bf16 v[52:55], v[172:175], v[180:183], v[52:55]
	v_mfma_f32_16x16x32_bf16 v[40:43], v[164:167], v[188:191], v[40:43]
	v_mfma_f32_16x16x32_bf16 v[36:39], v[172:175], v[188:191], v[36:39]
	v_mfma_f32_16x16x32_bf16 v[24:27], v[164:167], v[196:199], v[24:27]
	v_mfma_f32_16x16x32_bf16 v[20:23], v[172:175], v[196:199], v[20:23]
	v_mfma_f32_16x16x32_bf16 v[8:11], v[164:167], v[208:211], v[8:11]
	v_mfma_f32_16x16x32_bf16 v[4:7], v[172:175], v[208:211], v[4:7]
	s_barrier
	s_add_i32 s74, 0, 0x18000
	v_add_u32_e32 v2, s74, v203
	s_add_i32 s75, 0, 0x1c000
	ds_read_b128 v[144:147], v2
	ds_read_b128 v[148:151], v2 offset:1024
	ds_read_b128 v[152:155], v2 offset:2048
	ds_read_b128 v[156:159], v2 offset:3072
	v_add_u32_e32 v2, s75, v203
	ds_read_b128 v[160:163], v2
	ds_read_b128 v[164:167], v2 offset:1024
	ds_read_b128 v[168:171], v2 offset:2048
	ds_read_b128 v[172:175], v2 offset:3072
	s_add_u32 s4, s4, 0x40000
	s_addc_u32 s5, s5, 0
	s_mov_b32 m0, s47
	v_lshl_add_u64 v[216:217], s[4:5], 0, v[134:135]
	ds_read_b128 v[176:179], v224 offset:32768
	ds_read_b128 v[180:183], v224 offset:33792
	ds_read_b128 v[184:187], v224 offset:34816
	ds_read_b128 v[188:191], v224 offset:35840
	ds_read_b128 v[192:195], v224 offset:36864
	ds_read_b128 v[196:199], v224 offset:37888
	ds_read_b128 v[204:207], v224 offset:38912
	ds_read_b128 v[208:211], v224 offset:39936
	global_load_lds_dwordx4 v[216:217], off
	s_mov_b32 m0, s56
	v_lshl_add_u64 v[216:217], s[4:5], 0, v[132:133]
	global_load_lds_dwordx4 v[216:217], off
	s_waitcnt vmcnt(8)
	s_waitcnt lgkmcnt(0)
	s_barrier
	v_mfma_f32_16x16x32_bf16 v[128:131], v[144:147], v[176:179], v[128:131]
	v_mfma_f32_16x16x32_bf16 v[124:127], v[152:155], v[176:179], v[124:127]
	v_mfma_f32_16x16x32_bf16 v[112:115], v[144:147], v[184:187], v[112:115]
	v_mfma_f32_16x16x32_bf16 v[108:111], v[152:155], v[184:187], v[108:111]
	v_mfma_f32_16x16x32_bf16 v[96:99], v[144:147], v[192:195], v[96:99]
	v_mfma_f32_16x16x32_bf16 v[92:95], v[152:155], v[192:195], v[92:95]
	v_mfma_f32_16x16x32_bf16 v[80:83], v[144:147], v[204:207], v[80:83]
	v_mfma_f32_16x16x32_bf16 v[76:79], v[152:155], v[204:207], v[76:79]
	v_mfma_f32_16x16x32_bf16 v[128:131], v[148:151], v[180:183], v[128:131]
	v_mfma_f32_16x16x32_bf16 v[124:127], v[156:159], v[180:183], v[124:127]
	v_mfma_f32_16x16x32_bf16 v[112:115], v[148:151], v[188:191], v[112:115]
	v_mfma_f32_16x16x32_bf16 v[108:111], v[156:159], v[188:191], v[108:111]
	v_mfma_f32_16x16x32_bf16 v[96:99], v[148:151], v[196:199], v[96:99]
	v_mfma_f32_16x16x32_bf16 v[92:95], v[156:159], v[196:199], v[92:95]
	v_mfma_f32_16x16x32_bf16 v[80:83], v[148:151], v[208:211], v[80:83]
	v_mfma_f32_16x16x32_bf16 v[76:79], v[156:159], v[208:211], v[76:79]
	v_mfma_f32_16x16x32_bf16 v[120:123], v[160:163], v[176:179], v[120:123]
	v_mfma_f32_16x16x32_bf16 v[116:119], v[168:171], v[176:179], v[116:119]
	v_mfma_f32_16x16x32_bf16 v[104:107], v[160:163], v[184:187], v[104:107]
	v_mfma_f32_16x16x32_bf16 v[100:103], v[168:171], v[184:187], v[100:103]
	v_mfma_f32_16x16x32_bf16 v[88:91], v[160:163], v[192:195], v[88:91]
	v_mfma_f32_16x16x32_bf16 v[84:87], v[168:171], v[192:195], v[84:87]
	v_mfma_f32_16x16x32_bf16 v[72:75], v[160:163], v[204:207], v[72:75]
	v_mfma_f32_16x16x32_bf16 v[68:71], v[168:171], v[204:207], v[68:71]
	v_mfma_f32_16x16x32_bf16 v[120:123], v[164:167], v[180:183], v[120:123]
	v_mfma_f32_16x16x32_bf16 v[116:119], v[172:175], v[180:183], v[116:119]
	v_mfma_f32_16x16x32_bf16 v[104:107], v[164:167], v[188:191], v[104:107]
	v_mfma_f32_16x16x32_bf16 v[100:103], v[172:175], v[188:191], v[100:103]
	v_mfma_f32_16x16x32_bf16 v[88:91], v[164:167], v[196:199], v[88:91]
	v_mfma_f32_16x16x32_bf16 v[84:87], v[172:175], v[196:199], v[84:87]
	v_mfma_f32_16x16x32_bf16 v[72:75], v[164:167], v[208:211], v[72:75]
	v_mfma_f32_16x16x32_bf16 v[68:71], v[172:175], v[208:211], v[68:71]
	s_barrier
	s_add_i32 s4, s74, s16
	v_lshl_add_u64 v[212:213], v[212:213], 0, s[34:35]
	s_mov_b32 m0, s4
	ds_read_b128 v[176:179], v224 offset:49152
	ds_read_b128 v[180:183], v224 offset:50176
	ds_read_b128 v[184:187], v224 offset:51200
	ds_read_b128 v[188:191], v224 offset:52224
	ds_read_b128 v[192:195], v224 offset:53248
	ds_read_b128 v[196:199], v224 offset:54272
	ds_read_b128 v[204:207], v224 offset:55296
	ds_read_b128 v[208:211], v224 offset:56320
	global_load_lds_dwordx4 v[212:213], off
	s_add_i32 m0, s4, 0x2000
	s_add_u32 s4, s52, 0x40080
	v_lshl_add_u64 v[212:213], v[214:215], 0, s[34:35]
	s_addc_u32 s5, s53, 0
	s_add_i32 s52, s75, s16
	global_load_lds_dwordx4 v[212:213], off
	s_mov_b32 m0, s52
	v_lshl_add_u64 v[212:213], s[4:5], 0, v[134:135]
	global_load_lds_dwordx4 v[212:213], off
	s_add_i32 m0, s52, 0x2000
	v_lshl_add_u64 v[212:213], s[4:5], 0, v[132:133]
	global_load_lds_dwordx4 v[212:213], off
	s_mov_b32 m0, s59
	v_lshl_add_u64 v[212:213], s[12:13], 0, v[134:135]
	global_load_lds_dwordx4 v[212:213], off
	s_mov_b32 m0, s60
	v_lshl_add_u64 v[212:213], s[12:13], 0, v[132:133]
	global_load_lds_dwordx4 v[212:213], off
	s_waitcnt vmcnt(8)
	s_waitcnt lgkmcnt(0)
	s_barrier
	v_mfma_f32_16x16x32_bf16 v[64:67], v[144:147], v[176:179], v[64:67]
	v_mfma_f32_16x16x32_bf16 v[60:63], v[152:155], v[176:179], v[60:63]
	v_mfma_f32_16x16x32_bf16 v[48:51], v[144:147], v[184:187], v[48:51]
	v_mfma_f32_16x16x32_bf16 v[44:47], v[152:155], v[184:187], v[44:47]
	v_mfma_f32_16x16x32_bf16 v[32:35], v[144:147], v[192:195], v[32:35]
	v_mfma_f32_16x16x32_bf16 v[28:31], v[152:155], v[192:195], v[28:31]
	v_mfma_f32_16x16x32_bf16 v[16:19], v[144:147], v[204:207], v[16:19]
	v_mfma_f32_16x16x32_bf16 v[12:15], v[152:155], v[204:207], v[12:15]
	v_mfma_f32_16x16x32_bf16 v[64:67], v[148:151], v[180:183], v[64:67]
	v_mfma_f32_16x16x32_bf16 v[60:63], v[156:159], v[180:183], v[60:63]
	v_mfma_f32_16x16x32_bf16 v[48:51], v[148:151], v[188:191], v[48:51]
	v_mfma_f32_16x16x32_bf16 v[44:47], v[156:159], v[188:191], v[44:47]
	v_mfma_f32_16x16x32_bf16 v[32:35], v[148:151], v[196:199], v[32:35]
	v_mfma_f32_16x16x32_bf16 v[28:31], v[156:159], v[196:199], v[28:31]
	v_mfma_f32_16x16x32_bf16 v[16:19], v[148:151], v[208:211], v[16:19]
	v_mfma_f32_16x16x32_bf16 v[12:15], v[156:159], v[208:211], v[12:15]
	v_mfma_f32_16x16x32_bf16 v[56:59], v[160:163], v[176:179], v[56:59]
	v_mfma_f32_16x16x32_bf16 v[52:55], v[168:171], v[176:179], v[52:55]
	v_mfma_f32_16x16x32_bf16 v[40:43], v[160:163], v[184:187], v[40:43]
	v_mfma_f32_16x16x32_bf16 v[36:39], v[168:171], v[184:187], v[36:39]
	v_mfma_f32_16x16x32_bf16 v[24:27], v[160:163], v[192:195], v[24:27]
	v_mfma_f32_16x16x32_bf16 v[20:23], v[168:171], v[192:195], v[20:23]
	v_mfma_f32_16x16x32_bf16 v[8:11], v[160:163], v[204:207], v[8:11]
	v_mfma_f32_16x16x32_bf16 v[4:7], v[168:171], v[204:207], v[4:7]
	v_mfma_f32_16x16x32_bf16 v[56:59], v[164:167], v[180:183], v[56:59]
	v_mfma_f32_16x16x32_bf16 v[52:55], v[172:175], v[180:183], v[52:55]
	v_mfma_f32_16x16x32_bf16 v[40:43], v[164:167], v[188:191], v[40:43]
	v_mfma_f32_16x16x32_bf16 v[36:39], v[172:175], v[188:191], v[36:39]
	v_mfma_f32_16x16x32_bf16 v[24:27], v[164:167], v[196:199], v[24:27]
	v_mfma_f32_16x16x32_bf16 v[20:23], v[172:175], v[196:199], v[20:23]
	v_mfma_f32_16x16x32_bf16 v[8:11], v[164:167], v[208:211], v[8:11]
	v_mfma_f32_16x16x32_bf16 v[4:7], v[172:175], v[208:211], v[4:7]
	s_barrier
	s_add_i32 s73, s73, 2
	s_add_u32 s50, s50, 0x100
	s_addc_u32 s51, s51, 0
	s_cmp_gt_u32 s73, 13
	s_cbranch_scc0 .LBB0_1044
	s_and_b64 vcc, exec, s[22:23]
	s_cbranch_vccz .LBB0_1047
	s_barrier

.LBB0_1117:
	s_ashr_i32 s37, s36, 31
	s_lshl_b64 s[4:5], s[36:37], 19
	s_add_u32 s40, s6, s4
	s_addc_u32 s41, s7, s5
	s_and_b64 s[4:5], s[38:39], exec
	s_cselect_b32 s37, s41, s45
	s_cselect_b32 s64, s40, s44
	s_ashr_i32 s23, s22, 31
	s_lshl_b64 s[4:5], s[22:23], 19
	s_add_u32 s42, s8, s4
	s_addc_u32 s43, s9, s5
	s_and_b64 s[4:5], s[38:39], exec
	s_cselect_b32 s23, s43, s49
	s_cselect_b32 s65, s42, s48
	s_add_u32 s68, s64, 0x80
	s_addc_u32 s69, s37, 0
	s_add_u32 s70, s48, 0x100
	s_addc_u32 s71, s49, 0
	s_add_u32 s4, s44, 0x40080
	s_addc_u32 s5, s45, 0
	v_lshl_add_u64 v[108:109], s[4:5], 0, v[210:211]
	v_lshl_add_u64 v[110:111], s[4:5], 0, v[212:213]
	s_mov_b32 s72, -2
	s_mov_b64 s[48:49], 0
	s_waitcnt lgkmcnt(0)
	s_waitcnt vmcnt(0)
	s_add_u32 s4, s44, s48
	s_addc_u32 s5, s45, s49
	s_add_u32 s73, s4, 0x100
	s_addc_u32 s74, s5, 0
	s_add_u32 s50, s70, s48
	s_addc_u32 s51, s71, s49
	s_add_u32 s4, s4, 0x180
	s_addc_u32 s5, s5, 0
	s_add_i32 s75, 0, 0x10000
	s_add_i32 s76, 0, 0x14000
	v_add_u32_e32 v148, s75, v203
	v_add_u32_e32 v164, s76, v203
	ds_read_b128 v[116:119], v148
	ds_read_b128 v[128:131], v148 offset:1024
	ds_read_b128 v[136:139], v148 offset:2048
	ds_read_b128 v[148:151], v148 offset:3072
	ds_read_b128 v[152:155], v164
	ds_read_b128 v[156:159], v164 offset:1024
	ds_read_b128 v[160:163], v164 offset:2048
	ds_read_b128 v[164:167], v164 offset:3072
	s_cmpk_eq_i32 s48, 0x700
	s_cselect_b32 s13, s69, s5
	s_cselect_b32 s12, s68, s4
	s_cselect_b32 s51, s23, s51
	s_cselect_b32 s50, s65, s50
	s_cselect_b32 s5, s37, s74
	s_cselect_b32 s4, s64, s73
	v_lshl_add_u64 v[214:215], v[108:109], 0, s[48:49]
	s_add_i32 m0, s17, 0xc000
	ds_read_b128 v[168:171], v236
	ds_read_b128 v[172:175], v236 offset:1024
	ds_read_b128 v[176:179], v236 offset:2048
	ds_read_b128 v[180:183], v236 offset:3072
	ds_read_b128 v[184:187], v236 offset:4096
	ds_read_b128 v[188:191], v236 offset:5120
	ds_read_b128 v[192:195], v236 offset:6144
	ds_read_b128 v[196:199], v236 offset:7168
	global_load_lds_dwordx4 v[214:215], off
	s_add_i32 m0, s17, 0xe000
	v_lshl_add_u64 v[214:215], v[110:111], 0, s[48:49]
	global_load_lds_dwordx4 v[214:215], off
	s_waitcnt vmcnt(8)
	s_waitcnt lgkmcnt(0)
	s_barrier
	v_mfma_f32_16x16x32_bf16 v[144:147], v[116:119], v[168:171], 0
	v_mfma_f32_16x16x32_bf16 v[140:143], v[136:139], v[168:171], 0
	v_mfma_f32_16x16x32_bf16 v[120:123], v[116:119], v[176:179], 0
	v_mfma_f32_16x16x32_bf16 v[112:115], v[136:139], v[176:179], 0
	v_mfma_f32_16x16x32_bf16 v[96:99], v[116:119], v[184:187], 0
	v_mfma_f32_16x16x32_bf16 v[92:95], v[136:139], v[184:187], 0
	v_mfma_f32_16x16x32_bf16 v[80:83], v[116:119], v[192:195], 0
	v_mfma_f32_16x16x32_bf16 v[76:79], v[136:139], v[192:195], 0
	v_mfma_f32_16x16x32_bf16 v[144:147], v[128:131], v[172:175], v[144:147]
	v_mfma_f32_16x16x32_bf16 v[140:143], v[148:151], v[172:175], v[140:143]
	v_mfma_f32_16x16x32_bf16 v[120:123], v[128:131], v[180:183], v[120:123]
	v_mfma_f32_16x16x32_bf16 v[112:115], v[148:151], v[180:183], v[112:115]
	v_mfma_f32_16x16x32_bf16 v[96:99], v[128:131], v[188:191], v[96:99]
	v_mfma_f32_16x16x32_bf16 v[92:95], v[148:151], v[188:191], v[92:95]
	v_mfma_f32_16x16x32_bf16 v[80:83], v[128:131], v[196:199], v[80:83]
	v_mfma_f32_16x16x32_bf16 v[76:79], v[148:151], v[196:199], v[76:79]
	v_mfma_f32_16x16x32_bf16 v[132:135], v[152:155], v[168:171], 0
	v_mfma_f32_16x16x32_bf16 v[124:127], v[160:163], v[168:171], 0
	v_mfma_f32_16x16x32_bf16 v[104:107], v[152:155], v[176:179], 0
	v_mfma_f32_16x16x32_bf16 v[100:103], v[160:163], v[176:179], 0
	v_mfma_f32_16x16x32_bf16 v[88:91], v[152:155], v[184:187], 0
	v_mfma_f32_16x16x32_bf16 v[84:87], v[160:163], v[184:187], 0
	v_mfma_f32_16x16x32_bf16 v[72:75], v[152:155], v[192:195], 0
	v_mfma_f32_16x16x32_bf16 v[68:71], v[160:163], v[192:195], 0
	v_mfma_f32_16x16x32_bf16 v[132:135], v[156:159], v[172:175], v[132:135]
	v_mfma_f32_16x16x32_bf16 v[124:127], v[164:167], v[172:175], v[124:127]
	v_mfma_f32_16x16x32_bf16 v[104:107], v[156:159], v[180:183], v[104:107]
	v_mfma_f32_16x16x32_bf16 v[100:103], v[164:167], v[180:183], v[100:103]
	v_mfma_f32_16x16x32_bf16 v[88:91], v[156:159], v[188:191], v[88:91]
	v_mfma_f32_16x16x32_bf16 v[84:87], v[164:167], v[188:191], v[84:87]
	v_mfma_f32_16x16x32_bf16 v[72:75], v[156:159], v[196:199], v[72:75]
	v_mfma_f32_16x16x32_bf16 v[68:71], v[164:167], v[196:199], v[68:71]
	s_barrier
	s_add_i32 s73, s75, s16
	v_lshl_add_u64 v[214:215], s[50:51], 0, v[2:3]
	s_mov_b32 m0, s73
	ds_read_b128 v[168:171], v236 offset:16384
	ds_read_b128 v[172:175], v236 offset:17408
	ds_read_b128 v[176:179], v236 offset:18432
	ds_read_b128 v[180:183], v236 offset:19456
	ds_read_b128 v[184:187], v236 offset:20480
	ds_read_b128 v[188:191], v236 offset:21504
	ds_read_b128 v[192:195], v236 offset:22528
	ds_read_b128 v[196:199], v236 offset:23552
	global_load_lds_dwordx4 v[214:215], off
	s_add_i32 m0, s73, 0x2000
	s_add_u32 s74, s50, 0x40000
	v_lshl_add_u64 v[216:217], s[50:51], 0, v[204:205]
	s_addc_u32 s75, s51, 0
	s_add_i32 s73, s76, s16
	global_load_lds_dwordx4 v[216:217], off
	s_mov_b32 m0, s73
	v_lshl_add_u64 v[218:219], s[74:75], 0, v[2:3]
	global_load_lds_dwordx4 v[218:219], off
	s_add_i32 m0, s73, 0x2000
	v_lshl_add_u64 v[218:219], s[74:75], 0, v[204:205]
	global_load_lds_dwordx4 v[218:219], off
	s_mov_b32 m0, s17
	v_lshl_add_u64 v[218:219], s[4:5], 0, v[208:209]
	global_load_lds_dwordx4 v[218:219], off
	s_mov_b32 m0, s46
	v_lshl_add_u64 v[218:219], s[4:5], 0, v[206:207]
	global_load_lds_dwordx4 v[218:219], off
	s_waitcnt vmcnt(8)
	s_waitcnt lgkmcnt(0)
	s_barrier
	v_mfma_f32_16x16x32_bf16 v[64:67], v[116:119], v[168:171], 0
	v_mfma_f32_16x16x32_bf16 v[60:63], v[136:139], v[168:171], 0
	v_mfma_f32_16x16x32_bf16 v[48:51], v[116:119], v[176:179], 0
	v_mfma_f32_16x16x32_bf16 v[44:47], v[136:139], v[176:179], 0
	v_mfma_f32_16x16x32_bf16 v[32:35], v[116:119], v[184:187], 0
	v_mfma_f32_16x16x32_bf16 v[28:31], v[136:139], v[184:187], 0
	v_mfma_f32_16x16x32_bf16 v[16:19], v[116:119], v[192:195], 0
	v_mfma_f32_16x16x32_bf16 v[12:15], v[136:139], v[192:195], 0
	v_mfma_f32_16x16x32_bf16 v[64:67], v[128:131], v[172:175], v[64:67]
	v_mfma_f32_16x16x32_bf16 v[60:63], v[148:151], v[172:175], v[60:63]
	v_mfma_f32_16x16x32_bf16 v[48:51], v[128:131], v[180:183], v[48:51]
	v_mfma_f32_16x16x32_bf16 v[44:47], v[148:151], v[180:183], v[44:47]
	v_mfma_f32_16x16x32_bf16 v[32:35], v[128:131], v[188:191], v[32:35]
	v_mfma_f32_16x16x32_bf16 v[28:31], v[148:151], v[188:191], v[28:31]
	v_mfma_f32_16x16x32_bf16 v[16:19], v[128:131], v[196:199], v[16:19]
	v_mfma_f32_16x16x32_bf16 v[12:15], v[148:151], v[196:199], v[12:15]
	v_mfma_f32_16x16x32_bf16 v[56:59], v[152:155], v[168:171], 0
	v_mfma_f32_16x16x32_bf16 v[52:55], v[160:163], v[168:171], 0
	v_mfma_f32_16x16x32_bf16 v[40:43], v[152:155], v[176:179], 0
	v_mfma_f32_16x16x32_bf16 v[36:39], v[160:163], v[176:179], 0
	v_mfma_f32_16x16x32_bf16 v[24:27], v[152:155], v[184:187], 0
	v_mfma_f32_16x16x32_bf16 v[20:23], v[160:163], v[184:187], 0
	v_mfma_f32_16x16x32_bf16 v[8:11], v[152:155], v[192:195], 0
	v_mfma_f32_16x16x32_bf16 v[4:7], v[160:163], v[192:195], 0
	v_mfma_f32_16x16x32_bf16 v[56:59], v[156:159], v[172:175], v[56:59]
	v_mfma_f32_16x16x32_bf16 v[52:55], v[164:167], v[172:175], v[52:55]
	v_mfma_f32_16x16x32_bf16 v[40:43], v[156:159], v[180:183], v[40:43]
	v_mfma_f32_16x16x32_bf16 v[36:39], v[164:167], v[180:183], v[36:39]
	v_mfma_f32_16x16x32_bf16 v[24:27], v[156:159], v[188:191], v[24:27]
	v_mfma_f32_16x16x32_bf16 v[20:23], v[164:167], v[188:191], v[20:23]
	v_mfma_f32_16x16x32_bf16 v[8:11], v[156:159], v[196:199], v[8:11]
	v_mfma_f32_16x16x32_bf16 v[4:7], v[164:167], v[196:199], v[4:7]
	s_barrier
	s_add_i32 s73, 0, 0x18000
	s_add_i32 s74, 0, 0x1c000
	v_add_u32_e32 v148, s73, v203
	v_add_u32_e32 v164, s74, v203
	ds_read_b128 v[116:119], v148
	ds_read_b128 v[128:131], v148 offset:1024
	ds_read_b128 v[136:139], v148 offset:2048
	ds_read_b128 v[148:151], v148 offset:3072
	ds_read_b128 v[152:155], v164
	ds_read_b128 v[156:159], v164 offset:1024
	ds_read_b128 v[160:163], v164 offset:2048
	ds_read_b128 v[164:167], v164 offset:3072
	s_add_u32 s4, s4, 0x40000
	s_addc_u32 s5, s5, 0
	s_mov_b32 m0, s47
	v_lshl_add_u64 v[218:219], s[4:5], 0, v[208:209]
	ds_read_b128 v[168:171], v236 offset:32768
	ds_read_b128 v[172:175], v236 offset:33792
	ds_read_b128 v[176:179], v236 offset:34816
	ds_read_b128 v[180:183], v236 offset:35840
	ds_read_b128 v[184:187], v236 offset:36864
	ds_read_b128 v[188:191], v236 offset:37888
	ds_read_b128 v[192:195], v236 offset:38912
	ds_read_b128 v[196:199], v236 offset:39936
	global_load_lds_dwordx4 v[218:219], off
	s_mov_b32 m0, s52
	v_lshl_add_u64 v[218:219], s[4:5], 0, v[206:207]
	global_load_lds_dwordx4 v[218:219], off
	s_waitcnt vmcnt(8)
	s_waitcnt lgkmcnt(0)
	s_barrier
	v_mfma_f32_16x16x32_bf16 v[144:147], v[116:119], v[168:171], v[144:147]
	v_mfma_f32_16x16x32_bf16 v[140:143], v[136:139], v[168:171], v[140:143]
	v_mfma_f32_16x16x32_bf16 v[120:123], v[116:119], v[176:179], v[120:123]
	v_mfma_f32_16x16x32_bf16 v[112:115], v[136:139], v[176:179], v[112:115]
	v_mfma_f32_16x16x32_bf16 v[96:99], v[116:119], v[184:187], v[96:99]
	v_mfma_f32_16x16x32_bf16 v[92:95], v[136:139], v[184:187], v[92:95]
	v_mfma_f32_16x16x32_bf16 v[80:83], v[116:119], v[192:195], v[80:83]
	v_mfma_f32_16x16x32_bf16 v[76:79], v[136:139], v[192:195], v[76:79]
	v_mfma_f32_16x16x32_bf16 v[144:147], v[128:131], v[172:175], v[144:147]
	v_mfma_f32_16x16x32_bf16 v[140:143], v[148:151], v[172:175], v[140:143]
	v_mfma_f32_16x16x32_bf16 v[120:123], v[128:131], v[180:183], v[120:123]
	v_mfma_f32_16x16x32_bf16 v[112:115], v[148:151], v[180:183], v[112:115]
	v_mfma_f32_16x16x32_bf16 v[96:99], v[128:131], v[188:191], v[96:99]
	v_mfma_f32_16x16x32_bf16 v[92:95], v[148:151], v[188:191], v[92:95]
	v_mfma_f32_16x16x32_bf16 v[80:83], v[128:131], v[196:199], v[80:83]
	v_mfma_f32_16x16x32_bf16 v[76:79], v[148:151], v[196:199], v[76:79]
	v_mfma_f32_16x16x32_bf16 v[132:135], v[152:155], v[168:171], v[132:135]
	v_mfma_f32_16x16x32_bf16 v[124:127], v[160:163], v[168:171], v[124:127]
	v_mfma_f32_16x16x32_bf16 v[104:107], v[152:155], v[176:179], v[104:107]
	v_mfma_f32_16x16x32_bf16 v[100:103], v[160:163], v[176:179], v[100:103]
	v_mfma_f32_16x16x32_bf16 v[88:91], v[152:155], v[184:187], v[88:91]
	v_mfma_f32_16x16x32_bf16 v[84:87], v[160:163], v[184:187], v[84:87]
	v_mfma_f32_16x16x32_bf16 v[72:75], v[152:155], v[192:195], v[72:75]
	v_mfma_f32_16x16x32_bf16 v[68:71], v[160:163], v[192:195], v[68:71]
	v_mfma_f32_16x16x32_bf16 v[132:135], v[156:159], v[172:175], v[132:135]
	v_mfma_f32_16x16x32_bf16 v[124:127], v[164:167], v[172:175], v[124:127]
	v_mfma_f32_16x16x32_bf16 v[104:107], v[156:159], v[180:183], v[104:107]
	v_mfma_f32_16x16x32_bf16 v[100:103], v[164:167], v[180:183], v[100:103]
	v_mfma_f32_16x16x32_bf16 v[88:91], v[156:159], v[188:191], v[88:91]
	v_mfma_f32_16x16x32_bf16 v[84:87], v[164:167], v[188:191], v[84:87]
	v_mfma_f32_16x16x32_bf16 v[72:75], v[156:159], v[196:199], v[72:75]
	v_mfma_f32_16x16x32_bf16 v[68:71], v[164:167], v[196:199], v[68:71]
	s_barrier
	s_add_i32 s4, s73, s16
	v_lshl_add_u64 v[214:215], v[214:215], 0, s[34:35]
	s_mov_b32 m0, s4
	ds_read_b128 v[168:171], v236 offset:49152
	ds_read_b128 v[172:175], v236 offset:50176
	ds_read_b128 v[176:179], v236 offset:51200
	ds_read_b128 v[180:183], v236 offset:52224
	ds_read_b128 v[184:187], v236 offset:53248
	ds_read_b128 v[188:191], v236 offset:54272
	ds_read_b128 v[192:195], v236 offset:55296
	ds_read_b128 v[196:199], v236 offset:56320
	global_load_lds_dwordx4 v[214:215], off
	s_add_i32 m0, s4, 0x2000
	s_add_u32 s4, s50, 0x40080
	v_lshl_add_u64 v[214:215], v[216:217], 0, s[34:35]
	s_addc_u32 s5, s51, 0
	s_add_i32 s50, s74, s16
	global_load_lds_dwordx4 v[214:215], off
	s_mov_b32 m0, s50
	v_lshl_add_u64 v[214:215], s[4:5], 0, v[2:3]
	global_load_lds_dwordx4 v[214:215], off
	s_add_i32 m0, s50, 0x2000
	v_lshl_add_u64 v[214:215], s[4:5], 0, v[204:205]
	global_load_lds_dwordx4 v[214:215], off
	s_mov_b32 m0, s60
	v_lshl_add_u64 v[214:215], s[12:13], 0, v[208:209]
	global_load_lds_dwordx4 v[214:215], off
	s_mov_b32 m0, s61
	v_lshl_add_u64 v[214:215], s[12:13], 0, v[206:207]
	global_load_lds_dwordx4 v[214:215], off
	s_waitcnt vmcnt(8)
	s_waitcnt lgkmcnt(0)
	s_barrier
	v_mfma_f32_16x16x32_bf16 v[64:67], v[116:119], v[168:171], v[64:67]
	v_mfma_f32_16x16x32_bf16 v[60:63], v[136:139], v[168:171], v[60:63]
	v_mfma_f32_16x16x32_bf16 v[48:51], v[116:119], v[176:179], v[48:51]
	v_mfma_f32_16x16x32_bf16 v[44:47], v[136:139], v[176:179], v[44:47]
	v_mfma_f32_16x16x32_bf16 v[32:35], v[116:119], v[184:187], v[32:35]
	v_mfma_f32_16x16x32_bf16 v[28:31], v[136:139], v[184:187], v[28:31]
	v_mfma_f32_16x16x32_bf16 v[16:19], v[116:119], v[192:195], v[16:19]
	v_mfma_f32_16x16x32_bf16 v[12:15], v[136:139], v[192:195], v[12:15]
	v_mfma_f32_16x16x32_bf16 v[64:67], v[128:131], v[172:175], v[64:67]
	v_mfma_f32_16x16x32_bf16 v[60:63], v[148:151], v[172:175], v[60:63]
	v_mfma_f32_16x16x32_bf16 v[48:51], v[128:131], v[180:183], v[48:51]
	v_mfma_f32_16x16x32_bf16 v[44:47], v[148:151], v[180:183], v[44:47]
	v_mfma_f32_16x16x32_bf16 v[32:35], v[128:131], v[188:191], v[32:35]
	v_mfma_f32_16x16x32_bf16 v[28:31], v[148:151], v[188:191], v[28:31]
	v_mfma_f32_16x16x32_bf16 v[16:19], v[128:131], v[196:199], v[16:19]
	v_mfma_f32_16x16x32_bf16 v[12:15], v[148:151], v[196:199], v[12:15]
	v_mfma_f32_16x16x32_bf16 v[56:59], v[152:155], v[168:171], v[56:59]
	v_mfma_f32_16x16x32_bf16 v[52:55], v[160:163], v[168:171], v[52:55]
	v_mfma_f32_16x16x32_bf16 v[40:43], v[152:155], v[176:179], v[40:43]
	v_mfma_f32_16x16x32_bf16 v[36:39], v[160:163], v[176:179], v[36:39]
	v_mfma_f32_16x16x32_bf16 v[24:27], v[152:155], v[184:187], v[24:27]
	v_mfma_f32_16x16x32_bf16 v[20:23], v[160:163], v[184:187], v[20:23]
	v_mfma_f32_16x16x32_bf16 v[8:11], v[152:155], v[192:195], v[8:11]
	v_mfma_f32_16x16x32_bf16 v[4:7], v[160:163], v[192:195], v[4:7]
	v_mfma_f32_16x16x32_bf16 v[56:59], v[156:159], v[172:175], v[56:59]
	v_mfma_f32_16x16x32_bf16 v[52:55], v[164:167], v[172:175], v[52:55]
	v_mfma_f32_16x16x32_bf16 v[40:43], v[156:159], v[180:183], v[40:43]
	v_mfma_f32_16x16x32_bf16 v[36:39], v[164:167], v[180:183], v[36:39]
	v_mfma_f32_16x16x32_bf16 v[24:27], v[156:159], v[188:191], v[24:27]
	v_mfma_f32_16x16x32_bf16 v[20:23], v[164:167], v[188:191], v[20:23]
	v_mfma_f32_16x16x32_bf16 v[8:11], v[156:159], v[196:199], v[8:11]
	v_mfma_f32_16x16x32_bf16 v[4:7], v[164:167], v[196:199], v[4:7]
	s_barrier
	s_add_i32 s72, s72, 2
	s_add_u32 s48, s48, 0x100
	s_addc_u32 s49, s49, 0
	s_cmp_gt_u32 s72, 13
.LBB0_1118:
	s_add_u32 s4, s44, s48
	s_addc_u32 s5, s45, s49
	s_add_u32 s73, s4, 0x100
	s_addc_u32 s74, s5, 0
	s_add_u32 s50, s70, s48
	s_addc_u32 s51, s71, s49
	s_add_u32 s4, s4, 0x180
	s_addc_u32 s5, s5, 0
	s_add_i32 s75, 0, 0x10000
	s_add_i32 s76, 0, 0x14000
	v_add_u32_e32 v148, s75, v203
	v_add_u32_e32 v164, s76, v203
	ds_read_b128 v[116:119], v148
	ds_read_b128 v[128:131], v148 offset:1024
	ds_read_b128 v[136:139], v148 offset:2048
	ds_read_b128 v[148:151], v148 offset:3072
	ds_read_b128 v[152:155], v164
	ds_read_b128 v[156:159], v164 offset:1024
	ds_read_b128 v[160:163], v164 offset:2048
	ds_read_b128 v[164:167], v164 offset:3072
	s_cmpk_eq_i32 s48, 0x700
	s_cselect_b32 s13, s69, s5
	s_cselect_b32 s12, s68, s4
	s_cselect_b32 s51, s23, s51
	s_cselect_b32 s50, s65, s50
	s_cselect_b32 s5, s37, s74
	s_cselect_b32 s4, s64, s73
	v_lshl_add_u64 v[214:215], v[108:109], 0, s[48:49]
	s_add_i32 m0, s17, 0xc000
	ds_read_b128 v[168:171], v236
	ds_read_b128 v[172:175], v236 offset:1024
	ds_read_b128 v[176:179], v236 offset:2048
	ds_read_b128 v[180:183], v236 offset:3072
	ds_read_b128 v[184:187], v236 offset:4096
	ds_read_b128 v[188:191], v236 offset:5120
	ds_read_b128 v[192:195], v236 offset:6144
	ds_read_b128 v[196:199], v236 offset:7168
	global_load_lds_dwordx4 v[214:215], off
	s_add_i32 m0, s17, 0xe000
	v_lshl_add_u64 v[214:215], v[110:111], 0, s[48:49]
	global_load_lds_dwordx4 v[214:215], off
	s_waitcnt vmcnt(8)
	s_waitcnt lgkmcnt(0)
	s_barrier
	v_mfma_f32_16x16x32_bf16 v[144:147], v[116:119], v[168:171], v[144:147]
	v_mfma_f32_16x16x32_bf16 v[140:143], v[136:139], v[168:171], v[140:143]
	v_mfma_f32_16x16x32_bf16 v[120:123], v[116:119], v[176:179], v[120:123]
	v_mfma_f32_16x16x32_bf16 v[112:115], v[136:139], v[176:179], v[112:115]
	v_mfma_f32_16x16x32_bf16 v[96:99], v[116:119], v[184:187], v[96:99]
	v_mfma_f32_16x16x32_bf16 v[92:95], v[136:139], v[184:187], v[92:95]
	v_mfma_f32_16x16x32_bf16 v[80:83], v[116:119], v[192:195], v[80:83]
	v_mfma_f32_16x16x32_bf16 v[76:79], v[136:139], v[192:195], v[76:79]
	v_mfma_f32_16x16x32_bf16 v[144:147], v[128:131], v[172:175], v[144:147]
	v_mfma_f32_16x16x32_bf16 v[140:143], v[148:151], v[172:175], v[140:143]
	v_mfma_f32_16x16x32_bf16 v[120:123], v[128:131], v[180:183], v[120:123]
	v_mfma_f32_16x16x32_bf16 v[112:115], v[148:151], v[180:183], v[112:115]
	v_mfma_f32_16x16x32_bf16 v[96:99], v[128:131], v[188:191], v[96:99]
	v_mfma_f32_16x16x32_bf16 v[92:95], v[148:151], v[188:191], v[92:95]
	v_mfma_f32_16x16x32_bf16 v[80:83], v[128:131], v[196:199], v[80:83]
	v_mfma_f32_16x16x32_bf16 v[76:79], v[148:151], v[196:199], v[76:79]
	v_mfma_f32_16x16x32_bf16 v[132:135], v[152:155], v[168:171], v[132:135]
	v_mfma_f32_16x16x32_bf16 v[124:127], v[160:163], v[168:171], v[124:127]
	v_mfma_f32_16x16x32_bf16 v[104:107], v[152:155], v[176:179], v[104:107]
	v_mfma_f32_16x16x32_bf16 v[100:103], v[160:163], v[176:179], v[100:103]
	v_mfma_f32_16x16x32_bf16 v[88:91], v[152:155], v[184:187], v[88:91]
	v_mfma_f32_16x16x32_bf16 v[84:87], v[160:163], v[184:187], v[84:87]
	v_mfma_f32_16x16x32_bf16 v[72:75], v[152:155], v[192:195], v[72:75]
	v_mfma_f32_16x16x32_bf16 v[68:71], v[160:163], v[192:195], v[68:71]
	v_mfma_f32_16x16x32_bf16 v[132:135], v[156:159], v[172:175], v[132:135]
	v_mfma_f32_16x16x32_bf16 v[124:127], v[164:167], v[172:175], v[124:127]
	v_mfma_f32_16x16x32_bf16 v[104:107], v[156:159], v[180:183], v[104:107]
	v_mfma_f32_16x16x32_bf16 v[100:103], v[164:167], v[180:183], v[100:103]
	v_mfma_f32_16x16x32_bf16 v[88:91], v[156:159], v[188:191], v[88:91]
	v_mfma_f32_16x16x32_bf16 v[84:87], v[164:167], v[188:191], v[84:87]
	v_mfma_f32_16x16x32_bf16 v[72:75], v[156:159], v[196:199], v[72:75]
	v_mfma_f32_16x16x32_bf16 v[68:71], v[164:167], v[196:199], v[68:71]
	s_barrier
	s_add_i32 s73, s75, s16
	v_lshl_add_u64 v[214:215], s[50:51], 0, v[2:3]
	s_mov_b32 m0, s73
	ds_read_b128 v[168:171], v236 offset:16384
	ds_read_b128 v[172:175], v236 offset:17408
	ds_read_b128 v[176:179], v236 offset:18432
	ds_read_b128 v[180:183], v236 offset:19456
	ds_read_b128 v[184:187], v236 offset:20480
	ds_read_b128 v[188:191], v236 offset:21504
	ds_read_b128 v[192:195], v236 offset:22528
	ds_read_b128 v[196:199], v236 offset:23552
	global_load_lds_dwordx4 v[214:215], off
	s_add_i32 m0, s73, 0x2000
	s_add_u32 s74, s50, 0x40000
	v_lshl_add_u64 v[216:217], s[50:51], 0, v[204:205]
	s_addc_u32 s75, s51, 0
	s_add_i32 s73, s76, s16
	global_load_lds_dwordx4 v[216:217], off
	s_mov_b32 m0, s73
	v_lshl_add_u64 v[218:219], s[74:75], 0, v[2:3]
	global_load_lds_dwordx4 v[218:219], off
	s_add_i32 m0, s73, 0x2000
	v_lshl_add_u64 v[218:219], s[74:75], 0, v[204:205]
	global_load_lds_dwordx4 v[218:219], off
	s_mov_b32 m0, s17
	v_lshl_add_u64 v[218:219], s[4:5], 0, v[208:209]
	global_load_lds_dwordx4 v[218:219], off
	s_mov_b32 m0, s46
	v_lshl_add_u64 v[218:219], s[4:5], 0, v[206:207]
	global_load_lds_dwordx4 v[218:219], off
	s_waitcnt vmcnt(8)
	s_waitcnt lgkmcnt(0)
	s_barrier
	v_mfma_f32_16x16x32_bf16 v[64:67], v[116:119], v[168:171], v[64:67]
	v_mfma_f32_16x16x32_bf16 v[60:63], v[136:139], v[168:171], v[60:63]
	v_mfma_f32_16x16x32_bf16 v[48:51], v[116:119], v[176:179], v[48:51]
	v_mfma_f32_16x16x32_bf16 v[44:47], v[136:139], v[176:179], v[44:47]
	v_mfma_f32_16x16x32_bf16 v[32:35], v[116:119], v[184:187], v[32:35]
	v_mfma_f32_16x16x32_bf16 v[28:31], v[136:139], v[184:187], v[28:31]
	v_mfma_f32_16x16x32_bf16 v[16:19], v[116:119], v[192:195], v[16:19]
	v_mfma_f32_16x16x32_bf16 v[12:15], v[136:139], v[192:195], v[12:15]
	v_mfma_f32_16x16x32_bf16 v[64:67], v[128:131], v[172:175], v[64:67]
	v_mfma_f32_16x16x32_bf16 v[60:63], v[148:151], v[172:175], v[60:63]
	v_mfma_f32_16x16x32_bf16 v[48:51], v[128:131], v[180:183], v[48:51]
	v_mfma_f32_16x16x32_bf16 v[44:47], v[148:151], v[180:183], v[44:47]
	v_mfma_f32_16x16x32_bf16 v[32:35], v[128:131], v[188:191], v[32:35]
	v_mfma_f32_16x16x32_bf16 v[28:31], v[148:151], v[188:191], v[28:31]
	v_mfma_f32_16x16x32_bf16 v[16:19], v[128:131], v[196:199], v[16:19]
	v_mfma_f32_16x16x32_bf16 v[12:15], v[148:151], v[196:199], v[12:15]
	v_mfma_f32_16x16x32_bf16 v[56:59], v[152:155], v[168:171], v[56:59]
	v_mfma_f32_16x16x32_bf16 v[52:55], v[160:163], v[168:171], v[52:55]
	v_mfma_f32_16x16x32_bf16 v[40:43], v[152:155], v[176:179], v[40:43]
	v_mfma_f32_16x16x32_bf16 v[36:39], v[160:163], v[176:179], v[36:39]
	v_mfma_f32_16x16x32_bf16 v[24:27], v[152:155], v[184:187], v[24:27]
	v_mfma_f32_16x16x32_bf16 v[20:23], v[160:163], v[184:187], v[20:23]
	v_mfma_f32_16x16x32_bf16 v[8:11], v[152:155], v[192:195], v[8:11]
	v_mfma_f32_16x16x32_bf16 v[4:7], v[160:163], v[192:195], v[4:7]
	v_mfma_f32_16x16x32_bf16 v[56:59], v[156:159], v[172:175], v[56:59]
	v_mfma_f32_16x16x32_bf16 v[52:55], v[164:167], v[172:175], v[52:55]
	v_mfma_f32_16x16x32_bf16 v[40:43], v[156:159], v[180:183], v[40:43]
	v_mfma_f32_16x16x32_bf16 v[36:39], v[164:167], v[180:183], v[36:39]
	v_mfma_f32_16x16x32_bf16 v[24:27], v[156:159], v[188:191], v[24:27]
	v_mfma_f32_16x16x32_bf16 v[20:23], v[164:167], v[188:191], v[20:23]
	v_mfma_f32_16x16x32_bf16 v[8:11], v[156:159], v[196:199], v[8:11]
	v_mfma_f32_16x16x32_bf16 v[4:7], v[164:167], v[196:199], v[4:7]
	s_barrier
	s_add_i32 s73, 0, 0x18000
	s_add_i32 s74, 0, 0x1c000
	v_add_u32_e32 v148, s73, v203
	v_add_u32_e32 v164, s74, v203
	ds_read_b128 v[116:119], v148
	ds_read_b128 v[128:131], v148 offset:1024
	ds_read_b128 v[136:139], v148 offset:2048
	ds_read_b128 v[148:151], v148 offset:3072
	ds_read_b128 v[152:155], v164
	ds_read_b128 v[156:159], v164 offset:1024
	ds_read_b128 v[160:163], v164 offset:2048
	ds_read_b128 v[164:167], v164 offset:3072
	s_add_u32 s4, s4, 0x40000
	s_addc_u32 s5, s5, 0
	s_mov_b32 m0, s47
	v_lshl_add_u64 v[218:219], s[4:5], 0, v[208:209]
	ds_read_b128 v[168:171], v236 offset:32768
	ds_read_b128 v[172:175], v236 offset:33792
	ds_read_b128 v[176:179], v236 offset:34816
	ds_read_b128 v[180:183], v236 offset:35840
	ds_read_b128 v[184:187], v236 offset:36864
	ds_read_b128 v[188:191], v236 offset:37888
	ds_read_b128 v[192:195], v236 offset:38912
	ds_read_b128 v[196:199], v236 offset:39936
	global_load_lds_dwordx4 v[218:219], off
	s_mov_b32 m0, s52
	v_lshl_add_u64 v[218:219], s[4:5], 0, v[206:207]
	global_load_lds_dwordx4 v[218:219], off
	s_waitcnt vmcnt(8)
	s_waitcnt lgkmcnt(0)
	s_barrier
	v_mfma_f32_16x16x32_bf16 v[144:147], v[116:119], v[168:171], v[144:147]
	v_mfma_f32_16x16x32_bf16 v[140:143], v[136:139], v[168:171], v[140:143]
	v_mfma_f32_16x16x32_bf16 v[120:123], v[116:119], v[176:179], v[120:123]
	v_mfma_f32_16x16x32_bf16 v[112:115], v[136:139], v[176:179], v[112:115]
	v_mfma_f32_16x16x32_bf16 v[96:99], v[116:119], v[184:187], v[96:99]
	v_mfma_f32_16x16x32_bf16 v[92:95], v[136:139], v[184:187], v[92:95]
	v_mfma_f32_16x16x32_bf16 v[80:83], v[116:119], v[192:195], v[80:83]
	v_mfma_f32_16x16x32_bf16 v[76:79], v[136:139], v[192:195], v[76:79]
	v_mfma_f32_16x16x32_bf16 v[144:147], v[128:131], v[172:175], v[144:147]
	v_mfma_f32_16x16x32_bf16 v[140:143], v[148:151], v[172:175], v[140:143]
	v_mfma_f32_16x16x32_bf16 v[120:123], v[128:131], v[180:183], v[120:123]
	v_mfma_f32_16x16x32_bf16 v[112:115], v[148:151], v[180:183], v[112:115]
	v_mfma_f32_16x16x32_bf16 v[96:99], v[128:131], v[188:191], v[96:99]
	v_mfma_f32_16x16x32_bf16 v[92:95], v[148:151], v[188:191], v[92:95]
	v_mfma_f32_16x16x32_bf16 v[80:83], v[128:131], v[196:199], v[80:83]
	v_mfma_f32_16x16x32_bf16 v[76:79], v[148:151], v[196:199], v[76:79]
	v_mfma_f32_16x16x32_bf16 v[132:135], v[152:155], v[168:171], v[132:135]
	v_mfma_f32_16x16x32_bf16 v[124:127], v[160:163], v[168:171], v[124:127]
	v_mfma_f32_16x16x32_bf16 v[104:107], v[152:155], v[176:179], v[104:107]
	v_mfma_f32_16x16x32_bf16 v[100:103], v[160:163], v[176:179], v[100:103]
	v_mfma_f32_16x16x32_bf16 v[88:91], v[152:155], v[184:187], v[88:91]
	v_mfma_f32_16x16x32_bf16 v[84:87], v[160:163], v[184:187], v[84:87]
	v_mfma_f32_16x16x32_bf16 v[72:75], v[152:155], v[192:195], v[72:75]
	v_mfma_f32_16x16x32_bf16 v[68:71], v[160:163], v[192:195], v[68:71]
	v_mfma_f32_16x16x32_bf16 v[132:135], v[156:159], v[172:175], v[132:135]
	v_mfma_f32_16x16x32_bf16 v[124:127], v[164:167], v[172:175], v[124:127]
	v_mfma_f32_16x16x32_bf16 v[104:107], v[156:159], v[180:183], v[104:107]
	v_mfma_f32_16x16x32_bf16 v[100:103], v[164:167], v[180:183], v[100:103]
	v_mfma_f32_16x16x32_bf16 v[88:91], v[156:159], v[188:191], v[88:91]
	v_mfma_f32_16x16x32_bf16 v[84:87], v[164:167], v[188:191], v[84:87]
	v_mfma_f32_16x16x32_bf16 v[72:75], v[156:159], v[196:199], v[72:75]
	v_mfma_f32_16x16x32_bf16 v[68:71], v[164:167], v[196:199], v[68:71]
	s_barrier
	s_add_i32 s4, s73, s16
	v_lshl_add_u64 v[214:215], v[214:215], 0, s[34:35]
	s_mov_b32 m0, s4
	ds_read_b128 v[168:171], v236 offset:49152
	ds_read_b128 v[172:175], v236 offset:50176
	ds_read_b128 v[176:179], v236 offset:51200
	ds_read_b128 v[180:183], v236 offset:52224
	ds_read_b128 v[184:187], v236 offset:53248
	ds_read_b128 v[188:191], v236 offset:54272
	ds_read_b128 v[192:195], v236 offset:55296
	ds_read_b128 v[196:199], v236 offset:56320
	global_load_lds_dwordx4 v[214:215], off
	s_add_i32 m0, s4, 0x2000
	s_add_u32 s4, s50, 0x40080
	v_lshl_add_u64 v[214:215], v[216:217], 0, s[34:35]
	s_addc_u32 s5, s51, 0
	s_add_i32 s50, s74, s16
	global_load_lds_dwordx4 v[214:215], off
	s_mov_b32 m0, s50
	v_lshl_add_u64 v[214:215], s[4:5], 0, v[2:3]
	global_load_lds_dwordx4 v[214:215], off
	s_add_i32 m0, s50, 0x2000
	v_lshl_add_u64 v[214:215], s[4:5], 0, v[204:205]
	global_load_lds_dwordx4 v[214:215], off
	s_mov_b32 m0, s60
	v_lshl_add_u64 v[214:215], s[12:13], 0, v[208:209]
	global_load_lds_dwordx4 v[214:215], off
	s_mov_b32 m0, s61
	v_lshl_add_u64 v[214:215], s[12:13], 0, v[206:207]
	global_load_lds_dwordx4 v[214:215], off
	s_waitcnt vmcnt(8)
	s_waitcnt lgkmcnt(0)
	s_barrier
	v_mfma_f32_16x16x32_bf16 v[64:67], v[116:119], v[168:171], v[64:67]
	v_mfma_f32_16x16x32_bf16 v[60:63], v[136:139], v[168:171], v[60:63]
	v_mfma_f32_16x16x32_bf16 v[48:51], v[116:119], v[176:179], v[48:51]
	v_mfma_f32_16x16x32_bf16 v[44:47], v[136:139], v[176:179], v[44:47]
	v_mfma_f32_16x16x32_bf16 v[32:35], v[116:119], v[184:187], v[32:35]
	v_mfma_f32_16x16x32_bf16 v[28:31], v[136:139], v[184:187], v[28:31]
	v_mfma_f32_16x16x32_bf16 v[16:19], v[116:119], v[192:195], v[16:19]
	v_mfma_f32_16x16x32_bf16 v[12:15], v[136:139], v[192:195], v[12:15]
	v_mfma_f32_16x16x32_bf16 v[64:67], v[128:131], v[172:175], v[64:67]
	v_mfma_f32_16x16x32_bf16 v[60:63], v[148:151], v[172:175], v[60:63]
	v_mfma_f32_16x16x32_bf16 v[48:51], v[128:131], v[180:183], v[48:51]
	v_mfma_f32_16x16x32_bf16 v[44:47], v[148:151], v[180:183], v[44:47]
	v_mfma_f32_16x16x32_bf16 v[32:35], v[128:131], v[188:191], v[32:35]
	v_mfma_f32_16x16x32_bf16 v[28:31], v[148:151], v[188:191], v[28:31]
	v_mfma_f32_16x16x32_bf16 v[16:19], v[128:131], v[196:199], v[16:19]
	v_mfma_f32_16x16x32_bf16 v[12:15], v[148:151], v[196:199], v[12:15]
	v_mfma_f32_16x16x32_bf16 v[56:59], v[152:155], v[168:171], v[56:59]
	v_mfma_f32_16x16x32_bf16 v[52:55], v[160:163], v[168:171], v[52:55]
	v_mfma_f32_16x16x32_bf16 v[40:43], v[152:155], v[176:179], v[40:43]
	v_mfma_f32_16x16x32_bf16 v[36:39], v[160:163], v[176:179], v[36:39]
	v_mfma_f32_16x16x32_bf16 v[24:27], v[152:155], v[184:187], v[24:27]
	v_mfma_f32_16x16x32_bf16 v[20:23], v[160:163], v[184:187], v[20:23]
	v_mfma_f32_16x16x32_bf16 v[8:11], v[152:155], v[192:195], v[8:11]
	v_mfma_f32_16x16x32_bf16 v[4:7], v[160:163], v[192:195], v[4:7]
	v_mfma_f32_16x16x32_bf16 v[56:59], v[156:159], v[172:175], v[56:59]
	v_mfma_f32_16x16x32_bf16 v[52:55], v[164:167], v[172:175], v[52:55]
	v_mfma_f32_16x16x32_bf16 v[40:43], v[156:159], v[180:183], v[40:43]
	v_mfma_f32_16x16x32_bf16 v[36:39], v[164:167], v[180:183], v[36:39]
	v_mfma_f32_16x16x32_bf16 v[24:27], v[156:159], v[188:191], v[24:27]
	v_mfma_f32_16x16x32_bf16 v[20:23], v[164:167], v[188:191], v[20:23]
	v_mfma_f32_16x16x32_bf16 v[8:11], v[156:159], v[196:199], v[8:11]
	v_mfma_f32_16x16x32_bf16 v[4:7], v[164:167], v[196:199], v[4:7]
	s_barrier
	s_add_i32 s72, s72, 2
	s_add_u32 s48, s48, 0x100
	s_addc_u32 s49, s49, 0
	s_cmp_gt_u32 s72, 13
	s_cbranch_scc0 .LBB0_1118
	s_and_b64 vcc, exec, s[20:21]
	s_cbranch_vccz .LBB0_1121
	s_barrier

.LBB0_1205:
	s_ashr_i32 s37, s36, 31
	s_lshl_b64 s[4:5], s[36:37], 19
	s_add_u32 s40, s6, s4
	s_addc_u32 s41, s7, s5
	s_and_b64 s[4:5], s[38:39], exec
	s_cselect_b32 s37, s41, s23
	s_cselect_b32 s61, s40, s22
	s_ashr_i32 s21, s20, 31
	s_lshl_b64 s[4:5], s[20:21], 19
	s_add_u32 s42, s8, s4
	s_addc_u32 s43, s9, s5
	s_and_b64 s[4:5], s[38:39], exec
	s_cselect_b32 s21, s43, s45
	s_cselect_b32 s62, s42, s44
	s_add_u32 s63, s61, 0x80
	s_addc_u32 s64, s37, 0
	s_add_u32 s4, s22, 0x40080
	s_addc_u32 s5, s23, 0
	s_add_u32 s65, s44, 0x100
	v_lshl_add_u64 v[142:143], s[4:5], 0, v[138:139]
	v_lshl_add_u64 v[144:145], s[4:5], 0, v[140:141]
	s_addc_u32 s68, s45, 0
	s_mov_b32 s69, -2
	s_mov_b64 s[44:45], 0
	s_add_u32 s4, s22, s44
	s_addc_u32 s5, s23, s45
	s_add_u32 s70, s4, 0x100
	s_addc_u32 s71, s5, 0
	s_add_u32 s48, s65, s44
	s_addc_u32 s49, s68, s45
	s_add_u32 s4, s4, 0x180
	s_addc_u32 s5, s5, 0
	s_add_i32 s72, 0, 0x10000
	s_add_i32 s73, 0, 0x14000
	v_add_u32_e32 v160, s72, v146
	v_add_u32_e32 v176, s73, v146
	ds_read_b128 v[148:151], v160
	ds_read_b128 v[152:155], v160 offset:1024
	ds_read_b128 v[156:159], v160 offset:2048
	ds_read_b128 v[160:163], v160 offset:3072
	ds_read_b128 v[164:167], v176
	ds_read_b128 v[168:171], v176 offset:1024
	ds_read_b128 v[172:175], v176 offset:2048
	ds_read_b128 v[176:179], v176 offset:3072
	s_cmpk_eq_i32 s44, 0x700
	s_cselect_b32 s13, s64, s5
	s_cselect_b32 s12, s63, s4
	s_cselect_b32 s49, s21, s49
	s_cselect_b32 s48, s62, s48
	s_cselect_b32 s5, s37, s71
	s_cselect_b32 s4, s61, s70
	v_lshl_add_u64 v[216:217], v[142:143], 0, s[44:45]
	s_add_i32 m0, s17, 0xc000
	ds_read_b128 v[180:183], v147
	ds_read_b128 v[184:187], v147 offset:1024
	ds_read_b128 v[188:191], v147 offset:2048
	ds_read_b128 v[192:195], v147 offset:3072
	ds_read_b128 v[196:199], v147 offset:4096
	ds_read_b128 v[204:207], v147 offset:5120
	ds_read_b128 v[208:211], v147 offset:6144
	ds_read_b128 v[212:215], v147 offset:7168
	global_load_lds_dwordx4 v[216:217], off
	s_add_i32 m0, s17, 0xe000
	v_lshl_add_u64 v[216:217], v[144:145], 0, s[44:45]
	global_load_lds_dwordx4 v[216:217], off
	s_waitcnt vmcnt(8)
	s_waitcnt lgkmcnt(0)
	s_barrier
	v_mfma_f32_16x16x32_bf16 v[128:131], v[148:151], v[180:183], 0
	v_mfma_f32_16x16x32_bf16 v[124:127], v[156:159], v[180:183], 0
	v_mfma_f32_16x16x32_bf16 v[120:123], v[148:151], v[188:191], 0
	v_mfma_f32_16x16x32_bf16 v[116:119], v[156:159], v[188:191], 0
	v_mfma_f32_16x16x32_bf16 v[104:107], v[148:151], v[196:199], 0
	v_mfma_f32_16x16x32_bf16 v[100:103], v[156:159], v[196:199], 0
	v_mfma_f32_16x16x32_bf16 v[88:91], v[148:151], v[208:211], 0
	v_mfma_f32_16x16x32_bf16 v[84:87], v[156:159], v[208:211], 0
	v_mfma_f32_16x16x32_bf16 v[128:131], v[152:155], v[184:187], v[128:131]
	v_mfma_f32_16x16x32_bf16 v[124:127], v[160:163], v[184:187], v[124:127]
	v_mfma_f32_16x16x32_bf16 v[120:123], v[152:155], v[192:195], v[120:123]
	v_mfma_f32_16x16x32_bf16 v[116:119], v[160:163], v[192:195], v[116:119]
	v_mfma_f32_16x16x32_bf16 v[104:107], v[152:155], v[204:207], v[104:107]
	v_mfma_f32_16x16x32_bf16 v[100:103], v[160:163], v[204:207], v[100:103]
	v_mfma_f32_16x16x32_bf16 v[88:91], v[152:155], v[212:215], v[88:91]
	v_mfma_f32_16x16x32_bf16 v[84:87], v[160:163], v[212:215], v[84:87]
	v_mfma_f32_16x16x32_bf16 v[112:115], v[164:167], v[180:183], 0
	v_mfma_f32_16x16x32_bf16 v[108:111], v[172:175], v[180:183], 0
	v_mfma_f32_16x16x32_bf16 v[96:99], v[164:167], v[188:191], 0
	v_mfma_f32_16x16x32_bf16 v[92:95], v[172:175], v[188:191], 0
	v_mfma_f32_16x16x32_bf16 v[80:83], v[164:167], v[196:199], 0
	v_mfma_f32_16x16x32_bf16 v[76:79], v[172:175], v[196:199], 0
	v_mfma_f32_16x16x32_bf16 v[72:75], v[164:167], v[208:211], 0
	v_mfma_f32_16x16x32_bf16 v[68:71], v[172:175], v[208:211], 0
	v_mfma_f32_16x16x32_bf16 v[112:115], v[168:171], v[184:187], v[112:115]
	v_mfma_f32_16x16x32_bf16 v[108:111], v[176:179], v[184:187], v[108:111]
	v_mfma_f32_16x16x32_bf16 v[96:99], v[168:171], v[192:195], v[96:99]
	v_mfma_f32_16x16x32_bf16 v[92:95], v[176:179], v[192:195], v[92:95]
	v_mfma_f32_16x16x32_bf16 v[80:83], v[168:171], v[204:207], v[80:83]
	v_mfma_f32_16x16x32_bf16 v[76:79], v[176:179], v[204:207], v[76:79]
	v_mfma_f32_16x16x32_bf16 v[72:75], v[168:171], v[212:215], v[72:75]
	v_mfma_f32_16x16x32_bf16 v[68:71], v[176:179], v[212:215], v[68:71]
	s_barrier
	s_add_i32 s70, s72, s16
	v_lshl_add_u64 v[216:217], s[48:49], 0, v[2:3]
	s_mov_b32 m0, s70
	ds_read_b128 v[180:183], v147 offset:16384
	ds_read_b128 v[184:187], v147 offset:17408
	ds_read_b128 v[188:191], v147 offset:18432
	ds_read_b128 v[192:195], v147 offset:19456
	ds_read_b128 v[196:199], v147 offset:20480
	ds_read_b128 v[204:207], v147 offset:21504
	ds_read_b128 v[208:211], v147 offset:22528
	ds_read_b128 v[212:215], v147 offset:23552
	global_load_lds_dwordx4 v[216:217], off
	s_add_i32 m0, s70, 0x2000
	s_add_u32 s70, s48, 0x40000
	v_lshl_add_u64 v[218:219], s[48:49], 0, v[132:133]
	s_addc_u32 s71, s49, 0
	s_add_i32 s72, s73, s16
	global_load_lds_dwordx4 v[218:219], off
	s_mov_b32 m0, s72
	v_lshl_add_u64 v[220:221], s[70:71], 0, v[2:3]
	global_load_lds_dwordx4 v[220:221], off
	s_add_i32 m0, s72, 0x2000
	v_lshl_add_u64 v[220:221], s[70:71], 0, v[132:133]
	global_load_lds_dwordx4 v[220:221], off
	s_mov_b32 m0, s17
	v_lshl_add_u64 v[220:221], s[4:5], 0, v[136:137]
	global_load_lds_dwordx4 v[220:221], off
	s_mov_b32 m0, s46
	v_lshl_add_u64 v[220:221], s[4:5], 0, v[134:135]
	global_load_lds_dwordx4 v[220:221], off
	s_waitcnt vmcnt(8)
	s_waitcnt lgkmcnt(0)
	s_barrier
	v_mfma_f32_16x16x32_bf16 v[64:67], v[148:151], v[180:183], 0
	v_mfma_f32_16x16x32_bf16 v[60:63], v[156:159], v[180:183], 0
	v_mfma_f32_16x16x32_bf16 v[56:59], v[148:151], v[188:191], 0
	v_mfma_f32_16x16x32_bf16 v[52:55], v[156:159], v[188:191], 0
	v_mfma_f32_16x16x32_bf16 v[40:43], v[148:151], v[196:199], 0
	v_mfma_f32_16x16x32_bf16 v[36:39], v[156:159], v[196:199], 0
	v_mfma_f32_16x16x32_bf16 v[24:27], v[148:151], v[208:211], 0
	v_mfma_f32_16x16x32_bf16 v[20:23], v[156:159], v[208:211], 0
	v_mfma_f32_16x16x32_bf16 v[64:67], v[152:155], v[184:187], v[64:67]
	v_mfma_f32_16x16x32_bf16 v[60:63], v[160:163], v[184:187], v[60:63]
	v_mfma_f32_16x16x32_bf16 v[56:59], v[152:155], v[192:195], v[56:59]
	v_mfma_f32_16x16x32_bf16 v[52:55], v[160:163], v[192:195], v[52:55]
	v_mfma_f32_16x16x32_bf16 v[40:43], v[152:155], v[204:207], v[40:43]
	v_mfma_f32_16x16x32_bf16 v[36:39], v[160:163], v[204:207], v[36:39]
	v_mfma_f32_16x16x32_bf16 v[24:27], v[152:155], v[212:215], v[24:27]
	v_mfma_f32_16x16x32_bf16 v[20:23], v[160:163], v[212:215], v[20:23]
	v_mfma_f32_16x16x32_bf16 v[48:51], v[164:167], v[180:183], 0
	v_mfma_f32_16x16x32_bf16 v[44:47], v[172:175], v[180:183], 0
	v_mfma_f32_16x16x32_bf16 v[32:35], v[164:167], v[188:191], 0
	v_mfma_f32_16x16x32_bf16 v[28:31], v[172:175], v[188:191], 0
	v_mfma_f32_16x16x32_bf16 v[16:19], v[164:167], v[196:199], 0
	v_mfma_f32_16x16x32_bf16 v[12:15], v[172:175], v[196:199], 0
	v_mfma_f32_16x16x32_bf16 v[8:11], v[164:167], v[208:211], 0
	v_mfma_f32_16x16x32_bf16 v[4:7], v[172:175], v[208:211], 0
	v_mfma_f32_16x16x32_bf16 v[48:51], v[168:171], v[184:187], v[48:51]
	v_mfma_f32_16x16x32_bf16 v[44:47], v[176:179], v[184:187], v[44:47]
	v_mfma_f32_16x16x32_bf16 v[32:35], v[168:171], v[192:195], v[32:35]
	v_mfma_f32_16x16x32_bf16 v[28:31], v[176:179], v[192:195], v[28:31]
	v_mfma_f32_16x16x32_bf16 v[16:19], v[168:171], v[204:207], v[16:19]
	v_mfma_f32_16x16x32_bf16 v[12:15], v[176:179], v[204:207], v[12:15]
	v_mfma_f32_16x16x32_bf16 v[8:11], v[168:171], v[212:215], v[8:11]
	v_mfma_f32_16x16x32_bf16 v[4:7], v[176:179], v[212:215], v[4:7]
	s_barrier
	s_add_i32 s70, 0, 0x18000
	s_add_i32 s71, 0, 0x1c000
	v_add_u32_e32 v160, s70, v146
	v_add_u32_e32 v176, s71, v146
	ds_read_b128 v[148:151], v160
	ds_read_b128 v[152:155], v160 offset:1024
	ds_read_b128 v[156:159], v160 offset:2048
	ds_read_b128 v[160:163], v160 offset:3072
	ds_read_b128 v[164:167], v176
	ds_read_b128 v[168:171], v176 offset:1024
	ds_read_b128 v[172:175], v176 offset:2048
	ds_read_b128 v[176:179], v176 offset:3072
	s_add_u32 s4, s4, 0x40000
	s_addc_u32 s5, s5, 0
	s_mov_b32 m0, s47
	v_lshl_add_u64 v[220:221], s[4:5], 0, v[136:137]
	ds_read_b128 v[180:183], v147 offset:32768
	ds_read_b128 v[184:187], v147 offset:33792
	ds_read_b128 v[188:191], v147 offset:34816
	ds_read_b128 v[192:195], v147 offset:35840
	ds_read_b128 v[196:199], v147 offset:36864
	ds_read_b128 v[204:207], v147 offset:37888
	ds_read_b128 v[208:211], v147 offset:38912
	ds_read_b128 v[212:215], v147 offset:39936
	global_load_lds_dwordx4 v[220:221], off
	s_mov_b32 m0, s50
	v_lshl_add_u64 v[220:221], s[4:5], 0, v[134:135]
	global_load_lds_dwordx4 v[220:221], off
	s_waitcnt vmcnt(8)
	s_waitcnt lgkmcnt(0)
	s_barrier
	v_mfma_f32_16x16x32_bf16 v[128:131], v[148:151], v[180:183], v[128:131]
	v_mfma_f32_16x16x32_bf16 v[124:127], v[156:159], v[180:183], v[124:127]
	v_mfma_f32_16x16x32_bf16 v[120:123], v[148:151], v[188:191], v[120:123]
	v_mfma_f32_16x16x32_bf16 v[116:119], v[156:159], v[188:191], v[116:119]
	v_mfma_f32_16x16x32_bf16 v[104:107], v[148:151], v[196:199], v[104:107]
	v_mfma_f32_16x16x32_bf16 v[100:103], v[156:159], v[196:199], v[100:103]
	v_mfma_f32_16x16x32_bf16 v[88:91], v[148:151], v[208:211], v[88:91]
	v_mfma_f32_16x16x32_bf16 v[84:87], v[156:159], v[208:211], v[84:87]
	v_mfma_f32_16x16x32_bf16 v[128:131], v[152:155], v[184:187], v[128:131]
	v_mfma_f32_16x16x32_bf16 v[124:127], v[160:163], v[184:187], v[124:127]
	v_mfma_f32_16x16x32_bf16 v[120:123], v[152:155], v[192:195], v[120:123]
	v_mfma_f32_16x16x32_bf16 v[116:119], v[160:163], v[192:195], v[116:119]
	v_mfma_f32_16x16x32_bf16 v[104:107], v[152:155], v[204:207], v[104:107]
	v_mfma_f32_16x16x32_bf16 v[100:103], v[160:163], v[204:207], v[100:103]
	v_mfma_f32_16x16x32_bf16 v[88:91], v[152:155], v[212:215], v[88:91]
	v_mfma_f32_16x16x32_bf16 v[84:87], v[160:163], v[212:215], v[84:87]
	v_mfma_f32_16x16x32_bf16 v[112:115], v[164:167], v[180:183], v[112:115]
	v_mfma_f32_16x16x32_bf16 v[108:111], v[172:175], v[180:183], v[108:111]
	v_mfma_f32_16x16x32_bf16 v[96:99], v[164:167], v[188:191], v[96:99]
	v_mfma_f32_16x16x32_bf16 v[92:95], v[172:175], v[188:191], v[92:95]
	v_mfma_f32_16x16x32_bf16 v[80:83], v[164:167], v[196:199], v[80:83]
	v_mfma_f32_16x16x32_bf16 v[76:79], v[172:175], v[196:199], v[76:79]
	v_mfma_f32_16x16x32_bf16 v[72:75], v[164:167], v[208:211], v[72:75]
	v_mfma_f32_16x16x32_bf16 v[68:71], v[172:175], v[208:211], v[68:71]
	v_mfma_f32_16x16x32_bf16 v[112:115], v[168:171], v[184:187], v[112:115]
	v_mfma_f32_16x16x32_bf16 v[108:111], v[176:179], v[184:187], v[108:111]
	v_mfma_f32_16x16x32_bf16 v[96:99], v[168:171], v[192:195], v[96:99]
	v_mfma_f32_16x16x32_bf16 v[92:95], v[176:179], v[192:195], v[92:95]
	v_mfma_f32_16x16x32_bf16 v[80:83], v[168:171], v[204:207], v[80:83]
	v_mfma_f32_16x16x32_bf16 v[76:79], v[176:179], v[204:207], v[76:79]
	v_mfma_f32_16x16x32_bf16 v[72:75], v[168:171], v[212:215], v[72:75]
	v_mfma_f32_16x16x32_bf16 v[68:71], v[176:179], v[212:215], v[68:71]
	s_barrier
	s_add_i32 s4, s70, s16
	v_lshl_add_u64 v[216:217], v[216:217], 0, s[34:35]
	s_mov_b32 m0, s4
	ds_read_b128 v[180:183], v147 offset:49152
	ds_read_b128 v[184:187], v147 offset:50176
	ds_read_b128 v[188:191], v147 offset:51200
	ds_read_b128 v[192:195], v147 offset:52224
	ds_read_b128 v[196:199], v147 offset:53248
	ds_read_b128 v[204:207], v147 offset:54272
	ds_read_b128 v[208:211], v147 offset:55296
	ds_read_b128 v[212:215], v147 offset:56320
	global_load_lds_dwordx4 v[216:217], off
	s_add_i32 m0, s4, 0x2000
	s_add_u32 s4, s48, 0x40080
	v_lshl_add_u64 v[216:217], v[218:219], 0, s[34:35]
	s_addc_u32 s5, s49, 0
	s_add_i32 s48, s71, s16
	global_load_lds_dwordx4 v[216:217], off
	s_mov_b32 m0, s48
	v_lshl_add_u64 v[216:217], s[4:5], 0, v[2:3]
	global_load_lds_dwordx4 v[216:217], off
	s_add_i32 m0, s48, 0x2000
	v_lshl_add_u64 v[216:217], s[4:5], 0, v[132:133]
	global_load_lds_dwordx4 v[216:217], off
	s_mov_b32 m0, s53
	v_lshl_add_u64 v[216:217], s[12:13], 0, v[136:137]
	global_load_lds_dwordx4 v[216:217], off
	s_mov_b32 m0, s56
	v_lshl_add_u64 v[216:217], s[12:13], 0, v[134:135]
	global_load_lds_dwordx4 v[216:217], off
	s_waitcnt vmcnt(8)
	s_waitcnt lgkmcnt(0)
	s_barrier
	v_mfma_f32_16x16x32_bf16 v[64:67], v[148:151], v[180:183], v[64:67]
	v_mfma_f32_16x16x32_bf16 v[60:63], v[156:159], v[180:183], v[60:63]
	v_mfma_f32_16x16x32_bf16 v[56:59], v[148:151], v[188:191], v[56:59]
	v_mfma_f32_16x16x32_bf16 v[52:55], v[156:159], v[188:191], v[52:55]
	v_mfma_f32_16x16x32_bf16 v[40:43], v[148:151], v[196:199], v[40:43]
	v_mfma_f32_16x16x32_bf16 v[36:39], v[156:159], v[196:199], v[36:39]
	v_mfma_f32_16x16x32_bf16 v[24:27], v[148:151], v[208:211], v[24:27]
	v_mfma_f32_16x16x32_bf16 v[20:23], v[156:159], v[208:211], v[20:23]
	v_mfma_f32_16x16x32_bf16 v[64:67], v[152:155], v[184:187], v[64:67]
	v_mfma_f32_16x16x32_bf16 v[60:63], v[160:163], v[184:187], v[60:63]
	v_mfma_f32_16x16x32_bf16 v[56:59], v[152:155], v[192:195], v[56:59]
	v_mfma_f32_16x16x32_bf16 v[52:55], v[160:163], v[192:195], v[52:55]
	v_mfma_f32_16x16x32_bf16 v[40:43], v[152:155], v[204:207], v[40:43]
	v_mfma_f32_16x16x32_bf16 v[36:39], v[160:163], v[204:207], v[36:39]
	v_mfma_f32_16x16x32_bf16 v[24:27], v[152:155], v[212:215], v[24:27]
	v_mfma_f32_16x16x32_bf16 v[20:23], v[160:163], v[212:215], v[20:23]
	v_mfma_f32_16x16x32_bf16 v[48:51], v[164:167], v[180:183], v[48:51]
	v_mfma_f32_16x16x32_bf16 v[44:47], v[172:175], v[180:183], v[44:47]
	v_mfma_f32_16x16x32_bf16 v[32:35], v[164:167], v[188:191], v[32:35]
	v_mfma_f32_16x16x32_bf16 v[28:31], v[172:175], v[188:191], v[28:31]
	v_mfma_f32_16x16x32_bf16 v[16:19], v[164:167], v[196:199], v[16:19]
	v_mfma_f32_16x16x32_bf16 v[12:15], v[172:175], v[196:199], v[12:15]
	v_mfma_f32_16x16x32_bf16 v[8:11], v[164:167], v[208:211], v[8:11]
	v_mfma_f32_16x16x32_bf16 v[4:7], v[172:175], v[208:211], v[4:7]
	v_mfma_f32_16x16x32_bf16 v[48:51], v[168:171], v[184:187], v[48:51]
	v_mfma_f32_16x16x32_bf16 v[44:47], v[176:179], v[184:187], v[44:47]
	v_mfma_f32_16x16x32_bf16 v[32:35], v[168:171], v[192:195], v[32:35]
	v_mfma_f32_16x16x32_bf16 v[28:31], v[176:179], v[192:195], v[28:31]
	v_mfma_f32_16x16x32_bf16 v[16:19], v[168:171], v[204:207], v[16:19]
	v_mfma_f32_16x16x32_bf16 v[12:15], v[176:179], v[204:207], v[12:15]
	v_mfma_f32_16x16x32_bf16 v[8:11], v[168:171], v[212:215], v[8:11]
	v_mfma_f32_16x16x32_bf16 v[4:7], v[176:179], v[212:215], v[4:7]
	s_barrier
	s_add_i32 s69, s69, 2
	s_add_u32 s44, s44, 0x100
	s_addc_u32 s45, s45, 0
	s_cmp_gt_u32 s69, 13
.LBB0_1206:
	s_add_u32 s4, s22, s44
	s_addc_u32 s5, s23, s45
	s_add_u32 s70, s4, 0x100
	s_addc_u32 s71, s5, 0
	s_add_u32 s48, s65, s44
	s_addc_u32 s49, s68, s45
	s_add_u32 s4, s4, 0x180
	s_addc_u32 s5, s5, 0
	s_add_i32 s72, 0, 0x10000
	s_add_i32 s73, 0, 0x14000
	v_add_u32_e32 v160, s72, v146
	v_add_u32_e32 v176, s73, v146
	ds_read_b128 v[148:151], v160
	ds_read_b128 v[152:155], v160 offset:1024
	ds_read_b128 v[156:159], v160 offset:2048
	ds_read_b128 v[160:163], v160 offset:3072
	ds_read_b128 v[164:167], v176
	ds_read_b128 v[168:171], v176 offset:1024
	ds_read_b128 v[172:175], v176 offset:2048
	ds_read_b128 v[176:179], v176 offset:3072
	s_cmpk_eq_i32 s44, 0x700
	s_cselect_b32 s13, s64, s5
	s_cselect_b32 s12, s63, s4
	s_cselect_b32 s49, s21, s49
	s_cselect_b32 s48, s62, s48
	s_cselect_b32 s5, s37, s71
	s_cselect_b32 s4, s61, s70
	v_lshl_add_u64 v[216:217], v[142:143], 0, s[44:45]
	s_add_i32 m0, s17, 0xc000
	ds_read_b128 v[180:183], v147
	ds_read_b128 v[184:187], v147 offset:1024
	ds_read_b128 v[188:191], v147 offset:2048
	ds_read_b128 v[192:195], v147 offset:3072
	ds_read_b128 v[196:199], v147 offset:4096
	ds_read_b128 v[204:207], v147 offset:5120
	ds_read_b128 v[208:211], v147 offset:6144
	ds_read_b128 v[212:215], v147 offset:7168
	global_load_lds_dwordx4 v[216:217], off
	s_add_i32 m0, s17, 0xe000
	v_lshl_add_u64 v[216:217], v[144:145], 0, s[44:45]
	global_load_lds_dwordx4 v[216:217], off
	s_waitcnt vmcnt(8)
	s_waitcnt lgkmcnt(0)
	s_barrier
	v_mfma_f32_16x16x32_bf16 v[128:131], v[148:151], v[180:183], v[128:131]
	v_mfma_f32_16x16x32_bf16 v[124:127], v[156:159], v[180:183], v[124:127]
	v_mfma_f32_16x16x32_bf16 v[120:123], v[148:151], v[188:191], v[120:123]
	v_mfma_f32_16x16x32_bf16 v[116:119], v[156:159], v[188:191], v[116:119]
	v_mfma_f32_16x16x32_bf16 v[104:107], v[148:151], v[196:199], v[104:107]
	v_mfma_f32_16x16x32_bf16 v[100:103], v[156:159], v[196:199], v[100:103]
	v_mfma_f32_16x16x32_bf16 v[88:91], v[148:151], v[208:211], v[88:91]
	v_mfma_f32_16x16x32_bf16 v[84:87], v[156:159], v[208:211], v[84:87]
	v_mfma_f32_16x16x32_bf16 v[128:131], v[152:155], v[184:187], v[128:131]
	v_mfma_f32_16x16x32_bf16 v[124:127], v[160:163], v[184:187], v[124:127]
	v_mfma_f32_16x16x32_bf16 v[120:123], v[152:155], v[192:195], v[120:123]
	v_mfma_f32_16x16x32_bf16 v[116:119], v[160:163], v[192:195], v[116:119]
	v_mfma_f32_16x16x32_bf16 v[104:107], v[152:155], v[204:207], v[104:107]
	v_mfma_f32_16x16x32_bf16 v[100:103], v[160:163], v[204:207], v[100:103]
	v_mfma_f32_16x16x32_bf16 v[88:91], v[152:155], v[212:215], v[88:91]
	v_mfma_f32_16x16x32_bf16 v[84:87], v[160:163], v[212:215], v[84:87]
	v_mfma_f32_16x16x32_bf16 v[112:115], v[164:167], v[180:183], v[112:115]
	v_mfma_f32_16x16x32_bf16 v[108:111], v[172:175], v[180:183], v[108:111]
	v_mfma_f32_16x16x32_bf16 v[96:99], v[164:167], v[188:191], v[96:99]
	v_mfma_f32_16x16x32_bf16 v[92:95], v[172:175], v[188:191], v[92:95]
	v_mfma_f32_16x16x32_bf16 v[80:83], v[164:167], v[196:199], v[80:83]
	v_mfma_f32_16x16x32_bf16 v[76:79], v[172:175], v[196:199], v[76:79]
	v_mfma_f32_16x16x32_bf16 v[72:75], v[164:167], v[208:211], v[72:75]
	v_mfma_f32_16x16x32_bf16 v[68:71], v[172:175], v[208:211], v[68:71]
	v_mfma_f32_16x16x32_bf16 v[112:115], v[168:171], v[184:187], v[112:115]
	v_mfma_f32_16x16x32_bf16 v[108:111], v[176:179], v[184:187], v[108:111]
	v_mfma_f32_16x16x32_bf16 v[96:99], v[168:171], v[192:195], v[96:99]
	v_mfma_f32_16x16x32_bf16 v[92:95], v[176:179], v[192:195], v[92:95]
	v_mfma_f32_16x16x32_bf16 v[80:83], v[168:171], v[204:207], v[80:83]
	v_mfma_f32_16x16x32_bf16 v[76:79], v[176:179], v[204:207], v[76:79]
	v_mfma_f32_16x16x32_bf16 v[72:75], v[168:171], v[212:215], v[72:75]
	v_mfma_f32_16x16x32_bf16 v[68:71], v[176:179], v[212:215], v[68:71]
	s_barrier
	s_add_i32 s70, s72, s16
	v_lshl_add_u64 v[216:217], s[48:49], 0, v[2:3]
	s_mov_b32 m0, s70
	ds_read_b128 v[180:183], v147 offset:16384
	ds_read_b128 v[184:187], v147 offset:17408
	ds_read_b128 v[188:191], v147 offset:18432
	ds_read_b128 v[192:195], v147 offset:19456
	ds_read_b128 v[196:199], v147 offset:20480
	ds_read_b128 v[204:207], v147 offset:21504
	ds_read_b128 v[208:211], v147 offset:22528
	ds_read_b128 v[212:215], v147 offset:23552
	global_load_lds_dwordx4 v[216:217], off
	s_add_i32 m0, s70, 0x2000
	s_add_u32 s70, s48, 0x40000
	v_lshl_add_u64 v[218:219], s[48:49], 0, v[132:133]
	s_addc_u32 s71, s49, 0
	s_add_i32 s72, s73, s16
	global_load_lds_dwordx4 v[218:219], off
	s_mov_b32 m0, s72
	v_lshl_add_u64 v[220:221], s[70:71], 0, v[2:3]
	global_load_lds_dwordx4 v[220:221], off
	s_add_i32 m0, s72, 0x2000
	v_lshl_add_u64 v[220:221], s[70:71], 0, v[132:133]
	global_load_lds_dwordx4 v[220:221], off
	s_mov_b32 m0, s17
	v_lshl_add_u64 v[220:221], s[4:5], 0, v[136:137]
	global_load_lds_dwordx4 v[220:221], off
	s_mov_b32 m0, s46
	v_lshl_add_u64 v[220:221], s[4:5], 0, v[134:135]
	global_load_lds_dwordx4 v[220:221], off
	s_waitcnt vmcnt(8)
	s_waitcnt lgkmcnt(0)
	s_barrier
	v_mfma_f32_16x16x32_bf16 v[64:67], v[148:151], v[180:183], v[64:67]
	v_mfma_f32_16x16x32_bf16 v[60:63], v[156:159], v[180:183], v[60:63]
	v_mfma_f32_16x16x32_bf16 v[56:59], v[148:151], v[188:191], v[56:59]
	v_mfma_f32_16x16x32_bf16 v[52:55], v[156:159], v[188:191], v[52:55]
	v_mfma_f32_16x16x32_bf16 v[40:43], v[148:151], v[196:199], v[40:43]
	v_mfma_f32_16x16x32_bf16 v[36:39], v[156:159], v[196:199], v[36:39]
	v_mfma_f32_16x16x32_bf16 v[24:27], v[148:151], v[208:211], v[24:27]
	v_mfma_f32_16x16x32_bf16 v[20:23], v[156:159], v[208:211], v[20:23]
	v_mfma_f32_16x16x32_bf16 v[64:67], v[152:155], v[184:187], v[64:67]
	v_mfma_f32_16x16x32_bf16 v[60:63], v[160:163], v[184:187], v[60:63]
	v_mfma_f32_16x16x32_bf16 v[56:59], v[152:155], v[192:195], v[56:59]
	v_mfma_f32_16x16x32_bf16 v[52:55], v[160:163], v[192:195], v[52:55]
	v_mfma_f32_16x16x32_bf16 v[40:43], v[152:155], v[204:207], v[40:43]
	v_mfma_f32_16x16x32_bf16 v[36:39], v[160:163], v[204:207], v[36:39]
	v_mfma_f32_16x16x32_bf16 v[24:27], v[152:155], v[212:215], v[24:27]
	v_mfma_f32_16x16x32_bf16 v[20:23], v[160:163], v[212:215], v[20:23]
	v_mfma_f32_16x16x32_bf16 v[48:51], v[164:167], v[180:183], v[48:51]
	v_mfma_f32_16x16x32_bf16 v[44:47], v[172:175], v[180:183], v[44:47]
	v_mfma_f32_16x16x32_bf16 v[32:35], v[164:167], v[188:191], v[32:35]
	v_mfma_f32_16x16x32_bf16 v[28:31], v[172:175], v[188:191], v[28:31]
	v_mfma_f32_16x16x32_bf16 v[16:19], v[164:167], v[196:199], v[16:19]
	v_mfma_f32_16x16x32_bf16 v[12:15], v[172:175], v[196:199], v[12:15]
	v_mfma_f32_16x16x32_bf16 v[8:11], v[164:167], v[208:211], v[8:11]
	v_mfma_f32_16x16x32_bf16 v[4:7], v[172:175], v[208:211], v[4:7]
	v_mfma_f32_16x16x32_bf16 v[48:51], v[168:171], v[184:187], v[48:51]
	v_mfma_f32_16x16x32_bf16 v[44:47], v[176:179], v[184:187], v[44:47]
	v_mfma_f32_16x16x32_bf16 v[32:35], v[168:171], v[192:195], v[32:35]
	v_mfma_f32_16x16x32_bf16 v[28:31], v[176:179], v[192:195], v[28:31]
	v_mfma_f32_16x16x32_bf16 v[16:19], v[168:171], v[204:207], v[16:19]
	v_mfma_f32_16x16x32_bf16 v[12:15], v[176:179], v[204:207], v[12:15]
	v_mfma_f32_16x16x32_bf16 v[8:11], v[168:171], v[212:215], v[8:11]
	v_mfma_f32_16x16x32_bf16 v[4:7], v[176:179], v[212:215], v[4:7]
	s_barrier
	s_add_i32 s70, 0, 0x18000
	s_add_i32 s71, 0, 0x1c000
	v_add_u32_e32 v160, s70, v146
	v_add_u32_e32 v176, s71, v146
	ds_read_b128 v[148:151], v160
	ds_read_b128 v[152:155], v160 offset:1024
	ds_read_b128 v[156:159], v160 offset:2048
	ds_read_b128 v[160:163], v160 offset:3072
	ds_read_b128 v[164:167], v176
	ds_read_b128 v[168:171], v176 offset:1024
	ds_read_b128 v[172:175], v176 offset:2048
	ds_read_b128 v[176:179], v176 offset:3072
	s_add_u32 s4, s4, 0x40000
	s_addc_u32 s5, s5, 0
	s_mov_b32 m0, s47
	v_lshl_add_u64 v[220:221], s[4:5], 0, v[136:137]
	ds_read_b128 v[180:183], v147 offset:32768
	ds_read_b128 v[184:187], v147 offset:33792
	ds_read_b128 v[188:191], v147 offset:34816
	ds_read_b128 v[192:195], v147 offset:35840
	ds_read_b128 v[196:199], v147 offset:36864
	ds_read_b128 v[204:207], v147 offset:37888
	ds_read_b128 v[208:211], v147 offset:38912
	ds_read_b128 v[212:215], v147 offset:39936
	global_load_lds_dwordx4 v[220:221], off
	s_mov_b32 m0, s50
	v_lshl_add_u64 v[220:221], s[4:5], 0, v[134:135]
	global_load_lds_dwordx4 v[220:221], off
	s_waitcnt vmcnt(8)
	s_waitcnt lgkmcnt(0)
	s_barrier
	v_mfma_f32_16x16x32_bf16 v[128:131], v[148:151], v[180:183], v[128:131]
	v_mfma_f32_16x16x32_bf16 v[124:127], v[156:159], v[180:183], v[124:127]
	v_mfma_f32_16x16x32_bf16 v[120:123], v[148:151], v[188:191], v[120:123]
	v_mfma_f32_16x16x32_bf16 v[116:119], v[156:159], v[188:191], v[116:119]
	v_mfma_f32_16x16x32_bf16 v[104:107], v[148:151], v[196:199], v[104:107]
	v_mfma_f32_16x16x32_bf16 v[100:103], v[156:159], v[196:199], v[100:103]
	v_mfma_f32_16x16x32_bf16 v[88:91], v[148:151], v[208:211], v[88:91]
	v_mfma_f32_16x16x32_bf16 v[84:87], v[156:159], v[208:211], v[84:87]
	v_mfma_f32_16x16x32_bf16 v[128:131], v[152:155], v[184:187], v[128:131]
	v_mfma_f32_16x16x32_bf16 v[124:127], v[160:163], v[184:187], v[124:127]
	v_mfma_f32_16x16x32_bf16 v[120:123], v[152:155], v[192:195], v[120:123]
	v_mfma_f32_16x16x32_bf16 v[116:119], v[160:163], v[192:195], v[116:119]
	v_mfma_f32_16x16x32_bf16 v[104:107], v[152:155], v[204:207], v[104:107]
	v_mfma_f32_16x16x32_bf16 v[100:103], v[160:163], v[204:207], v[100:103]
	v_mfma_f32_16x16x32_bf16 v[88:91], v[152:155], v[212:215], v[88:91]
	v_mfma_f32_16x16x32_bf16 v[84:87], v[160:163], v[212:215], v[84:87]
	v_mfma_f32_16x16x32_bf16 v[112:115], v[164:167], v[180:183], v[112:115]
	v_mfma_f32_16x16x32_bf16 v[108:111], v[172:175], v[180:183], v[108:111]
	v_mfma_f32_16x16x32_bf16 v[96:99], v[164:167], v[188:191], v[96:99]
	v_mfma_f32_16x16x32_bf16 v[92:95], v[172:175], v[188:191], v[92:95]
	v_mfma_f32_16x16x32_bf16 v[80:83], v[164:167], v[196:199], v[80:83]
	v_mfma_f32_16x16x32_bf16 v[76:79], v[172:175], v[196:199], v[76:79]
	v_mfma_f32_16x16x32_bf16 v[72:75], v[164:167], v[208:211], v[72:75]
	v_mfma_f32_16x16x32_bf16 v[68:71], v[172:175], v[208:211], v[68:71]
	v_mfma_f32_16x16x32_bf16 v[112:115], v[168:171], v[184:187], v[112:115]
	v_mfma_f32_16x16x32_bf16 v[108:111], v[176:179], v[184:187], v[108:111]
	v_mfma_f32_16x16x32_bf16 v[96:99], v[168:171], v[192:195], v[96:99]
	v_mfma_f32_16x16x32_bf16 v[92:95], v[176:179], v[192:195], v[92:95]
	v_mfma_f32_16x16x32_bf16 v[80:83], v[168:171], v[204:207], v[80:83]
	v_mfma_f32_16x16x32_bf16 v[76:79], v[176:179], v[204:207], v[76:79]
	v_mfma_f32_16x16x32_bf16 v[72:75], v[168:171], v[212:215], v[72:75]
	v_mfma_f32_16x16x32_bf16 v[68:71], v[176:179], v[212:215], v[68:71]
	s_barrier
	s_add_i32 s4, s70, s16
	v_lshl_add_u64 v[216:217], v[216:217], 0, s[34:35]
	s_mov_b32 m0, s4
	ds_read_b128 v[180:183], v147 offset:49152
	ds_read_b128 v[184:187], v147 offset:50176
	ds_read_b128 v[188:191], v147 offset:51200
	ds_read_b128 v[192:195], v147 offset:52224
	ds_read_b128 v[196:199], v147 offset:53248
	ds_read_b128 v[204:207], v147 offset:54272
	ds_read_b128 v[208:211], v147 offset:55296
	ds_read_b128 v[212:215], v147 offset:56320
	global_load_lds_dwordx4 v[216:217], off
	s_add_i32 m0, s4, 0x2000
	s_add_u32 s4, s48, 0x40080
	v_lshl_add_u64 v[216:217], v[218:219], 0, s[34:35]
	s_addc_u32 s5, s49, 0
	s_add_i32 s48, s71, s16
	global_load_lds_dwordx4 v[216:217], off
	s_mov_b32 m0, s48
	v_lshl_add_u64 v[216:217], s[4:5], 0, v[2:3]
	global_load_lds_dwordx4 v[216:217], off
	s_add_i32 m0, s48, 0x2000
	v_lshl_add_u64 v[216:217], s[4:5], 0, v[132:133]
	global_load_lds_dwordx4 v[216:217], off
	s_mov_b32 m0, s53
	v_lshl_add_u64 v[216:217], s[12:13], 0, v[136:137]
	global_load_lds_dwordx4 v[216:217], off
	s_mov_b32 m0, s56
	v_lshl_add_u64 v[216:217], s[12:13], 0, v[134:135]
	global_load_lds_dwordx4 v[216:217], off
	s_waitcnt vmcnt(8)
	s_waitcnt lgkmcnt(0)
	s_barrier
	v_mfma_f32_16x16x32_bf16 v[64:67], v[148:151], v[180:183], v[64:67]
	v_mfma_f32_16x16x32_bf16 v[60:63], v[156:159], v[180:183], v[60:63]
	v_mfma_f32_16x16x32_bf16 v[56:59], v[148:151], v[188:191], v[56:59]
	v_mfma_f32_16x16x32_bf16 v[52:55], v[156:159], v[188:191], v[52:55]
	v_mfma_f32_16x16x32_bf16 v[40:43], v[148:151], v[196:199], v[40:43]
	v_mfma_f32_16x16x32_bf16 v[36:39], v[156:159], v[196:199], v[36:39]
	v_mfma_f32_16x16x32_bf16 v[24:27], v[148:151], v[208:211], v[24:27]
	v_mfma_f32_16x16x32_bf16 v[20:23], v[156:159], v[208:211], v[20:23]
	v_mfma_f32_16x16x32_bf16 v[64:67], v[152:155], v[184:187], v[64:67]
	v_mfma_f32_16x16x32_bf16 v[60:63], v[160:163], v[184:187], v[60:63]
	v_mfma_f32_16x16x32_bf16 v[56:59], v[152:155], v[192:195], v[56:59]
	v_mfma_f32_16x16x32_bf16 v[52:55], v[160:163], v[192:195], v[52:55]
	v_mfma_f32_16x16x32_bf16 v[40:43], v[152:155], v[204:207], v[40:43]
	v_mfma_f32_16x16x32_bf16 v[36:39], v[160:163], v[204:207], v[36:39]
	v_mfma_f32_16x16x32_bf16 v[24:27], v[152:155], v[212:215], v[24:27]
	v_mfma_f32_16x16x32_bf16 v[20:23], v[160:163], v[212:215], v[20:23]
	v_mfma_f32_16x16x32_bf16 v[48:51], v[164:167], v[180:183], v[48:51]
	v_mfma_f32_16x16x32_bf16 v[44:47], v[172:175], v[180:183], v[44:47]
	v_mfma_f32_16x16x32_bf16 v[32:35], v[164:167], v[188:191], v[32:35]
	v_mfma_f32_16x16x32_bf16 v[28:31], v[172:175], v[188:191], v[28:31]
	v_mfma_f32_16x16x32_bf16 v[16:19], v[164:167], v[196:199], v[16:19]
	v_mfma_f32_16x16x32_bf16 v[12:15], v[172:175], v[196:199], v[12:15]
	v_mfma_f32_16x16x32_bf16 v[8:11], v[164:167], v[208:211], v[8:11]
	v_mfma_f32_16x16x32_bf16 v[4:7], v[172:175], v[208:211], v[4:7]
	v_mfma_f32_16x16x32_bf16 v[48:51], v[168:171], v[184:187], v[48:51]
	v_mfma_f32_16x16x32_bf16 v[44:47], v[176:179], v[184:187], v[44:47]
	v_mfma_f32_16x16x32_bf16 v[32:35], v[168:171], v[192:195], v[32:35]
	v_mfma_f32_16x16x32_bf16 v[28:31], v[176:179], v[192:195], v[28:31]
	v_mfma_f32_16x16x32_bf16 v[16:19], v[168:171], v[204:207], v[16:19]
	v_mfma_f32_16x16x32_bf16 v[12:15], v[176:179], v[204:207], v[12:15]
	v_mfma_f32_16x16x32_bf16 v[8:11], v[168:171], v[212:215], v[8:11]
	v_mfma_f32_16x16x32_bf16 v[4:7], v[176:179], v[212:215], v[4:7]
	s_barrier
	s_add_i32 s69, s69, 2
	s_add_u32 s44, s44, 0x100
	s_addc_u32 s45, s45, 0
	s_cmp_gt_u32 s69, 13
	s_cbranch_scc0 .LBB0_1206
	s_and_b64 vcc, exec, s[18:19]
	s_mov_b32 s62, 0x18000
	s_mov_b32 s63, 0x1a000
	s_cbranch_vccz .LBB0_1209
	s_barrier

.LBB0_1379:
	s_ashr_i32 s43, s42, 31
	s_lshl_b64 s[4:5], s[42:43], 19
	s_add_u32 s44, s6, s4
	s_addc_u32 s45, s7, s5
	s_and_b64 s[4:5], s[38:39], exec
	s_cselect_b32 s43, s45, s41
	s_cselect_b32 s68, s44, s40
	s_ashr_i32 s37, s36, 31
	s_lshl_b64 s[4:5], s[36:37], 19
	s_add_u32 s48, s8, s4
	s_addc_u32 s49, s9, s5
	s_and_b64 s[4:5], s[38:39], exec
	s_cselect_b32 s37, s49, s51
	s_cselect_b32 s69, s48, s50
	s_add_u32 s70, s68, 0x80
	s_addc_u32 s71, s43, 0
	s_add_u32 s4, s40, 0x40080
	s_addc_u32 s5, s41, 0
	s_add_u32 s72, s50, 0x100
	v_lshl_add_u64 v[144:145], s[4:5], 0, v[140:141]
	v_lshl_add_u64 v[146:147], s[4:5], 0, v[142:143]
	s_addc_u32 s73, s51, 0
	s_mov_b32 s74, -2
	s_mov_b64 s[50:51], 0
	s_waitcnt vmcnt(0)
	s_add_u32 s4, s40, s50
	s_addc_u32 s5, s41, s51
	s_add_u32 s75, s4, 0x100
	s_addc_u32 s76, s5, 0
	s_add_u32 s52, s72, s50
	s_addc_u32 s53, s73, s51
	s_add_u32 s4, s4, 0x180
	s_addc_u32 s5, s5, 0
	s_add_i32 s77, 0, 0x10000
	s_add_i32 s78, 0, 0x14000
	v_add_u32_e32 v2, s77, v160
	ds_read_b128 v[148:151], v2
	ds_read_b128 v[152:155], v2 offset:1024
	ds_read_b128 v[156:159], v2 offset:2048
	ds_read_b128 v[162:165], v2 offset:3072
	v_add_u32_e32 v2, s78, v160
	ds_read_b128 v[166:169], v2
	s_waitcnt lgkmcnt(0)
	ds_read_b128 v[170:173], v2 offset:1024
	ds_read_b128 v[174:177], v2 offset:2048
	ds_read_b128 v[178:181], v2 offset:3072
	s_cmpk_eq_i32 s50, 0x700
	s_cselect_b32 s13, s71, s5
	s_cselect_b32 s12, s70, s4
	s_cselect_b32 s53, s37, s53
	s_cselect_b32 s52, s69, s52
	s_cselect_b32 s5, s43, s76
	s_cselect_b32 s4, s68, s75
	v_lshl_add_u64 v[198:199], v[144:145], 0, s[50:51]
	s_add_i32 m0, s17, 0xc000
	ds_read_b128 v[182:185], v161
	ds_read_b128 v[186:189], v161 offset:1024
	ds_read_b128 v[190:193], v161 offset:2048
	ds_read_b128 v[194:197], v161 offset:3072
	ds_read_b128 v[204:207], v161 offset:4096
	ds_read_b128 v[208:211], v161 offset:5120
	ds_read_b128 v[212:215], v161 offset:6144
	ds_read_b128 v[216:219], v161 offset:7168
	global_load_lds_dwordx4 v[198:199], off
	s_add_i32 m0, s17, 0xe000
	v_lshl_add_u64 v[198:199], v[146:147], 0, s[50:51]
	global_load_lds_dwordx4 v[198:199], off
	s_waitcnt vmcnt(8)
	s_waitcnt lgkmcnt(0)
	s_barrier
	v_mfma_f32_16x16x32_bf16 v[128:131], v[148:151], v[182:185], 0
	v_mfma_f32_16x16x32_bf16 v[124:127], v[156:159], v[182:185], 0
	v_mfma_f32_16x16x32_bf16 v[112:115], v[148:151], v[190:193], 0
	v_mfma_f32_16x16x32_bf16 v[108:111], v[156:159], v[190:193], 0
	v_mfma_f32_16x16x32_bf16 v[96:99], v[148:151], v[204:207], 0
	v_mfma_f32_16x16x32_bf16 v[92:95], v[156:159], v[204:207], 0
	v_mfma_f32_16x16x32_bf16 v[80:83], v[148:151], v[212:215], 0
	v_mfma_f32_16x16x32_bf16 v[76:79], v[156:159], v[212:215], 0
	v_mfma_f32_16x16x32_bf16 v[128:131], v[152:155], v[186:189], v[128:131]
	v_mfma_f32_16x16x32_bf16 v[124:127], v[162:165], v[186:189], v[124:127]
	v_mfma_f32_16x16x32_bf16 v[112:115], v[152:155], v[194:197], v[112:115]
	v_mfma_f32_16x16x32_bf16 v[108:111], v[162:165], v[194:197], v[108:111]
	v_mfma_f32_16x16x32_bf16 v[96:99], v[152:155], v[208:211], v[96:99]
	v_mfma_f32_16x16x32_bf16 v[92:95], v[162:165], v[208:211], v[92:95]
	v_mfma_f32_16x16x32_bf16 v[80:83], v[152:155], v[216:219], v[80:83]
	v_mfma_f32_16x16x32_bf16 v[76:79], v[162:165], v[216:219], v[76:79]
	v_mfma_f32_16x16x32_bf16 v[120:123], v[166:169], v[182:185], 0
	v_mfma_f32_16x16x32_bf16 v[116:119], v[174:177], v[182:185], 0
	v_mfma_f32_16x16x32_bf16 v[104:107], v[166:169], v[190:193], 0
	v_mfma_f32_16x16x32_bf16 v[100:103], v[174:177], v[190:193], 0
	v_mfma_f32_16x16x32_bf16 v[88:91], v[166:169], v[204:207], 0
	v_mfma_f32_16x16x32_bf16 v[84:87], v[174:177], v[204:207], 0
	v_mfma_f32_16x16x32_bf16 v[72:75], v[166:169], v[212:215], 0
	v_mfma_f32_16x16x32_bf16 v[68:71], v[174:177], v[212:215], 0
	v_mfma_f32_16x16x32_bf16 v[120:123], v[170:173], v[186:189], v[120:123]
	v_mfma_f32_16x16x32_bf16 v[116:119], v[178:181], v[186:189], v[116:119]
	v_mfma_f32_16x16x32_bf16 v[104:107], v[170:173], v[194:197], v[104:107]
	v_mfma_f32_16x16x32_bf16 v[100:103], v[178:181], v[194:197], v[100:103]
	v_mfma_f32_16x16x32_bf16 v[88:91], v[170:173], v[208:211], v[88:91]
	v_mfma_f32_16x16x32_bf16 v[84:87], v[178:181], v[208:211], v[84:87]
	v_mfma_f32_16x16x32_bf16 v[72:75], v[170:173], v[216:219], v[72:75]
	v_mfma_f32_16x16x32_bf16 v[68:71], v[178:181], v[216:219], v[68:71]
	s_barrier
	s_add_i32 s75, s77, s16
	v_lshl_add_u64 v[198:199], s[52:53], 0, v[136:137]
	s_mov_b32 m0, s75
	ds_read_b128 v[182:185], v161 offset:16384
	ds_read_b128 v[186:189], v161 offset:17408
	ds_read_b128 v[190:193], v161 offset:18432
	ds_read_b128 v[194:197], v161 offset:19456
	ds_read_b128 v[204:207], v161 offset:20480
	ds_read_b128 v[208:211], v161 offset:21504
	ds_read_b128 v[212:215], v161 offset:22528
	ds_read_b128 v[216:219], v161 offset:23552
	global_load_lds_dwordx4 v[198:199], off
	s_add_i32 m0, s75, 0x2000
	s_add_u32 s76, s52, 0x40000
	v_lshl_add_u64 v[220:221], s[52:53], 0, v[132:133]
	s_addc_u32 s77, s53, 0
	s_add_i32 s75, s78, s16
	global_load_lds_dwordx4 v[220:221], off
	s_mov_b32 m0, s75
	v_lshl_add_u64 v[222:223], s[76:77], 0, v[136:137]
	global_load_lds_dwordx4 v[222:223], off
	s_add_i32 m0, s75, 0x2000
	v_lshl_add_u64 v[222:223], s[76:77], 0, v[132:133]
	global_load_lds_dwordx4 v[222:223], off
	s_mov_b32 m0, s17
	v_lshl_add_u64 v[222:223], s[4:5], 0, v[138:139]
	global_load_lds_dwordx4 v[222:223], off
	s_mov_b32 m0, s46
	v_lshl_add_u64 v[222:223], s[4:5], 0, v[134:135]
	global_load_lds_dwordx4 v[222:223], off
	s_waitcnt vmcnt(8)
	s_waitcnt lgkmcnt(0)
	s_barrier
	v_mfma_f32_16x16x32_bf16 v[64:67], v[148:151], v[182:185], 0
	v_mfma_f32_16x16x32_bf16 v[60:63], v[156:159], v[182:185], 0
	v_mfma_f32_16x16x32_bf16 v[48:51], v[148:151], v[190:193], 0
	v_mfma_f32_16x16x32_bf16 v[44:47], v[156:159], v[190:193], 0
	v_mfma_f32_16x16x32_bf16 v[32:35], v[148:151], v[204:207], 0
	v_mfma_f32_16x16x32_bf16 v[28:31], v[156:159], v[204:207], 0
	v_mfma_f32_16x16x32_bf16 v[16:19], v[148:151], v[212:215], 0
	v_mfma_f32_16x16x32_bf16 v[12:15], v[156:159], v[212:215], 0
	v_mfma_f32_16x16x32_bf16 v[64:67], v[152:155], v[186:189], v[64:67]
	v_mfma_f32_16x16x32_bf16 v[60:63], v[162:165], v[186:189], v[60:63]
	v_mfma_f32_16x16x32_bf16 v[48:51], v[152:155], v[194:197], v[48:51]
	v_mfma_f32_16x16x32_bf16 v[44:47], v[162:165], v[194:197], v[44:47]
	v_mfma_f32_16x16x32_bf16 v[32:35], v[152:155], v[208:211], v[32:35]
	v_mfma_f32_16x16x32_bf16 v[28:31], v[162:165], v[208:211], v[28:31]
	v_mfma_f32_16x16x32_bf16 v[16:19], v[152:155], v[216:219], v[16:19]
	v_mfma_f32_16x16x32_bf16 v[12:15], v[162:165], v[216:219], v[12:15]
	v_mfma_f32_16x16x32_bf16 v[56:59], v[166:169], v[182:185], 0
	v_mfma_f32_16x16x32_bf16 v[52:55], v[174:177], v[182:185], 0
	v_mfma_f32_16x16x32_bf16 v[40:43], v[166:169], v[190:193], 0
	v_mfma_f32_16x16x32_bf16 v[36:39], v[174:177], v[190:193], 0
	v_mfma_f32_16x16x32_bf16 v[24:27], v[166:169], v[204:207], 0
	v_mfma_f32_16x16x32_bf16 v[20:23], v[174:177], v[204:207], 0
	v_mfma_f32_16x16x32_bf16 v[8:11], v[166:169], v[212:215], 0
	v_mfma_f32_16x16x32_bf16 v[4:7], v[174:177], v[212:215], 0
	v_mfma_f32_16x16x32_bf16 v[56:59], v[170:173], v[186:189], v[56:59]
	v_mfma_f32_16x16x32_bf16 v[52:55], v[178:181], v[186:189], v[52:55]
	v_mfma_f32_16x16x32_bf16 v[40:43], v[170:173], v[194:197], v[40:43]
	v_mfma_f32_16x16x32_bf16 v[36:39], v[178:181], v[194:197], v[36:39]
	v_mfma_f32_16x16x32_bf16 v[24:27], v[170:173], v[208:211], v[24:27]
	v_mfma_f32_16x16x32_bf16 v[20:23], v[178:181], v[208:211], v[20:23]
	v_mfma_f32_16x16x32_bf16 v[8:11], v[170:173], v[216:219], v[8:11]
	v_mfma_f32_16x16x32_bf16 v[4:7], v[178:181], v[216:219], v[4:7]
	s_barrier
	s_add_i32 s75, 0, 0x18000
	v_add_u32_e32 v2, s75, v160
	s_add_i32 s76, 0, 0x1c000
	ds_read_b128 v[148:151], v2
	ds_read_b128 v[152:155], v2 offset:1024
	ds_read_b128 v[156:159], v2 offset:2048
	ds_read_b128 v[162:165], v2 offset:3072
	v_add_u32_e32 v2, s76, v160
	ds_read_b128 v[166:169], v2
	ds_read_b128 v[170:173], v2 offset:1024
	ds_read_b128 v[174:177], v2 offset:2048
	ds_read_b128 v[178:181], v2 offset:3072
	s_add_u32 s4, s4, 0x40000
	s_addc_u32 s5, s5, 0
	s_mov_b32 m0, s47
	v_lshl_add_u64 v[222:223], s[4:5], 0, v[138:139]
	ds_read_b128 v[182:185], v161 offset:32768
	ds_read_b128 v[186:189], v161 offset:33792
	ds_read_b128 v[190:193], v161 offset:34816
	ds_read_b128 v[194:197], v161 offset:35840
	ds_read_b128 v[204:207], v161 offset:36864
	ds_read_b128 v[208:211], v161 offset:37888
	ds_read_b128 v[212:215], v161 offset:38912
	ds_read_b128 v[216:219], v161 offset:39936
	global_load_lds_dwordx4 v[222:223], off
	s_mov_b32 m0, s56
	v_lshl_add_u64 v[222:223], s[4:5], 0, v[134:135]
	global_load_lds_dwordx4 v[222:223], off
	s_waitcnt vmcnt(8)
	s_waitcnt lgkmcnt(0)
	s_barrier
	v_mfma_f32_16x16x32_bf16 v[128:131], v[148:151], v[182:185], v[128:131]
	v_mfma_f32_16x16x32_bf16 v[124:127], v[156:159], v[182:185], v[124:127]
	v_mfma_f32_16x16x32_bf16 v[112:115], v[148:151], v[190:193], v[112:115]
	v_mfma_f32_16x16x32_bf16 v[108:111], v[156:159], v[190:193], v[108:111]
	v_mfma_f32_16x16x32_bf16 v[96:99], v[148:151], v[204:207], v[96:99]
	v_mfma_f32_16x16x32_bf16 v[92:95], v[156:159], v[204:207], v[92:95]
	v_mfma_f32_16x16x32_bf16 v[80:83], v[148:151], v[212:215], v[80:83]
	v_mfma_f32_16x16x32_bf16 v[76:79], v[156:159], v[212:215], v[76:79]
	v_mfma_f32_16x16x32_bf16 v[128:131], v[152:155], v[186:189], v[128:131]
	v_mfma_f32_16x16x32_bf16 v[124:127], v[162:165], v[186:189], v[124:127]
	v_mfma_f32_16x16x32_bf16 v[112:115], v[152:155], v[194:197], v[112:115]
	v_mfma_f32_16x16x32_bf16 v[108:111], v[162:165], v[194:197], v[108:111]
	v_mfma_f32_16x16x32_bf16 v[96:99], v[152:155], v[208:211], v[96:99]
	v_mfma_f32_16x16x32_bf16 v[92:95], v[162:165], v[208:211], v[92:95]
	v_mfma_f32_16x16x32_bf16 v[80:83], v[152:155], v[216:219], v[80:83]
	v_mfma_f32_16x16x32_bf16 v[76:79], v[162:165], v[216:219], v[76:79]
	v_mfma_f32_16x16x32_bf16 v[120:123], v[166:169], v[182:185], v[120:123]
	v_mfma_f32_16x16x32_bf16 v[116:119], v[174:177], v[182:185], v[116:119]
	v_mfma_f32_16x16x32_bf16 v[104:107], v[166:169], v[190:193], v[104:107]
	v_mfma_f32_16x16x32_bf16 v[100:103], v[174:177], v[190:193], v[100:103]
	v_mfma_f32_16x16x32_bf16 v[88:91], v[166:169], v[204:207], v[88:91]
	v_mfma_f32_16x16x32_bf16 v[84:87], v[174:177], v[204:207], v[84:87]
	v_mfma_f32_16x16x32_bf16 v[72:75], v[166:169], v[212:215], v[72:75]
	v_mfma_f32_16x16x32_bf16 v[68:71], v[174:177], v[212:215], v[68:71]
	v_mfma_f32_16x16x32_bf16 v[120:123], v[170:173], v[186:189], v[120:123]
	v_mfma_f32_16x16x32_bf16 v[116:119], v[178:181], v[186:189], v[116:119]
	v_mfma_f32_16x16x32_bf16 v[104:107], v[170:173], v[194:197], v[104:107]
	v_mfma_f32_16x16x32_bf16 v[100:103], v[178:181], v[194:197], v[100:103]
	v_mfma_f32_16x16x32_bf16 v[88:91], v[170:173], v[208:211], v[88:91]
	v_mfma_f32_16x16x32_bf16 v[84:87], v[178:181], v[208:211], v[84:87]
	v_mfma_f32_16x16x32_bf16 v[72:75], v[170:173], v[216:219], v[72:75]
	v_mfma_f32_16x16x32_bf16 v[68:71], v[178:181], v[216:219], v[68:71]
	s_barrier
	s_add_i32 s4, s75, s16
	v_lshl_add_u64 v[198:199], v[198:199], 0, s[34:35]
	s_mov_b32 m0, s4
	ds_read_b128 v[182:185], v161 offset:49152
	ds_read_b128 v[186:189], v161 offset:50176
	ds_read_b128 v[190:193], v161 offset:51200
	ds_read_b128 v[194:197], v161 offset:52224
	ds_read_b128 v[204:207], v161 offset:53248
	ds_read_b128 v[208:211], v161 offset:54272
	ds_read_b128 v[212:215], v161 offset:55296
	ds_read_b128 v[216:219], v161 offset:56320
	global_load_lds_dwordx4 v[198:199], off
	s_add_i32 m0, s4, 0x2000
	s_add_u32 s4, s52, 0x40080
	v_lshl_add_u64 v[198:199], v[220:221], 0, s[34:35]
	s_addc_u32 s5, s53, 0
	s_add_i32 s52, s76, s16
	global_load_lds_dwordx4 v[198:199], off
	s_mov_b32 m0, s52
	v_lshl_add_u64 v[198:199], s[4:5], 0, v[136:137]
	global_load_lds_dwordx4 v[198:199], off
	s_add_i32 m0, s52, 0x2000
	v_lshl_add_u64 v[198:199], s[4:5], 0, v[132:133]
	global_load_lds_dwordx4 v[198:199], off
	s_mov_b32 m0, s61
	v_lshl_add_u64 v[198:199], s[12:13], 0, v[138:139]
	global_load_lds_dwordx4 v[198:199], off
	s_mov_b32 m0, s62
	v_lshl_add_u64 v[198:199], s[12:13], 0, v[134:135]
	global_load_lds_dwordx4 v[198:199], off
	s_waitcnt vmcnt(8)
	s_waitcnt lgkmcnt(0)
	s_barrier
	v_mfma_f32_16x16x32_bf16 v[64:67], v[148:151], v[182:185], v[64:67]
	v_mfma_f32_16x16x32_bf16 v[60:63], v[156:159], v[182:185], v[60:63]
	v_mfma_f32_16x16x32_bf16 v[48:51], v[148:151], v[190:193], v[48:51]
	v_mfma_f32_16x16x32_bf16 v[44:47], v[156:159], v[190:193], v[44:47]
	v_mfma_f32_16x16x32_bf16 v[32:35], v[148:151], v[204:207], v[32:35]
	v_mfma_f32_16x16x32_bf16 v[28:31], v[156:159], v[204:207], v[28:31]
	v_mfma_f32_16x16x32_bf16 v[16:19], v[148:151], v[212:215], v[16:19]
	v_mfma_f32_16x16x32_bf16 v[12:15], v[156:159], v[212:215], v[12:15]
	v_mfma_f32_16x16x32_bf16 v[64:67], v[152:155], v[186:189], v[64:67]
	v_mfma_f32_16x16x32_bf16 v[60:63], v[162:165], v[186:189], v[60:63]
	v_mfma_f32_16x16x32_bf16 v[48:51], v[152:155], v[194:197], v[48:51]
	v_mfma_f32_16x16x32_bf16 v[44:47], v[162:165], v[194:197], v[44:47]
	v_mfma_f32_16x16x32_bf16 v[32:35], v[152:155], v[208:211], v[32:35]
	v_mfma_f32_16x16x32_bf16 v[28:31], v[162:165], v[208:211], v[28:31]
	v_mfma_f32_16x16x32_bf16 v[16:19], v[152:155], v[216:219], v[16:19]
	v_mfma_f32_16x16x32_bf16 v[12:15], v[162:165], v[216:219], v[12:15]
	v_mfma_f32_16x16x32_bf16 v[56:59], v[166:169], v[182:185], v[56:59]
	v_mfma_f32_16x16x32_bf16 v[52:55], v[174:177], v[182:185], v[52:55]
	v_mfma_f32_16x16x32_bf16 v[40:43], v[166:169], v[190:193], v[40:43]
	v_mfma_f32_16x16x32_bf16 v[36:39], v[174:177], v[190:193], v[36:39]
	v_mfma_f32_16x16x32_bf16 v[24:27], v[166:169], v[204:207], v[24:27]
	v_mfma_f32_16x16x32_bf16 v[20:23], v[174:177], v[204:207], v[20:23]
	v_mfma_f32_16x16x32_bf16 v[8:11], v[166:169], v[212:215], v[8:11]
	v_mfma_f32_16x16x32_bf16 v[4:7], v[174:177], v[212:215], v[4:7]
	v_mfma_f32_16x16x32_bf16 v[56:59], v[170:173], v[186:189], v[56:59]
	v_mfma_f32_16x16x32_bf16 v[52:55], v[178:181], v[186:189], v[52:55]
	v_mfma_f32_16x16x32_bf16 v[40:43], v[170:173], v[194:197], v[40:43]
	v_mfma_f32_16x16x32_bf16 v[36:39], v[178:181], v[194:197], v[36:39]
	v_mfma_f32_16x16x32_bf16 v[24:27], v[170:173], v[208:211], v[24:27]
	v_mfma_f32_16x16x32_bf16 v[20:23], v[178:181], v[208:211], v[20:23]
	v_mfma_f32_16x16x32_bf16 v[8:11], v[170:173], v[216:219], v[8:11]
	v_mfma_f32_16x16x32_bf16 v[4:7], v[178:181], v[216:219], v[4:7]
	s_barrier
	s_add_i32 s74, s74, 2
	s_add_u32 s50, s50, 0x100
	s_addc_u32 s51, s51, 0
	s_cmp_gt_u32 s74, 13
.LBB0_1380:
	s_add_u32 s4, s40, s50
	s_addc_u32 s5, s41, s51
	s_add_u32 s75, s4, 0x100
	s_addc_u32 s76, s5, 0
	s_add_u32 s52, s72, s50
	s_addc_u32 s53, s73, s51
	s_add_u32 s4, s4, 0x180
	s_addc_u32 s5, s5, 0
	s_add_i32 s77, 0, 0x10000
	s_add_i32 s78, 0, 0x14000
	v_add_u32_e32 v2, s77, v160
	ds_read_b128 v[148:151], v2
	ds_read_b128 v[152:155], v2 offset:1024
	ds_read_b128 v[156:159], v2 offset:2048
	ds_read_b128 v[162:165], v2 offset:3072
	v_add_u32_e32 v2, s78, v160
	ds_read_b128 v[166:169], v2
	s_waitcnt lgkmcnt(0)
	ds_read_b128 v[170:173], v2 offset:1024
	ds_read_b128 v[174:177], v2 offset:2048
	ds_read_b128 v[178:181], v2 offset:3072
	s_cmpk_eq_i32 s50, 0x700
	s_cselect_b32 s13, s71, s5
	s_cselect_b32 s12, s70, s4
	s_cselect_b32 s53, s37, s53
	s_cselect_b32 s52, s69, s52
	s_cselect_b32 s5, s43, s76
	s_cselect_b32 s4, s68, s75
	v_lshl_add_u64 v[198:199], v[144:145], 0, s[50:51]
	s_add_i32 m0, s17, 0xc000
	ds_read_b128 v[182:185], v161
	ds_read_b128 v[186:189], v161 offset:1024
	ds_read_b128 v[190:193], v161 offset:2048
	ds_read_b128 v[194:197], v161 offset:3072
	ds_read_b128 v[204:207], v161 offset:4096
	ds_read_b128 v[208:211], v161 offset:5120
	ds_read_b128 v[212:215], v161 offset:6144
	ds_read_b128 v[216:219], v161 offset:7168
	global_load_lds_dwordx4 v[198:199], off
	s_add_i32 m0, s17, 0xe000
	v_lshl_add_u64 v[198:199], v[146:147], 0, s[50:51]
	global_load_lds_dwordx4 v[198:199], off
	s_waitcnt vmcnt(8)
	s_waitcnt lgkmcnt(0)
	s_barrier
	v_mfma_f32_16x16x32_bf16 v[128:131], v[148:151], v[182:185], v[128:131]
	v_mfma_f32_16x16x32_bf16 v[124:127], v[156:159], v[182:185], v[124:127]
	v_mfma_f32_16x16x32_bf16 v[112:115], v[148:151], v[190:193], v[112:115]
	v_mfma_f32_16x16x32_bf16 v[108:111], v[156:159], v[190:193], v[108:111]
	v_mfma_f32_16x16x32_bf16 v[96:99], v[148:151], v[204:207], v[96:99]
	v_mfma_f32_16x16x32_bf16 v[92:95], v[156:159], v[204:207], v[92:95]
	v_mfma_f32_16x16x32_bf16 v[80:83], v[148:151], v[212:215], v[80:83]
	v_mfma_f32_16x16x32_bf16 v[76:79], v[156:159], v[212:215], v[76:79]
	v_mfma_f32_16x16x32_bf16 v[128:131], v[152:155], v[186:189], v[128:131]
	v_mfma_f32_16x16x32_bf16 v[124:127], v[162:165], v[186:189], v[124:127]
	v_mfma_f32_16x16x32_bf16 v[112:115], v[152:155], v[194:197], v[112:115]
	v_mfma_f32_16x16x32_bf16 v[108:111], v[162:165], v[194:197], v[108:111]
	v_mfma_f32_16x16x32_bf16 v[96:99], v[152:155], v[208:211], v[96:99]
	v_mfma_f32_16x16x32_bf16 v[92:95], v[162:165], v[208:211], v[92:95]
	v_mfma_f32_16x16x32_bf16 v[80:83], v[152:155], v[216:219], v[80:83]
	v_mfma_f32_16x16x32_bf16 v[76:79], v[162:165], v[216:219], v[76:79]
	v_mfma_f32_16x16x32_bf16 v[120:123], v[166:169], v[182:185], v[120:123]
	v_mfma_f32_16x16x32_bf16 v[116:119], v[174:177], v[182:185], v[116:119]
	v_mfma_f32_16x16x32_bf16 v[104:107], v[166:169], v[190:193], v[104:107]
	v_mfma_f32_16x16x32_bf16 v[100:103], v[174:177], v[190:193], v[100:103]
	v_mfma_f32_16x16x32_bf16 v[88:91], v[166:169], v[204:207], v[88:91]
	v_mfma_f32_16x16x32_bf16 v[84:87], v[174:177], v[204:207], v[84:87]
	v_mfma_f32_16x16x32_bf16 v[72:75], v[166:169], v[212:215], v[72:75]
	v_mfma_f32_16x16x32_bf16 v[68:71], v[174:177], v[212:215], v[68:71]
	v_mfma_f32_16x16x32_bf16 v[120:123], v[170:173], v[186:189], v[120:123]
	v_mfma_f32_16x16x32_bf16 v[116:119], v[178:181], v[186:189], v[116:119]
	v_mfma_f32_16x16x32_bf16 v[104:107], v[170:173], v[194:197], v[104:107]
	v_mfma_f32_16x16x32_bf16 v[100:103], v[178:181], v[194:197], v[100:103]
	v_mfma_f32_16x16x32_bf16 v[88:91], v[170:173], v[208:211], v[88:91]
	v_mfma_f32_16x16x32_bf16 v[84:87], v[178:181], v[208:211], v[84:87]
	v_mfma_f32_16x16x32_bf16 v[72:75], v[170:173], v[216:219], v[72:75]
	v_mfma_f32_16x16x32_bf16 v[68:71], v[178:181], v[216:219], v[68:71]
	s_barrier
	s_add_i32 s75, s77, s16
	v_lshl_add_u64 v[198:199], s[52:53], 0, v[136:137]
	s_mov_b32 m0, s75
	ds_read_b128 v[182:185], v161 offset:16384
	ds_read_b128 v[186:189], v161 offset:17408
	ds_read_b128 v[190:193], v161 offset:18432
	ds_read_b128 v[194:197], v161 offset:19456
	ds_read_b128 v[204:207], v161 offset:20480
	ds_read_b128 v[208:211], v161 offset:21504
	ds_read_b128 v[212:215], v161 offset:22528
	ds_read_b128 v[216:219], v161 offset:23552
	global_load_lds_dwordx4 v[198:199], off
	s_add_i32 m0, s75, 0x2000
	s_add_u32 s76, s52, 0x40000
	v_lshl_add_u64 v[220:221], s[52:53], 0, v[132:133]
	s_addc_u32 s77, s53, 0
	s_add_i32 s75, s78, s16
	global_load_lds_dwordx4 v[220:221], off
	s_mov_b32 m0, s75
	v_lshl_add_u64 v[222:223], s[76:77], 0, v[136:137]
	global_load_lds_dwordx4 v[222:223], off
	s_add_i32 m0, s75, 0x2000
	v_lshl_add_u64 v[222:223], s[76:77], 0, v[132:133]
	global_load_lds_dwordx4 v[222:223], off
	s_mov_b32 m0, s17
	v_lshl_add_u64 v[222:223], s[4:5], 0, v[138:139]
	global_load_lds_dwordx4 v[222:223], off
	s_mov_b32 m0, s46
	v_lshl_add_u64 v[222:223], s[4:5], 0, v[134:135]
	global_load_lds_dwordx4 v[222:223], off
	s_waitcnt vmcnt(8)
	s_waitcnt lgkmcnt(0)
	s_barrier
	v_mfma_f32_16x16x32_bf16 v[64:67], v[148:151], v[182:185], v[64:67]
	v_mfma_f32_16x16x32_bf16 v[60:63], v[156:159], v[182:185], v[60:63]
	v_mfma_f32_16x16x32_bf16 v[48:51], v[148:151], v[190:193], v[48:51]
	v_mfma_f32_16x16x32_bf16 v[44:47], v[156:159], v[190:193], v[44:47]
	v_mfma_f32_16x16x32_bf16 v[32:35], v[148:151], v[204:207], v[32:35]
	v_mfma_f32_16x16x32_bf16 v[28:31], v[156:159], v[204:207], v[28:31]
	v_mfma_f32_16x16x32_bf16 v[16:19], v[148:151], v[212:215], v[16:19]
	v_mfma_f32_16x16x32_bf16 v[12:15], v[156:159], v[212:215], v[12:15]
	v_mfma_f32_16x16x32_bf16 v[64:67], v[152:155], v[186:189], v[64:67]
	v_mfma_f32_16x16x32_bf16 v[60:63], v[162:165], v[186:189], v[60:63]
	v_mfma_f32_16x16x32_bf16 v[48:51], v[152:155], v[194:197], v[48:51]
	v_mfma_f32_16x16x32_bf16 v[44:47], v[162:165], v[194:197], v[44:47]
	v_mfma_f32_16x16x32_bf16 v[32:35], v[152:155], v[208:211], v[32:35]
	v_mfma_f32_16x16x32_bf16 v[28:31], v[162:165], v[208:211], v[28:31]
	v_mfma_f32_16x16x32_bf16 v[16:19], v[152:155], v[216:219], v[16:19]
	v_mfma_f32_16x16x32_bf16 v[12:15], v[162:165], v[216:219], v[12:15]
	v_mfma_f32_16x16x32_bf16 v[56:59], v[166:169], v[182:185], v[56:59]
	v_mfma_f32_16x16x32_bf16 v[52:55], v[174:177], v[182:185], v[52:55]
	v_mfma_f32_16x16x32_bf16 v[40:43], v[166:169], v[190:193], v[40:43]
	v_mfma_f32_16x16x32_bf16 v[36:39], v[174:177], v[190:193], v[36:39]
	v_mfma_f32_16x16x32_bf16 v[24:27], v[166:169], v[204:207], v[24:27]
	v_mfma_f32_16x16x32_bf16 v[20:23], v[174:177], v[204:207], v[20:23]
	v_mfma_f32_16x16x32_bf16 v[8:11], v[166:169], v[212:215], v[8:11]
	v_mfma_f32_16x16x32_bf16 v[4:7], v[174:177], v[212:215], v[4:7]
	v_mfma_f32_16x16x32_bf16 v[56:59], v[170:173], v[186:189], v[56:59]
	v_mfma_f32_16x16x32_bf16 v[52:55], v[178:181], v[186:189], v[52:55]
	v_mfma_f32_16x16x32_bf16 v[40:43], v[170:173], v[194:197], v[40:43]
	v_mfma_f32_16x16x32_bf16 v[36:39], v[178:181], v[194:197], v[36:39]
	v_mfma_f32_16x16x32_bf16 v[24:27], v[170:173], v[208:211], v[24:27]
	v_mfma_f32_16x16x32_bf16 v[20:23], v[178:181], v[208:211], v[20:23]
	v_mfma_f32_16x16x32_bf16 v[8:11], v[170:173], v[216:219], v[8:11]
	v_mfma_f32_16x16x32_bf16 v[4:7], v[178:181], v[216:219], v[4:7]
	s_barrier
	s_add_i32 s75, 0, 0x18000
	v_add_u32_e32 v2, s75, v160
	s_add_i32 s76, 0, 0x1c000
	ds_read_b128 v[148:151], v2
	ds_read_b128 v[152:155], v2 offset:1024
	ds_read_b128 v[156:159], v2 offset:2048
	ds_read_b128 v[162:165], v2 offset:3072
	v_add_u32_e32 v2, s76, v160
	ds_read_b128 v[166:169], v2
	ds_read_b128 v[170:173], v2 offset:1024
	ds_read_b128 v[174:177], v2 offset:2048
	ds_read_b128 v[178:181], v2 offset:3072
	s_add_u32 s4, s4, 0x40000
	s_addc_u32 s5, s5, 0
	s_mov_b32 m0, s47
	v_lshl_add_u64 v[222:223], s[4:5], 0, v[138:139]
	ds_read_b128 v[182:185], v161 offset:32768
	ds_read_b128 v[186:189], v161 offset:33792
	ds_read_b128 v[190:193], v161 offset:34816
	ds_read_b128 v[194:197], v161 offset:35840
	ds_read_b128 v[204:207], v161 offset:36864
	ds_read_b128 v[208:211], v161 offset:37888
	ds_read_b128 v[212:215], v161 offset:38912
	ds_read_b128 v[216:219], v161 offset:39936
	global_load_lds_dwordx4 v[222:223], off
	s_mov_b32 m0, s56
	v_lshl_add_u64 v[222:223], s[4:5], 0, v[134:135]
	global_load_lds_dwordx4 v[222:223], off
	s_waitcnt vmcnt(8)
	s_waitcnt lgkmcnt(0)
	s_barrier
	v_mfma_f32_16x16x32_bf16 v[128:131], v[148:151], v[182:185], v[128:131]
	v_mfma_f32_16x16x32_bf16 v[124:127], v[156:159], v[182:185], v[124:127]
	v_mfma_f32_16x16x32_bf16 v[112:115], v[148:151], v[190:193], v[112:115]
	v_mfma_f32_16x16x32_bf16 v[108:111], v[156:159], v[190:193], v[108:111]
	v_mfma_f32_16x16x32_bf16 v[96:99], v[148:151], v[204:207], v[96:99]
	v_mfma_f32_16x16x32_bf16 v[92:95], v[156:159], v[204:207], v[92:95]
	v_mfma_f32_16x16x32_bf16 v[80:83], v[148:151], v[212:215], v[80:83]
	v_mfma_f32_16x16x32_bf16 v[76:79], v[156:159], v[212:215], v[76:79]
	v_mfma_f32_16x16x32_bf16 v[128:131], v[152:155], v[186:189], v[128:131]
	v_mfma_f32_16x16x32_bf16 v[124:127], v[162:165], v[186:189], v[124:127]
	v_mfma_f32_16x16x32_bf16 v[112:115], v[152:155], v[194:197], v[112:115]
	v_mfma_f32_16x16x32_bf16 v[108:111], v[162:165], v[194:197], v[108:111]
	v_mfma_f32_16x16x32_bf16 v[96:99], v[152:155], v[208:211], v[96:99]
	v_mfma_f32_16x16x32_bf16 v[92:95], v[162:165], v[208:211], v[92:95]
	v_mfma_f32_16x16x32_bf16 v[80:83], v[152:155], v[216:219], v[80:83]
	v_mfma_f32_16x16x32_bf16 v[76:79], v[162:165], v[216:219], v[76:79]
	v_mfma_f32_16x16x32_bf16 v[120:123], v[166:169], v[182:185], v[120:123]
	v_mfma_f32_16x16x32_bf16 v[116:119], v[174:177], v[182:185], v[116:119]
	v_mfma_f32_16x16x32_bf16 v[104:107], v[166:169], v[190:193], v[104:107]
	v_mfma_f32_16x16x32_bf16 v[100:103], v[174:177], v[190:193], v[100:103]
	v_mfma_f32_16x16x32_bf16 v[88:91], v[166:169], v[204:207], v[88:91]
	v_mfma_f32_16x16x32_bf16 v[84:87], v[174:177], v[204:207], v[84:87]
	v_mfma_f32_16x16x32_bf16 v[72:75], v[166:169], v[212:215], v[72:75]
	v_mfma_f32_16x16x32_bf16 v[68:71], v[174:177], v[212:215], v[68:71]
	v_mfma_f32_16x16x32_bf16 v[120:123], v[170:173], v[186:189], v[120:123]
	v_mfma_f32_16x16x32_bf16 v[116:119], v[178:181], v[186:189], v[116:119]
	v_mfma_f32_16x16x32_bf16 v[104:107], v[170:173], v[194:197], v[104:107]
	v_mfma_f32_16x16x32_bf16 v[100:103], v[178:181], v[194:197], v[100:103]
	v_mfma_f32_16x16x32_bf16 v[88:91], v[170:173], v[208:211], v[88:91]
	v_mfma_f32_16x16x32_bf16 v[84:87], v[178:181], v[208:211], v[84:87]
	v_mfma_f32_16x16x32_bf16 v[72:75], v[170:173], v[216:219], v[72:75]
	v_mfma_f32_16x16x32_bf16 v[68:71], v[178:181], v[216:219], v[68:71]
	s_barrier
	s_add_i32 s4, s75, s16
	v_lshl_add_u64 v[198:199], v[198:199], 0, s[34:35]
	s_mov_b32 m0, s4
	ds_read_b128 v[182:185], v161 offset:49152
	ds_read_b128 v[186:189], v161 offset:50176
	ds_read_b128 v[190:193], v161 offset:51200
	ds_read_b128 v[194:197], v161 offset:52224
	ds_read_b128 v[204:207], v161 offset:53248
	ds_read_b128 v[208:211], v161 offset:54272
	ds_read_b128 v[212:215], v161 offset:55296
	ds_read_b128 v[216:219], v161 offset:56320
	global_load_lds_dwordx4 v[198:199], off
	s_add_i32 m0, s4, 0x2000
	s_add_u32 s4, s52, 0x40080
	v_lshl_add_u64 v[198:199], v[220:221], 0, s[34:35]
	s_addc_u32 s5, s53, 0
	s_add_i32 s52, s76, s16
	global_load_lds_dwordx4 v[198:199], off
	s_mov_b32 m0, s52
	v_lshl_add_u64 v[198:199], s[4:5], 0, v[136:137]
	global_load_lds_dwordx4 v[198:199], off
	s_add_i32 m0, s52, 0x2000
	v_lshl_add_u64 v[198:199], s[4:5], 0, v[132:133]
	global_load_lds_dwordx4 v[198:199], off
	s_mov_b32 m0, s61
	v_lshl_add_u64 v[198:199], s[12:13], 0, v[138:139]
	global_load_lds_dwordx4 v[198:199], off
	s_mov_b32 m0, s62
	v_lshl_add_u64 v[198:199], s[12:13], 0, v[134:135]
	global_load_lds_dwordx4 v[198:199], off
	s_waitcnt vmcnt(8)
	s_waitcnt lgkmcnt(0)
	s_barrier
	v_mfma_f32_16x16x32_bf16 v[64:67], v[148:151], v[182:185], v[64:67]
	v_mfma_f32_16x16x32_bf16 v[60:63], v[156:159], v[182:185], v[60:63]
	v_mfma_f32_16x16x32_bf16 v[48:51], v[148:151], v[190:193], v[48:51]
	v_mfma_f32_16x16x32_bf16 v[44:47], v[156:159], v[190:193], v[44:47]
	v_mfma_f32_16x16x32_bf16 v[32:35], v[148:151], v[204:207], v[32:35]
	v_mfma_f32_16x16x32_bf16 v[28:31], v[156:159], v[204:207], v[28:31]
	v_mfma_f32_16x16x32_bf16 v[16:19], v[148:151], v[212:215], v[16:19]
	v_mfma_f32_16x16x32_bf16 v[12:15], v[156:159], v[212:215], v[12:15]
	v_mfma_f32_16x16x32_bf16 v[64:67], v[152:155], v[186:189], v[64:67]
	v_mfma_f32_16x16x32_bf16 v[60:63], v[162:165], v[186:189], v[60:63]
	v_mfma_f32_16x16x32_bf16 v[48:51], v[152:155], v[194:197], v[48:51]
	v_mfma_f32_16x16x32_bf16 v[44:47], v[162:165], v[194:197], v[44:47]
	v_mfma_f32_16x16x32_bf16 v[32:35], v[152:155], v[208:211], v[32:35]
	v_mfma_f32_16x16x32_bf16 v[28:31], v[162:165], v[208:211], v[28:31]
	v_mfma_f32_16x16x32_bf16 v[16:19], v[152:155], v[216:219], v[16:19]
	v_mfma_f32_16x16x32_bf16 v[12:15], v[162:165], v[216:219], v[12:15]
	v_mfma_f32_16x16x32_bf16 v[56:59], v[166:169], v[182:185], v[56:59]
	v_mfma_f32_16x16x32_bf16 v[52:55], v[174:177], v[182:185], v[52:55]
	v_mfma_f32_16x16x32_bf16 v[40:43], v[166:169], v[190:193], v[40:43]
	v_mfma_f32_16x16x32_bf16 v[36:39], v[174:177], v[190:193], v[36:39]
	v_mfma_f32_16x16x32_bf16 v[24:27], v[166:169], v[204:207], v[24:27]
	v_mfma_f32_16x16x32_bf16 v[20:23], v[174:177], v[204:207], v[20:23]
	v_mfma_f32_16x16x32_bf16 v[8:11], v[166:169], v[212:215], v[8:11]
	v_mfma_f32_16x16x32_bf16 v[4:7], v[174:177], v[212:215], v[4:7]
	v_mfma_f32_16x16x32_bf16 v[56:59], v[170:173], v[186:189], v[56:59]
	v_mfma_f32_16x16x32_bf16 v[52:55], v[178:181], v[186:189], v[52:55]
	v_mfma_f32_16x16x32_bf16 v[40:43], v[170:173], v[194:197], v[40:43]
	v_mfma_f32_16x16x32_bf16 v[36:39], v[178:181], v[194:197], v[36:39]
	v_mfma_f32_16x16x32_bf16 v[24:27], v[170:173], v[208:211], v[24:27]
	v_mfma_f32_16x16x32_bf16 v[20:23], v[178:181], v[208:211], v[20:23]
	v_mfma_f32_16x16x32_bf16 v[8:11], v[170:173], v[216:219], v[8:11]
	v_mfma_f32_16x16x32_bf16 v[4:7], v[178:181], v[216:219], v[4:7]
	s_barrier
	s_add_i32 s74, s74, 2
	s_add_u32 s50, s50, 0x100
	s_addc_u32 s51, s51, 0
	s_cmp_gt_u32 s74, 13
	s_cbranch_scc0 .LBB0_1380
	s_and_b64 vcc, exec, s[22:23]
	s_cbranch_vccz .LBB0_1383
	s_barrier

.LBB0_1458:
	s_ashr_i32 s41, s40, 31
	s_lshl_b64 s[4:5], s[40:41], 21
	s_add_u32 s42, s6, s4
	s_addc_u32 s43, s7, s5
	s_and_b64 s[4:5], s[38:39], exec
	s_cselect_b32 s41, s43, s49
	s_cselect_b32 s68, s42, s48
	s_ashr_i32 s37, s36, 31
	s_lshl_b64 s[4:5], s[36:37], 21
	s_add_u32 s44, s8, s4
	s_addc_u32 s45, s9, s5
	s_and_b64 s[4:5], s[38:39], exec
	s_cselect_b32 s37, s45, s51
	s_cselect_b32 s69, s44, s50
	s_add_u32 s70, s68, 0x80
	s_addc_u32 s71, s41, 0
	s_add_u32 s72, s50, 0x100
	s_addc_u32 s73, s51, 0
	s_add_u32 s4, s48, 0x100080
	s_addc_u32 s5, s49, 0
	v_lshl_add_u64 v[112:113], s[4:5], 0, v[210:211]
	v_lshl_add_u64 v[114:115], s[4:5], 0, v[212:213]
	s_mov_b32 s74, -2
	s_mov_b64 s[50:51], 0
	s_waitcnt lgkmcnt(0)
	s_waitcnt vmcnt(0)
	s_add_u32 s4, s48, s50
	s_addc_u32 s5, s49, s51
	s_add_u32 s75, s4, 0x100
	s_addc_u32 s76, s5, 0
	s_add_u32 s52, s72, s50
	s_addc_u32 s53, s73, s51
	s_add_u32 s4, s4, 0x180
	s_addc_u32 s5, s5, 0
	s_add_i32 s77, 0, 0x10000
	s_add_i32 s78, 0, 0x14000
	v_add_u32_e32 v148, s77, v203
	v_add_u32_e32 v164, s78, v203
	ds_read_b128 v[120:123], v148
	ds_read_b128 v[132:135], v148 offset:1024
	ds_read_b128 v[144:147], v148 offset:2048
	ds_read_b128 v[148:151], v148 offset:3072
	ds_read_b128 v[152:155], v164
	ds_read_b128 v[156:159], v164 offset:1024
	ds_read_b128 v[160:163], v164 offset:2048
	ds_read_b128 v[164:167], v164 offset:3072
	s_cmpk_eq_i32 s50, 0x1f00
	s_cselect_b32 s13, s71, s5
	s_cselect_b32 s12, s70, s4
	s_cselect_b32 s53, s37, s53
	s_cselect_b32 s52, s69, s52
	s_cselect_b32 s5, s41, s76
	s_cselect_b32 s4, s68, s75
	v_lshl_add_u64 v[214:215], v[112:113], 0, s[50:51]
	s_add_i32 m0, s17, 0xc000
	ds_read_b128 v[168:171], v233
	ds_read_b128 v[172:175], v233 offset:1024
	ds_read_b128 v[176:179], v233 offset:2048
	ds_read_b128 v[180:183], v233 offset:3072
	ds_read_b128 v[184:187], v233 offset:4096
	ds_read_b128 v[188:191], v233 offset:5120
	ds_read_b128 v[192:195], v233 offset:6144
	ds_read_b128 v[196:199], v233 offset:7168
	global_load_lds_dwordx4 v[214:215], off
	s_add_i32 m0, s17, 0xe000
	v_lshl_add_u64 v[214:215], v[114:115], 0, s[50:51]
	global_load_lds_dwordx4 v[214:215], off
	s_waitcnt vmcnt(8)
	s_waitcnt lgkmcnt(0)
	s_barrier
	v_mfma_f32_16x16x32_bf16 v[140:143], v[120:123], v[168:171], 0
	v_mfma_f32_16x16x32_bf16 v[136:139], v[144:147], v[168:171], 0
	v_mfma_f32_16x16x32_bf16 v[116:119], v[120:123], v[176:179], 0
	v_mfma_f32_16x16x32_bf16 v[108:111], v[144:147], v[176:179], 0
	v_mfma_f32_16x16x32_bf16 v[96:99], v[120:123], v[184:187], 0
	v_mfma_f32_16x16x32_bf16 v[92:95], v[144:147], v[184:187], 0
	v_mfma_f32_16x16x32_bf16 v[80:83], v[120:123], v[192:195], 0
	v_mfma_f32_16x16x32_bf16 v[76:79], v[144:147], v[192:195], 0
	v_mfma_f32_16x16x32_bf16 v[140:143], v[132:135], v[172:175], v[140:143]
	v_mfma_f32_16x16x32_bf16 v[136:139], v[148:151], v[172:175], v[136:139]
	v_mfma_f32_16x16x32_bf16 v[116:119], v[132:135], v[180:183], v[116:119]
	v_mfma_f32_16x16x32_bf16 v[108:111], v[148:151], v[180:183], v[108:111]
	v_mfma_f32_16x16x32_bf16 v[96:99], v[132:135], v[188:191], v[96:99]
	v_mfma_f32_16x16x32_bf16 v[92:95], v[148:151], v[188:191], v[92:95]
	v_mfma_f32_16x16x32_bf16 v[80:83], v[132:135], v[196:199], v[80:83]
	v_mfma_f32_16x16x32_bf16 v[76:79], v[148:151], v[196:199], v[76:79]
	v_mfma_f32_16x16x32_bf16 v[128:131], v[152:155], v[168:171], 0
	v_mfma_f32_16x16x32_bf16 v[124:127], v[160:163], v[168:171], 0
	v_mfma_f32_16x16x32_bf16 v[104:107], v[152:155], v[176:179], 0
	v_mfma_f32_16x16x32_bf16 v[100:103], v[160:163], v[176:179], 0
	v_mfma_f32_16x16x32_bf16 v[88:91], v[152:155], v[184:187], 0
	v_mfma_f32_16x16x32_bf16 v[84:87], v[160:163], v[184:187], 0
	v_mfma_f32_16x16x32_bf16 v[72:75], v[152:155], v[192:195], 0
	v_mfma_f32_16x16x32_bf16 v[68:71], v[160:163], v[192:195], 0
	v_mfma_f32_16x16x32_bf16 v[128:131], v[156:159], v[172:175], v[128:131]
	v_mfma_f32_16x16x32_bf16 v[124:127], v[164:167], v[172:175], v[124:127]
	v_mfma_f32_16x16x32_bf16 v[104:107], v[156:159], v[180:183], v[104:107]
	v_mfma_f32_16x16x32_bf16 v[100:103], v[164:167], v[180:183], v[100:103]
	v_mfma_f32_16x16x32_bf16 v[88:91], v[156:159], v[188:191], v[88:91]
	v_mfma_f32_16x16x32_bf16 v[84:87], v[164:167], v[188:191], v[84:87]
	v_mfma_f32_16x16x32_bf16 v[72:75], v[156:159], v[196:199], v[72:75]
	v_mfma_f32_16x16x32_bf16 v[68:71], v[164:167], v[196:199], v[68:71]
	s_barrier
	s_add_i32 s75, s77, s16
	v_lshl_add_u64 v[214:215], s[52:53], 0, v[2:3]
	s_mov_b32 m0, s75
	ds_read_b128 v[168:171], v233 offset:16384
	ds_read_b128 v[172:175], v233 offset:17408
	ds_read_b128 v[176:179], v233 offset:18432
	ds_read_b128 v[180:183], v233 offset:19456
	ds_read_b128 v[184:187], v233 offset:20480
	ds_read_b128 v[188:191], v233 offset:21504
	ds_read_b128 v[192:195], v233 offset:22528
	ds_read_b128 v[196:199], v233 offset:23552
	global_load_lds_dwordx4 v[214:215], off
	s_add_i32 m0, s75, 0x2000
	s_add_u32 s76, s52, 0x100000
	v_lshl_add_u64 v[216:217], s[52:53], 0, v[204:205]
	s_addc_u32 s77, s53, 0
	s_add_i32 s75, s78, s16
	global_load_lds_dwordx4 v[216:217], off
	s_mov_b32 m0, s75
	v_lshl_add_u64 v[218:219], s[76:77], 0, v[2:3]
	global_load_lds_dwordx4 v[218:219], off
	s_add_i32 m0, s75, 0x2000
	v_lshl_add_u64 v[218:219], s[76:77], 0, v[204:205]
	global_load_lds_dwordx4 v[218:219], off
	s_mov_b32 m0, s17
	v_lshl_add_u64 v[218:219], s[4:5], 0, v[208:209]
	global_load_lds_dwordx4 v[218:219], off
	s_mov_b32 m0, s46
	v_lshl_add_u64 v[218:219], s[4:5], 0, v[206:207]
	global_load_lds_dwordx4 v[218:219], off
	s_waitcnt vmcnt(8)
	s_waitcnt lgkmcnt(0)
	s_barrier
	v_mfma_f32_16x16x32_bf16 v[64:67], v[120:123], v[168:171], 0
	v_mfma_f32_16x16x32_bf16 v[60:63], v[144:147], v[168:171], 0
	v_mfma_f32_16x16x32_bf16 v[48:51], v[120:123], v[176:179], 0
	v_mfma_f32_16x16x32_bf16 v[44:47], v[144:147], v[176:179], 0
	v_mfma_f32_16x16x32_bf16 v[32:35], v[120:123], v[184:187], 0
	v_mfma_f32_16x16x32_bf16 v[28:31], v[144:147], v[184:187], 0
	v_mfma_f32_16x16x32_bf16 v[16:19], v[120:123], v[192:195], 0
	v_mfma_f32_16x16x32_bf16 v[12:15], v[144:147], v[192:195], 0
	v_mfma_f32_16x16x32_bf16 v[64:67], v[132:135], v[172:175], v[64:67]
	v_mfma_f32_16x16x32_bf16 v[60:63], v[148:151], v[172:175], v[60:63]
	v_mfma_f32_16x16x32_bf16 v[48:51], v[132:135], v[180:183], v[48:51]
	v_mfma_f32_16x16x32_bf16 v[44:47], v[148:151], v[180:183], v[44:47]
	v_mfma_f32_16x16x32_bf16 v[32:35], v[132:135], v[188:191], v[32:35]
	v_mfma_f32_16x16x32_bf16 v[28:31], v[148:151], v[188:191], v[28:31]
	v_mfma_f32_16x16x32_bf16 v[16:19], v[132:135], v[196:199], v[16:19]
	v_mfma_f32_16x16x32_bf16 v[12:15], v[148:151], v[196:199], v[12:15]
	v_mfma_f32_16x16x32_bf16 v[56:59], v[152:155], v[168:171], 0
	v_mfma_f32_16x16x32_bf16 v[52:55], v[160:163], v[168:171], 0
	v_mfma_f32_16x16x32_bf16 v[40:43], v[152:155], v[176:179], 0
	v_mfma_f32_16x16x32_bf16 v[36:39], v[160:163], v[176:179], 0
	v_mfma_f32_16x16x32_bf16 v[24:27], v[152:155], v[184:187], 0
	v_mfma_f32_16x16x32_bf16 v[20:23], v[160:163], v[184:187], 0
	v_mfma_f32_16x16x32_bf16 v[8:11], v[152:155], v[192:195], 0
	v_mfma_f32_16x16x32_bf16 v[4:7], v[160:163], v[192:195], 0
	v_mfma_f32_16x16x32_bf16 v[56:59], v[156:159], v[172:175], v[56:59]
	v_mfma_f32_16x16x32_bf16 v[52:55], v[164:167], v[172:175], v[52:55]
	v_mfma_f32_16x16x32_bf16 v[40:43], v[156:159], v[180:183], v[40:43]
	v_mfma_f32_16x16x32_bf16 v[36:39], v[164:167], v[180:183], v[36:39]
	v_mfma_f32_16x16x32_bf16 v[24:27], v[156:159], v[188:191], v[24:27]
	v_mfma_f32_16x16x32_bf16 v[20:23], v[164:167], v[188:191], v[20:23]
	v_mfma_f32_16x16x32_bf16 v[8:11], v[156:159], v[196:199], v[8:11]
	v_mfma_f32_16x16x32_bf16 v[4:7], v[164:167], v[196:199], v[4:7]
	s_barrier
	s_add_i32 s75, 0, 0x18000
	s_add_i32 s76, 0, 0x1c000
	v_add_u32_e32 v148, s75, v203
	v_add_u32_e32 v164, s76, v203
	ds_read_b128 v[120:123], v148
	ds_read_b128 v[132:135], v148 offset:1024
	ds_read_b128 v[144:147], v148 offset:2048
	ds_read_b128 v[148:151], v148 offset:3072
	ds_read_b128 v[152:155], v164
	ds_read_b128 v[156:159], v164 offset:1024
	ds_read_b128 v[160:163], v164 offset:2048
	ds_read_b128 v[164:167], v164 offset:3072
	s_add_u32 s4, s4, 0x100000
	s_addc_u32 s5, s5, 0
	s_mov_b32 m0, s47
	v_lshl_add_u64 v[218:219], s[4:5], 0, v[208:209]
	ds_read_b128 v[168:171], v233 offset:32768
	ds_read_b128 v[172:175], v233 offset:33792
	ds_read_b128 v[176:179], v233 offset:34816
	ds_read_b128 v[180:183], v233 offset:35840
	ds_read_b128 v[184:187], v233 offset:36864
	ds_read_b128 v[188:191], v233 offset:37888
	ds_read_b128 v[192:195], v233 offset:38912
	ds_read_b128 v[196:199], v233 offset:39936
	global_load_lds_dwordx4 v[218:219], off
	s_mov_b32 m0, s58
	v_lshl_add_u64 v[218:219], s[4:5], 0, v[206:207]
	global_load_lds_dwordx4 v[218:219], off
	s_waitcnt vmcnt(8)
	s_waitcnt lgkmcnt(0)
	s_barrier
	v_mfma_f32_16x16x32_bf16 v[140:143], v[120:123], v[168:171], v[140:143]
	v_mfma_f32_16x16x32_bf16 v[136:139], v[144:147], v[168:171], v[136:139]
	v_mfma_f32_16x16x32_bf16 v[116:119], v[120:123], v[176:179], v[116:119]
	v_mfma_f32_16x16x32_bf16 v[108:111], v[144:147], v[176:179], v[108:111]
	v_mfma_f32_16x16x32_bf16 v[96:99], v[120:123], v[184:187], v[96:99]
	v_mfma_f32_16x16x32_bf16 v[92:95], v[144:147], v[184:187], v[92:95]
	v_mfma_f32_16x16x32_bf16 v[80:83], v[120:123], v[192:195], v[80:83]
	v_mfma_f32_16x16x32_bf16 v[76:79], v[144:147], v[192:195], v[76:79]
	v_mfma_f32_16x16x32_bf16 v[140:143], v[132:135], v[172:175], v[140:143]
	v_mfma_f32_16x16x32_bf16 v[136:139], v[148:151], v[172:175], v[136:139]
	v_mfma_f32_16x16x32_bf16 v[116:119], v[132:135], v[180:183], v[116:119]
	v_mfma_f32_16x16x32_bf16 v[108:111], v[148:151], v[180:183], v[108:111]
	v_mfma_f32_16x16x32_bf16 v[96:99], v[132:135], v[188:191], v[96:99]
	v_mfma_f32_16x16x32_bf16 v[92:95], v[148:151], v[188:191], v[92:95]
	v_mfma_f32_16x16x32_bf16 v[80:83], v[132:135], v[196:199], v[80:83]
	v_mfma_f32_16x16x32_bf16 v[76:79], v[148:151], v[196:199], v[76:79]
	v_mfma_f32_16x16x32_bf16 v[128:131], v[152:155], v[168:171], v[128:131]
	v_mfma_f32_16x16x32_bf16 v[124:127], v[160:163], v[168:171], v[124:127]
	v_mfma_f32_16x16x32_bf16 v[104:107], v[152:155], v[176:179], v[104:107]
	v_mfma_f32_16x16x32_bf16 v[100:103], v[160:163], v[176:179], v[100:103]
	v_mfma_f32_16x16x32_bf16 v[88:91], v[152:155], v[184:187], v[88:91]
	v_mfma_f32_16x16x32_bf16 v[84:87], v[160:163], v[184:187], v[84:87]
	v_mfma_f32_16x16x32_bf16 v[72:75], v[152:155], v[192:195], v[72:75]
	v_mfma_f32_16x16x32_bf16 v[68:71], v[160:163], v[192:195], v[68:71]
	v_mfma_f32_16x16x32_bf16 v[128:131], v[156:159], v[172:175], v[128:131]
	v_mfma_f32_16x16x32_bf16 v[124:127], v[164:167], v[172:175], v[124:127]
	v_mfma_f32_16x16x32_bf16 v[104:107], v[156:159], v[180:183], v[104:107]
	v_mfma_f32_16x16x32_bf16 v[100:103], v[164:167], v[180:183], v[100:103]
	v_mfma_f32_16x16x32_bf16 v[88:91], v[156:159], v[188:191], v[88:91]
	v_mfma_f32_16x16x32_bf16 v[84:87], v[164:167], v[188:191], v[84:87]
	v_mfma_f32_16x16x32_bf16 v[72:75], v[156:159], v[196:199], v[72:75]
	v_mfma_f32_16x16x32_bf16 v[68:71], v[164:167], v[196:199], v[68:71]
	s_barrier
	s_add_i32 s4, s75, s16
	v_lshl_add_u64 v[214:215], v[214:215], 0, s[34:35]
	s_mov_b32 m0, s4
	ds_read_b128 v[168:171], v233 offset:49152
	ds_read_b128 v[172:175], v233 offset:50176
	ds_read_b128 v[176:179], v233 offset:51200
	ds_read_b128 v[180:183], v233 offset:52224
	ds_read_b128 v[184:187], v233 offset:53248
	ds_read_b128 v[188:191], v233 offset:54272
	ds_read_b128 v[192:195], v233 offset:55296
	ds_read_b128 v[196:199], v233 offset:56320
	global_load_lds_dwordx4 v[214:215], off
	s_add_i32 m0, s4, 0x2000
	s_add_u32 s4, s52, 0x100080
	v_lshl_add_u64 v[214:215], v[216:217], 0, s[34:35]
	s_addc_u32 s5, s53, 0
	s_add_i32 s52, s76, s16
	global_load_lds_dwordx4 v[214:215], off
	s_mov_b32 m0, s52
	v_lshl_add_u64 v[214:215], s[4:5], 0, v[2:3]
	global_load_lds_dwordx4 v[214:215], off
	s_add_i32 m0, s52, 0x2000
	v_lshl_add_u64 v[214:215], s[4:5], 0, v[204:205]
	global_load_lds_dwordx4 v[214:215], off
	s_mov_b32 m0, s62
	v_lshl_add_u64 v[214:215], s[12:13], 0, v[208:209]
	global_load_lds_dwordx4 v[214:215], off
	s_mov_b32 m0, s63
	v_lshl_add_u64 v[214:215], s[12:13], 0, v[206:207]
	global_load_lds_dwordx4 v[214:215], off
	s_waitcnt vmcnt(8)
	s_waitcnt lgkmcnt(0)
	s_barrier
	v_mfma_f32_16x16x32_bf16 v[64:67], v[120:123], v[168:171], v[64:67]
	v_mfma_f32_16x16x32_bf16 v[60:63], v[144:147], v[168:171], v[60:63]
	v_mfma_f32_16x16x32_bf16 v[48:51], v[120:123], v[176:179], v[48:51]
	v_mfma_f32_16x16x32_bf16 v[44:47], v[144:147], v[176:179], v[44:47]
	v_mfma_f32_16x16x32_bf16 v[32:35], v[120:123], v[184:187], v[32:35]
	v_mfma_f32_16x16x32_bf16 v[28:31], v[144:147], v[184:187], v[28:31]
	v_mfma_f32_16x16x32_bf16 v[16:19], v[120:123], v[192:195], v[16:19]
	v_mfma_f32_16x16x32_bf16 v[12:15], v[144:147], v[192:195], v[12:15]
	v_mfma_f32_16x16x32_bf16 v[64:67], v[132:135], v[172:175], v[64:67]
	v_mfma_f32_16x16x32_bf16 v[60:63], v[148:151], v[172:175], v[60:63]
	v_mfma_f32_16x16x32_bf16 v[48:51], v[132:135], v[180:183], v[48:51]
	v_mfma_f32_16x16x32_bf16 v[44:47], v[148:151], v[180:183], v[44:47]
	v_mfma_f32_16x16x32_bf16 v[32:35], v[132:135], v[188:191], v[32:35]
	v_mfma_f32_16x16x32_bf16 v[28:31], v[148:151], v[188:191], v[28:31]
	v_mfma_f32_16x16x32_bf16 v[16:19], v[132:135], v[196:199], v[16:19]
	v_mfma_f32_16x16x32_bf16 v[12:15], v[148:151], v[196:199], v[12:15]
	v_mfma_f32_16x16x32_bf16 v[56:59], v[152:155], v[168:171], v[56:59]
	v_mfma_f32_16x16x32_bf16 v[52:55], v[160:163], v[168:171], v[52:55]
	v_mfma_f32_16x16x32_bf16 v[40:43], v[152:155], v[176:179], v[40:43]
	v_mfma_f32_16x16x32_bf16 v[36:39], v[160:163], v[176:179], v[36:39]
	v_mfma_f32_16x16x32_bf16 v[24:27], v[152:155], v[184:187], v[24:27]
	v_mfma_f32_16x16x32_bf16 v[20:23], v[160:163], v[184:187], v[20:23]
	v_mfma_f32_16x16x32_bf16 v[8:11], v[152:155], v[192:195], v[8:11]
	v_mfma_f32_16x16x32_bf16 v[4:7], v[160:163], v[192:195], v[4:7]
	v_mfma_f32_16x16x32_bf16 v[56:59], v[156:159], v[172:175], v[56:59]
	v_mfma_f32_16x16x32_bf16 v[52:55], v[164:167], v[172:175], v[52:55]
	v_mfma_f32_16x16x32_bf16 v[40:43], v[156:159], v[180:183], v[40:43]
	v_mfma_f32_16x16x32_bf16 v[36:39], v[164:167], v[180:183], v[36:39]
	v_mfma_f32_16x16x32_bf16 v[24:27], v[156:159], v[188:191], v[24:27]
	v_mfma_f32_16x16x32_bf16 v[20:23], v[164:167], v[188:191], v[20:23]
	v_mfma_f32_16x16x32_bf16 v[8:11], v[156:159], v[196:199], v[8:11]
	v_mfma_f32_16x16x32_bf16 v[4:7], v[164:167], v[196:199], v[4:7]
	s_barrier
	s_add_i32 s74, s74, 2
	s_add_u32 s50, s50, 0x100
	s_addc_u32 s51, s51, 0
	s_cmp_gt_u32 s74, 61
.LBB0_1459:
	s_add_u32 s4, s48, s50
	s_addc_u32 s5, s49, s51
	s_add_u32 s75, s4, 0x100
	s_addc_u32 s76, s5, 0
	s_add_u32 s52, s72, s50
	s_addc_u32 s53, s73, s51
	s_add_u32 s4, s4, 0x180
	s_addc_u32 s5, s5, 0
	s_add_i32 s77, 0, 0x10000
	s_add_i32 s78, 0, 0x14000
	v_add_u32_e32 v148, s77, v203
	v_add_u32_e32 v164, s78, v203
	ds_read_b128 v[120:123], v148
	ds_read_b128 v[132:135], v148 offset:1024
	ds_read_b128 v[144:147], v148 offset:2048
	ds_read_b128 v[148:151], v148 offset:3072
	ds_read_b128 v[152:155], v164
	ds_read_b128 v[156:159], v164 offset:1024
	ds_read_b128 v[160:163], v164 offset:2048
	ds_read_b128 v[164:167], v164 offset:3072
	s_cmpk_eq_i32 s50, 0x1f00
	s_cselect_b32 s13, s71, s5
	s_cselect_b32 s12, s70, s4
	s_cselect_b32 s53, s37, s53
	s_cselect_b32 s52, s69, s52
	s_cselect_b32 s5, s41, s76
	s_cselect_b32 s4, s68, s75
	v_lshl_add_u64 v[214:215], v[112:113], 0, s[50:51]
	s_add_i32 m0, s17, 0xc000
	ds_read_b128 v[168:171], v233
	ds_read_b128 v[172:175], v233 offset:1024
	ds_read_b128 v[176:179], v233 offset:2048
	ds_read_b128 v[180:183], v233 offset:3072
	ds_read_b128 v[184:187], v233 offset:4096
	ds_read_b128 v[188:191], v233 offset:5120
	ds_read_b128 v[192:195], v233 offset:6144
	ds_read_b128 v[196:199], v233 offset:7168
	global_load_lds_dwordx4 v[214:215], off
	s_add_i32 m0, s17, 0xe000
	v_lshl_add_u64 v[214:215], v[114:115], 0, s[50:51]
	global_load_lds_dwordx4 v[214:215], off
	s_waitcnt vmcnt(8)
	s_waitcnt lgkmcnt(0)
	s_barrier
	v_mfma_f32_16x16x32_bf16 v[140:143], v[120:123], v[168:171], v[140:143]
	v_mfma_f32_16x16x32_bf16 v[136:139], v[144:147], v[168:171], v[136:139]
	v_mfma_f32_16x16x32_bf16 v[116:119], v[120:123], v[176:179], v[116:119]
	v_mfma_f32_16x16x32_bf16 v[108:111], v[144:147], v[176:179], v[108:111]
	v_mfma_f32_16x16x32_bf16 v[96:99], v[120:123], v[184:187], v[96:99]
	v_mfma_f32_16x16x32_bf16 v[92:95], v[144:147], v[184:187], v[92:95]
	v_mfma_f32_16x16x32_bf16 v[80:83], v[120:123], v[192:195], v[80:83]
	v_mfma_f32_16x16x32_bf16 v[76:79], v[144:147], v[192:195], v[76:79]
	v_mfma_f32_16x16x32_bf16 v[140:143], v[132:135], v[172:175], v[140:143]
	v_mfma_f32_16x16x32_bf16 v[136:139], v[148:151], v[172:175], v[136:139]
	v_mfma_f32_16x16x32_bf16 v[116:119], v[132:135], v[180:183], v[116:119]
	v_mfma_f32_16x16x32_bf16 v[108:111], v[148:151], v[180:183], v[108:111]
	v_mfma_f32_16x16x32_bf16 v[96:99], v[132:135], v[188:191], v[96:99]
	v_mfma_f32_16x16x32_bf16 v[92:95], v[148:151], v[188:191], v[92:95]
	v_mfma_f32_16x16x32_bf16 v[80:83], v[132:135], v[196:199], v[80:83]
	v_mfma_f32_16x16x32_bf16 v[76:79], v[148:151], v[196:199], v[76:79]
	v_mfma_f32_16x16x32_bf16 v[128:131], v[152:155], v[168:171], v[128:131]
	v_mfma_f32_16x16x32_bf16 v[124:127], v[160:163], v[168:171], v[124:127]
	v_mfma_f32_16x16x32_bf16 v[104:107], v[152:155], v[176:179], v[104:107]
	v_mfma_f32_16x16x32_bf16 v[100:103], v[160:163], v[176:179], v[100:103]
	v_mfma_f32_16x16x32_bf16 v[88:91], v[152:155], v[184:187], v[88:91]
	v_mfma_f32_16x16x32_bf16 v[84:87], v[160:163], v[184:187], v[84:87]
	v_mfma_f32_16x16x32_bf16 v[72:75], v[152:155], v[192:195], v[72:75]
	v_mfma_f32_16x16x32_bf16 v[68:71], v[160:163], v[192:195], v[68:71]
	v_mfma_f32_16x16x32_bf16 v[128:131], v[156:159], v[172:175], v[128:131]
	v_mfma_f32_16x16x32_bf16 v[124:127], v[164:167], v[172:175], v[124:127]
	v_mfma_f32_16x16x32_bf16 v[104:107], v[156:159], v[180:183], v[104:107]
	v_mfma_f32_16x16x32_bf16 v[100:103], v[164:167], v[180:183], v[100:103]
	v_mfma_f32_16x16x32_bf16 v[88:91], v[156:159], v[188:191], v[88:91]
	v_mfma_f32_16x16x32_bf16 v[84:87], v[164:167], v[188:191], v[84:87]
	v_mfma_f32_16x16x32_bf16 v[72:75], v[156:159], v[196:199], v[72:75]
	v_mfma_f32_16x16x32_bf16 v[68:71], v[164:167], v[196:199], v[68:71]
	s_barrier
	s_add_i32 s75, s77, s16
	v_lshl_add_u64 v[214:215], s[52:53], 0, v[2:3]
	s_mov_b32 m0, s75
	ds_read_b128 v[168:171], v233 offset:16384
	ds_read_b128 v[172:175], v233 offset:17408
	ds_read_b128 v[176:179], v233 offset:18432
	ds_read_b128 v[180:183], v233 offset:19456
	ds_read_b128 v[184:187], v233 offset:20480
	ds_read_b128 v[188:191], v233 offset:21504
	ds_read_b128 v[192:195], v233 offset:22528
	ds_read_b128 v[196:199], v233 offset:23552
	global_load_lds_dwordx4 v[214:215], off
	s_add_i32 m0, s75, 0x2000
	s_add_u32 s76, s52, 0x100000
	v_lshl_add_u64 v[216:217], s[52:53], 0, v[204:205]
	s_addc_u32 s77, s53, 0
	s_add_i32 s75, s78, s16
	global_load_lds_dwordx4 v[216:217], off
	s_mov_b32 m0, s75
	v_lshl_add_u64 v[218:219], s[76:77], 0, v[2:3]
	global_load_lds_dwordx4 v[218:219], off
	s_add_i32 m0, s75, 0x2000
	v_lshl_add_u64 v[218:219], s[76:77], 0, v[204:205]
	global_load_lds_dwordx4 v[218:219], off
	s_mov_b32 m0, s17
	v_lshl_add_u64 v[218:219], s[4:5], 0, v[208:209]
	global_load_lds_dwordx4 v[218:219], off
	s_mov_b32 m0, s46
	v_lshl_add_u64 v[218:219], s[4:5], 0, v[206:207]
	global_load_lds_dwordx4 v[218:219], off
	s_waitcnt vmcnt(8)
	s_waitcnt lgkmcnt(0)
	s_barrier
	v_mfma_f32_16x16x32_bf16 v[64:67], v[120:123], v[168:171], v[64:67]
	v_mfma_f32_16x16x32_bf16 v[60:63], v[144:147], v[168:171], v[60:63]
	v_mfma_f32_16x16x32_bf16 v[48:51], v[120:123], v[176:179], v[48:51]
	v_mfma_f32_16x16x32_bf16 v[44:47], v[144:147], v[176:179], v[44:47]
	v_mfma_f32_16x16x32_bf16 v[32:35], v[120:123], v[184:187], v[32:35]
	v_mfma_f32_16x16x32_bf16 v[28:31], v[144:147], v[184:187], v[28:31]
	v_mfma_f32_16x16x32_bf16 v[16:19], v[120:123], v[192:195], v[16:19]
	v_mfma_f32_16x16x32_bf16 v[12:15], v[144:147], v[192:195], v[12:15]
	v_mfma_f32_16x16x32_bf16 v[64:67], v[132:135], v[172:175], v[64:67]
	v_mfma_f32_16x16x32_bf16 v[60:63], v[148:151], v[172:175], v[60:63]
	v_mfma_f32_16x16x32_bf16 v[48:51], v[132:135], v[180:183], v[48:51]
	v_mfma_f32_16x16x32_bf16 v[44:47], v[148:151], v[180:183], v[44:47]
	v_mfma_f32_16x16x32_bf16 v[32:35], v[132:135], v[188:191], v[32:35]
	v_mfma_f32_16x16x32_bf16 v[28:31], v[148:151], v[188:191], v[28:31]
	v_mfma_f32_16x16x32_bf16 v[16:19], v[132:135], v[196:199], v[16:19]
	v_mfma_f32_16x16x32_bf16 v[12:15], v[148:151], v[196:199], v[12:15]
	v_mfma_f32_16x16x32_bf16 v[56:59], v[152:155], v[168:171], v[56:59]
	v_mfma_f32_16x16x32_bf16 v[52:55], v[160:163], v[168:171], v[52:55]
	v_mfma_f32_16x16x32_bf16 v[40:43], v[152:155], v[176:179], v[40:43]
	v_mfma_f32_16x16x32_bf16 v[36:39], v[160:163], v[176:179], v[36:39]
	v_mfma_f32_16x16x32_bf16 v[24:27], v[152:155], v[184:187], v[24:27]
	v_mfma_f32_16x16x32_bf16 v[20:23], v[160:163], v[184:187], v[20:23]
	v_mfma_f32_16x16x32_bf16 v[8:11], v[152:155], v[192:195], v[8:11]
	v_mfma_f32_16x16x32_bf16 v[4:7], v[160:163], v[192:195], v[4:7]
	v_mfma_f32_16x16x32_bf16 v[56:59], v[156:159], v[172:175], v[56:59]
	v_mfma_f32_16x16x32_bf16 v[52:55], v[164:167], v[172:175], v[52:55]
	v_mfma_f32_16x16x32_bf16 v[40:43], v[156:159], v[180:183], v[40:43]
	v_mfma_f32_16x16x32_bf16 v[36:39], v[164:167], v[180:183], v[36:39]
	v_mfma_f32_16x16x32_bf16 v[24:27], v[156:159], v[188:191], v[24:27]
	v_mfma_f32_16x16x32_bf16 v[20:23], v[164:167], v[188:191], v[20:23]
	v_mfma_f32_16x16x32_bf16 v[8:11], v[156:159], v[196:199], v[8:11]
	v_mfma_f32_16x16x32_bf16 v[4:7], v[164:167], v[196:199], v[4:7]
	s_barrier
	s_add_i32 s75, 0, 0x18000
	s_add_i32 s76, 0, 0x1c000
	v_add_u32_e32 v148, s75, v203
	v_add_u32_e32 v164, s76, v203
	ds_read_b128 v[120:123], v148
	ds_read_b128 v[132:135], v148 offset:1024
	ds_read_b128 v[144:147], v148 offset:2048
	ds_read_b128 v[148:151], v148 offset:3072
	ds_read_b128 v[152:155], v164
	ds_read_b128 v[156:159], v164 offset:1024
	ds_read_b128 v[160:163], v164 offset:2048
	ds_read_b128 v[164:167], v164 offset:3072
	s_add_u32 s4, s4, 0x100000
	s_addc_u32 s5, s5, 0
	s_mov_b32 m0, s47
	v_lshl_add_u64 v[218:219], s[4:5], 0, v[208:209]
	ds_read_b128 v[168:171], v233 offset:32768
	ds_read_b128 v[172:175], v233 offset:33792
	ds_read_b128 v[176:179], v233 offset:34816
	ds_read_b128 v[180:183], v233 offset:35840
	ds_read_b128 v[184:187], v233 offset:36864
	ds_read_b128 v[188:191], v233 offset:37888
	ds_read_b128 v[192:195], v233 offset:38912
	ds_read_b128 v[196:199], v233 offset:39936
	global_load_lds_dwordx4 v[218:219], off
	s_mov_b32 m0, s58
	v_lshl_add_u64 v[218:219], s[4:5], 0, v[206:207]
	global_load_lds_dwordx4 v[218:219], off
	s_waitcnt vmcnt(8)
	s_waitcnt lgkmcnt(0)
	s_barrier
	v_mfma_f32_16x16x32_bf16 v[140:143], v[120:123], v[168:171], v[140:143]
	v_mfma_f32_16x16x32_bf16 v[136:139], v[144:147], v[168:171], v[136:139]
	v_mfma_f32_16x16x32_bf16 v[116:119], v[120:123], v[176:179], v[116:119]
	v_mfma_f32_16x16x32_bf16 v[108:111], v[144:147], v[176:179], v[108:111]
	v_mfma_f32_16x16x32_bf16 v[96:99], v[120:123], v[184:187], v[96:99]
	v_mfma_f32_16x16x32_bf16 v[92:95], v[144:147], v[184:187], v[92:95]
	v_mfma_f32_16x16x32_bf16 v[80:83], v[120:123], v[192:195], v[80:83]
	v_mfma_f32_16x16x32_bf16 v[76:79], v[144:147], v[192:195], v[76:79]
	v_mfma_f32_16x16x32_bf16 v[140:143], v[132:135], v[172:175], v[140:143]
	v_mfma_f32_16x16x32_bf16 v[136:139], v[148:151], v[172:175], v[136:139]
	v_mfma_f32_16x16x32_bf16 v[116:119], v[132:135], v[180:183], v[116:119]
	v_mfma_f32_16x16x32_bf16 v[108:111], v[148:151], v[180:183], v[108:111]
	v_mfma_f32_16x16x32_bf16 v[96:99], v[132:135], v[188:191], v[96:99]
	v_mfma_f32_16x16x32_bf16 v[92:95], v[148:151], v[188:191], v[92:95]
	v_mfma_f32_16x16x32_bf16 v[80:83], v[132:135], v[196:199], v[80:83]
	v_mfma_f32_16x16x32_bf16 v[76:79], v[148:151], v[196:199], v[76:79]
	v_mfma_f32_16x16x32_bf16 v[128:131], v[152:155], v[168:171], v[128:131]
	v_mfma_f32_16x16x32_bf16 v[124:127], v[160:163], v[168:171], v[124:127]
	v_mfma_f32_16x16x32_bf16 v[104:107], v[152:155], v[176:179], v[104:107]
	v_mfma_f32_16x16x32_bf16 v[100:103], v[160:163], v[176:179], v[100:103]
	v_mfma_f32_16x16x32_bf16 v[88:91], v[152:155], v[184:187], v[88:91]
	v_mfma_f32_16x16x32_bf16 v[84:87], v[160:163], v[184:187], v[84:87]
	v_mfma_f32_16x16x32_bf16 v[72:75], v[152:155], v[192:195], v[72:75]
	v_mfma_f32_16x16x32_bf16 v[68:71], v[160:163], v[192:195], v[68:71]
	v_mfma_f32_16x16x32_bf16 v[128:131], v[156:159], v[172:175], v[128:131]
	v_mfma_f32_16x16x32_bf16 v[124:127], v[164:167], v[172:175], v[124:127]
	v_mfma_f32_16x16x32_bf16 v[104:107], v[156:159], v[180:183], v[104:107]
	v_mfma_f32_16x16x32_bf16 v[100:103], v[164:167], v[180:183], v[100:103]
	v_mfma_f32_16x16x32_bf16 v[88:91], v[156:159], v[188:191], v[88:91]
	v_mfma_f32_16x16x32_bf16 v[84:87], v[164:167], v[188:191], v[84:87]
	v_mfma_f32_16x16x32_bf16 v[72:75], v[156:159], v[196:199], v[72:75]
	v_mfma_f32_16x16x32_bf16 v[68:71], v[164:167], v[196:199], v[68:71]
	s_barrier
	s_add_i32 s4, s75, s16
	v_lshl_add_u64 v[214:215], v[214:215], 0, s[34:35]
	s_mov_b32 m0, s4
	ds_read_b128 v[168:171], v233 offset:49152
	ds_read_b128 v[172:175], v233 offset:50176
	ds_read_b128 v[176:179], v233 offset:51200
	ds_read_b128 v[180:183], v233 offset:52224
	ds_read_b128 v[184:187], v233 offset:53248
	ds_read_b128 v[188:191], v233 offset:54272
	ds_read_b128 v[192:195], v233 offset:55296
	ds_read_b128 v[196:199], v233 offset:56320
	global_load_lds_dwordx4 v[214:215], off
	s_add_i32 m0, s4, 0x2000
	s_add_u32 s4, s52, 0x100080
	v_lshl_add_u64 v[214:215], v[216:217], 0, s[34:35]
	s_addc_u32 s5, s53, 0
	s_add_i32 s52, s76, s16
	global_load_lds_dwordx4 v[214:215], off
	s_mov_b32 m0, s52
	v_lshl_add_u64 v[214:215], s[4:5], 0, v[2:3]
	global_load_lds_dwordx4 v[214:215], off
	s_add_i32 m0, s52, 0x2000
	v_lshl_add_u64 v[214:215], s[4:5], 0, v[204:205]
	global_load_lds_dwordx4 v[214:215], off
	s_mov_b32 m0, s62
	v_lshl_add_u64 v[214:215], s[12:13], 0, v[208:209]
	global_load_lds_dwordx4 v[214:215], off
	s_mov_b32 m0, s63
	v_lshl_add_u64 v[214:215], s[12:13], 0, v[206:207]
	global_load_lds_dwordx4 v[214:215], off
	s_waitcnt vmcnt(8)
	s_waitcnt lgkmcnt(0)
	s_barrier
	v_mfma_f32_16x16x32_bf16 v[64:67], v[120:123], v[168:171], v[64:67]
	v_mfma_f32_16x16x32_bf16 v[60:63], v[144:147], v[168:171], v[60:63]
	v_mfma_f32_16x16x32_bf16 v[48:51], v[120:123], v[176:179], v[48:51]
	v_mfma_f32_16x16x32_bf16 v[44:47], v[144:147], v[176:179], v[44:47]
	v_mfma_f32_16x16x32_bf16 v[32:35], v[120:123], v[184:187], v[32:35]
	v_mfma_f32_16x16x32_bf16 v[28:31], v[144:147], v[184:187], v[28:31]
	v_mfma_f32_16x16x32_bf16 v[16:19], v[120:123], v[192:195], v[16:19]
	v_mfma_f32_16x16x32_bf16 v[12:15], v[144:147], v[192:195], v[12:15]
	v_mfma_f32_16x16x32_bf16 v[64:67], v[132:135], v[172:175], v[64:67]
	v_mfma_f32_16x16x32_bf16 v[60:63], v[148:151], v[172:175], v[60:63]
	v_mfma_f32_16x16x32_bf16 v[48:51], v[132:135], v[180:183], v[48:51]
	v_mfma_f32_16x16x32_bf16 v[44:47], v[148:151], v[180:183], v[44:47]
	v_mfma_f32_16x16x32_bf16 v[32:35], v[132:135], v[188:191], v[32:35]
	v_mfma_f32_16x16x32_bf16 v[28:31], v[148:151], v[188:191], v[28:31]
	v_mfma_f32_16x16x32_bf16 v[16:19], v[132:135], v[196:199], v[16:19]
	v_mfma_f32_16x16x32_bf16 v[12:15], v[148:151], v[196:199], v[12:15]
	v_mfma_f32_16x16x32_bf16 v[56:59], v[152:155], v[168:171], v[56:59]
	v_mfma_f32_16x16x32_bf16 v[52:55], v[160:163], v[168:171], v[52:55]
	v_mfma_f32_16x16x32_bf16 v[40:43], v[152:155], v[176:179], v[40:43]
	v_mfma_f32_16x16x32_bf16 v[36:39], v[160:163], v[176:179], v[36:39]
	v_mfma_f32_16x16x32_bf16 v[24:27], v[152:155], v[184:187], v[24:27]
	v_mfma_f32_16x16x32_bf16 v[20:23], v[160:163], v[184:187], v[20:23]
	v_mfma_f32_16x16x32_bf16 v[8:11], v[152:155], v[192:195], v[8:11]
	v_mfma_f32_16x16x32_bf16 v[4:7], v[160:163], v[192:195], v[4:7]
	v_mfma_f32_16x16x32_bf16 v[56:59], v[156:159], v[172:175], v[56:59]
	v_mfma_f32_16x16x32_bf16 v[52:55], v[164:167], v[172:175], v[52:55]
	v_mfma_f32_16x16x32_bf16 v[40:43], v[156:159], v[180:183], v[40:43]
	v_mfma_f32_16x16x32_bf16 v[36:39], v[164:167], v[180:183], v[36:39]
	v_mfma_f32_16x16x32_bf16 v[24:27], v[156:159], v[188:191], v[24:27]
	v_mfma_f32_16x16x32_bf16 v[20:23], v[164:167], v[188:191], v[20:23]
	v_mfma_f32_16x16x32_bf16 v[8:11], v[156:159], v[196:199], v[8:11]
	v_mfma_f32_16x16x32_bf16 v[4:7], v[164:167], v[196:199], v[4:7]
	s_barrier
	s_add_i32 s74, s74, 2
	s_add_u32 s50, s50, 0x100
	s_addc_u32 s51, s51, 0
	s_cmp_gt_u32 s74, 61
	s_cbranch_scc0 .LBB0_1459
	s_and_b64 vcc, exec, s[22:23]
	s_cbranch_vccz .LBB0_1462
	s_barrier
